# v54 + first K-trip of fp8 GEMM units uses SrcC=0 MFMA copies, accumulator zeroing removed
# speedup vs baseline: 1.0315x; 1.0062x over previous
.LBB0_176:
	s_add_u32 s56, s26, 0x100
	s_addc_u32 s57, s27, 0
	v_mov_b32_e32 v167, v165
	v_mov_b32_e32 v169, v165
	s_add_u32 s58, s28, 0x100
	v_mov_b32_e32 v175, v165
	v_mov_b32_e32 v177, v165
	v_lshl_add_u64 v[178:179], s[16:17], 0, v[168:169]
	v_lshl_add_u64 v[180:181], s[16:17], 0, v[166:167]
	s_addc_u32 s59, s29, 0
	s_mov_b32 s60, -2
	s_mov_b64 s[26:27], 0
	v_add_u32_e32 v252, 0x10000, v204
	v_add_u32_e32 v253, 0x10000, v205
	s_branch .LBB0_178
.LBB0_177:
	s_add_u32 s28, s4, s26
	s_addc_u32 s29, s5, s27
	s_add_u32 s30, s28, 0xe000100
	s_addc_u32 s31, s29, 0
	ds_read_b128 v[24:27], v252
	ds_read_b128 v[28:31], v253
	s_and_b64 s[28:29], s[34:35], exec
	ds_read_b128 v[16:19], v252 offset:2048
	ds_read_b128 v[20:23], v253 offset:2048
	s_cselect_b32 s29, s7, s31
	s_cselect_b32 s28, s6, s30
	s_add_u32 s61, s56, s26
	ds_read_b128 v[8:11], v252 offset:16384
	ds_read_b128 v[12:15], v253 offset:16384
	s_addc_u32 s62, s57, s27
	ds_read_b128 v[0:3], v252 offset:18432
	ds_read_b128 v[4:7], v253 offset:18432
	s_and_b64 s[30:31], s[34:35], exec
	s_cselect_b32 s31, s23, s62
	s_cselect_b32 s30, s22, s61
	s_add_u32 s61, s58, s26
	s_addc_u32 s62, s59, s27
	s_and_b64 s[34:35], s[34:35], exec
	s_cselect_b32 s35, s25, s62
	s_cselect_b32 s34, s24, s61
	s_add_u32 s100, s16, s26
	s_addc_u32 s101, s17, s27
	s_add_i32 m0, s37, 0xc000
	ds_read_b128 v[186:189], v206
	ds_read_b128 v[214:217], v206 offset:2048
	ds_read_b128 v[190:193], v207
	ds_read_b128 v[218:221], v207 offset:2048
	ds_read_b128 v[222:225], v206 offset:4096
	ds_read_b128 v[230:233], v206 offset:6144
	ds_read_b128 v[226:229], v207 offset:4096
	ds_read_b128 v[234:237], v207 offset:6144
	global_load_lds_dwordx4 v166, s[100:101]
	s_add_i32 m0, s37, 0xe000
	s_nop 0
	global_load_lds_dwordx4 v168, s[100:101]
	s_waitcnt vmcnt(8)
	s_waitcnt lgkmcnt(0)
	s_barrier
	s_setprio 1
	s_waitcnt lgkmcnt(0)
	s_cmp_eq_u32 s26, 0
	s_cbranch_scc1 .Lc0_P2_0
	v_mfma_f32_16x16x128_f8f6f4 v[156:159], v[24:31], v[186:193], v[156:159]
	v_mfma_f32_16x16x128_f8f6f4 v[152:155], v[16:23], v[186:193], v[152:155]
	v_mfma_f32_16x16x128_f8f6f4 v[136:139], v[16:23], v[214:221], v[136:139]
	v_mfma_f32_16x16x128_f8f6f4 v[144:147], v[24:31], v[214:221], v[144:147]
	v_mfma_f32_16x16x128_f8f6f4 v[128:131], v[24:31], v[222:229], v[128:131]
	v_mfma_f32_16x16x128_f8f6f4 v[120:123], v[16:23], v[222:229], v[120:123]
	v_mfma_f32_16x16x128_f8f6f4 v[104:107], v[16:23], v[230:237], v[104:107]
	v_mfma_f32_16x16x128_f8f6f4 v[112:115], v[24:31], v[230:237], v[112:115]
	v_mfma_f32_16x16x128_f8f6f4 v[148:151], v[8:15], v[186:193], v[148:151]
	v_mfma_f32_16x16x128_f8f6f4 v[140:143], v[0:7], v[186:193], v[140:143]
	v_mfma_f32_16x16x128_f8f6f4 v[124:127], v[0:7], v[214:221], v[124:127]
	v_mfma_f32_16x16x128_f8f6f4 v[132:135], v[8:15], v[214:221], v[132:135]
	v_mfma_f32_16x16x128_f8f6f4 v[116:119], v[8:15], v[222:229], v[116:119]
	v_mfma_f32_16x16x128_f8f6f4 v[108:111], v[0:7], v[222:229], v[108:111]
	v_mfma_f32_16x16x128_f8f6f4 v[96:99], v[0:7], v[230:237], v[96:99]
	v_mfma_f32_16x16x128_f8f6f4 v[100:103], v[8:15], v[230:237], v[100:103]
.Lc0b_P2_0:
	s_setprio 0
	s_barrier
	s_add_i32 s61, s44, s36
	s_mov_b32 m0, s61
	ds_read_b128 v[214:217], v206 offset:16384
	ds_read_b128 v[222:225], v206 offset:18432
	ds_read_b128 v[218:221], v207 offset:16384
	ds_read_b128 v[226:229], v207 offset:18432
	ds_read_b128 v[230:233], v206 offset:20480
	ds_read_b128 v[238:241], v206 offset:22528
	ds_read_b128 v[234:237], v207 offset:20480
	ds_read_b128 v[242:245], v207 offset:22528
	global_load_lds_dwordx4 v160, s[30:31]
	s_add_i32 m0, s61, 0x2000
	s_add_i32 s98, s46, s36
	global_load_lds_dwordx4 v162, s[30:31]
	s_mov_b32 m0, s98
	s_nop 0
	global_load_lds_dwordx4 v160, s[34:35]
	s_add_i32 m0, s98, 0x2000
	v_mov_b32_e32 v173, v165
	global_load_lds_dwordx4 v162, s[34:35]
	s_waitcnt vmcnt(6)
	s_waitcnt lgkmcnt(0)
	s_barrier
	s_setprio 1
	s_waitcnt lgkmcnt(0)
	s_cmp_eq_u32 s26, 0
	s_cbranch_scc1 .Lc0_P2_1
	v_mfma_f32_16x16x128_f8f6f4 v[92:95], v[24:31], v[214:221], v[92:95]
	v_mfma_f32_16x16x128_f8f6f4 v[88:91], v[16:23], v[214:221], v[88:91]
	v_mfma_f32_16x16x128_f8f6f4 v[72:75], v[16:23], v[222:229], v[72:75]
	v_mfma_f32_16x16x128_f8f6f4 v[80:83], v[24:31], v[222:229], v[80:83]
	s_mov_b32 m0, s37
	v_mfma_f32_16x16x128_f8f6f4 v[64:67], v[24:31], v[230:237], v[64:67]
	global_load_lds_dwordx4 v164, s[28:29]
	v_mfma_f32_16x16x128_f8f6f4 v[56:59], v[16:23], v[230:237], v[56:59]
	v_mfma_f32_16x16x128_f8f6f4 v[40:43], v[16:23], v[238:245], v[40:43]
	v_mfma_f32_16x16x128_f8f6f4 v[48:51], v[24:31], v[238:245], v[48:51]
	v_mfma_f32_16x16x128_f8f6f4 v[84:87], v[8:15], v[214:221], v[84:87]
	s_mov_b32 m0, s38
	v_mfma_f32_16x16x128_f8f6f4 v[76:79], v[0:7], v[214:221], v[76:79]
	global_load_lds_dwordx4 v172, s[28:29]
	v_mfma_f32_16x16x128_f8f6f4 v[60:63], v[0:7], v[222:229], v[60:63]
	v_mfma_f32_16x16x128_f8f6f4 v[68:71], v[8:15], v[222:229], v[68:71]
	v_mfma_f32_16x16x128_f8f6f4 v[52:55], v[8:15], v[230:237], v[52:55]
	v_mfma_f32_16x16x128_f8f6f4 v[44:47], v[0:7], v[230:237], v[44:47]
	v_mfma_f32_16x16x128_f8f6f4 v[32:35], v[0:7], v[238:245], v[32:35]
	v_mfma_f32_16x16x128_f8f6f4 v[36:39], v[8:15], v[238:245], v[36:39]
.Lc0b_P2_1:
	s_setprio 0
	s_barrier
	ds_read_b128 v[0:3], v252 offset:32768
	ds_read_b128 v[4:7], v253 offset:32768
	ds_read_b128 v[8:11], v252 offset:34816
	ds_read_b128 v[12:15], v253 offset:34816
	ds_read_b128 v[16:19], v252 offset:49152
	ds_read_b128 v[20:23], v253 offset:49152
	ds_read_b128 v[24:27], v252 offset:51200
	ds_read_b128 v[28:31], v253 offset:51200
	s_mov_b32 m0, s39
	ds_read_b128 v[214:217], v206 offset:32768
	ds_read_b128 v[222:225], v206 offset:34816
	ds_read_b128 v[218:221], v207 offset:32768
	ds_read_b128 v[226:229], v207 offset:34816
	ds_read_b128 v[230:233], v206 offset:36864
	ds_read_b128 v[238:241], v206 offset:38912
	ds_read_b128 v[234:237], v207 offset:36864
	ds_read_b128 v[242:245], v207 offset:38912
	global_load_lds_dwordx4 v184, s[28:29]
	s_mov_b32 m0, s40
	s_nop 0
	global_load_lds_dwordx4 v182, s[28:29]
	s_waitcnt vmcnt(8)
	s_waitcnt lgkmcnt(0)
	s_barrier
	s_setprio 1
	s_waitcnt lgkmcnt(0)
	v_mfma_f32_16x16x128_f8f6f4 v[156:159], v[0:7], v[214:221], v[156:159]
	v_mfma_f32_16x16x128_f8f6f4 v[152:155], v[8:15], v[214:221], v[152:155]
	v_mfma_f32_16x16x128_f8f6f4 v[136:139], v[8:15], v[222:229], v[136:139]
	v_mfma_f32_16x16x128_f8f6f4 v[144:147], v[0:7], v[222:229], v[144:147]
	v_mfma_f32_16x16x128_f8f6f4 v[128:131], v[0:7], v[230:237], v[128:131]
	v_mfma_f32_16x16x128_f8f6f4 v[120:123], v[8:15], v[230:237], v[120:123]
	v_mfma_f32_16x16x128_f8f6f4 v[104:107], v[8:15], v[238:245], v[104:107]
	v_mfma_f32_16x16x128_f8f6f4 v[112:115], v[0:7], v[238:245], v[112:115]
	v_mfma_f32_16x16x128_f8f6f4 v[148:151], v[16:23], v[214:221], v[148:151]
	v_mfma_f32_16x16x128_f8f6f4 v[140:143], v[24:31], v[214:221], v[140:143]
	v_mfma_f32_16x16x128_f8f6f4 v[124:127], v[24:31], v[222:229], v[124:127]
	v_mfma_f32_16x16x128_f8f6f4 v[132:135], v[16:23], v[222:229], v[132:135]
	v_mfma_f32_16x16x128_f8f6f4 v[116:119], v[16:23], v[230:237], v[116:119]
	v_mfma_f32_16x16x128_f8f6f4 v[108:111], v[24:31], v[230:237], v[108:111]
	v_mfma_f32_16x16x128_f8f6f4 v[96:99], v[24:31], v[238:245], v[96:99]
	v_mfma_f32_16x16x128_f8f6f4 v[100:103], v[16:23], v[238:245], v[100:103]
	s_setprio 0
	s_barrier
	s_add_i32 s99, s36, 0x17f80
	s_mov_b32 m0, s99
	ds_read_b128 v[214:217], v206 offset:49152
	ds_read_b128 v[222:225], v206 offset:51200
	ds_read_b128 v[218:221], v207 offset:49152
	ds_read_b128 v[226:229], v207 offset:51200
	ds_read_b128 v[230:233], v206 offset:53248
	ds_read_b128 v[238:241], v206 offset:55296
	ds_read_b128 v[234:237], v207 offset:53248
	ds_read_b128 v[242:245], v207 offset:55296
	global_load_lds_dwordx4 v160, s[30:31] offset:128
	s_add_i32 m0, s99, 0x2000
	s_add_i32 s99, s36, 0x1bf80
	global_load_lds_dwordx4 v162, s[30:31] offset:128
	s_mov_b32 m0, s99
	s_nop 0
	global_load_lds_dwordx4 v160, s[34:35] offset:128
	s_add_i32 m0, s99, 0x2000
	s_nop 0
	global_load_lds_dwordx4 v162, s[34:35] offset:128
	s_waitcnt vmcnt(6)
	s_waitcnt lgkmcnt(0)
	s_barrier
	s_setprio 1
	s_waitcnt lgkmcnt(0)
	v_mfma_f32_16x16x128_f8f6f4 v[92:95], v[0:7], v[214:221], v[92:95]
	v_mfma_f32_16x16x128_f8f6f4 v[88:91], v[8:15], v[214:221], v[88:91]
	v_mfma_f32_16x16x128_f8f6f4 v[72:75], v[8:15], v[222:229], v[72:75]
	v_mfma_f32_16x16x128_f8f6f4 v[80:83], v[0:7], v[222:229], v[80:83]
	s_add_i32 m0, s41, 0xffffff80
	v_mfma_f32_16x16x128_f8f6f4 v[64:67], v[0:7], v[230:237], v[64:67]
	global_load_lds_dwordx4 v164, s[28:29] offset:128
	v_mfma_f32_16x16x128_f8f6f4 v[56:59], v[8:15], v[230:237], v[56:59]
	v_mfma_f32_16x16x128_f8f6f4 v[40:43], v[8:15], v[238:245], v[40:43]
	v_mfma_f32_16x16x128_f8f6f4 v[48:51], v[0:7], v[238:245], v[48:51]
	v_mfma_f32_16x16x128_f8f6f4 v[84:87], v[16:23], v[214:221], v[84:87]
	s_add_i32 m0, s42, 0xffffff80
	v_mfma_f32_16x16x128_f8f6f4 v[76:79], v[24:31], v[214:221], v[76:79]
	global_load_lds_dwordx4 v172, s[28:29] offset:128
	v_mfma_f32_16x16x128_f8f6f4 v[60:63], v[24:31], v[222:229], v[60:63]
	v_mfma_f32_16x16x128_f8f6f4 v[68:71], v[16:23], v[222:229], v[68:71]
	v_mfma_f32_16x16x128_f8f6f4 v[52:55], v[16:23], v[230:237], v[52:55]
	v_mfma_f32_16x16x128_f8f6f4 v[44:47], v[24:31], v[230:237], v[44:47]
	v_mfma_f32_16x16x128_f8f6f4 v[32:35], v[24:31], v[238:245], v[32:35]
	v_mfma_f32_16x16x128_f8f6f4 v[36:39], v[16:23], v[238:245], v[36:39]
	s_setprio 0
	s_barrier
	s_add_i32 s60, s60, 2
	s_add_u32 s26, s26, 0x100
	s_addc_u32 s27, s27, 0
	s_cmp_gt_u32 s60, 5
	s_cbranch_scc1 .LBB0_180

.Lc0_P2_0:
	v_mfma_f32_16x16x128_f8f6f4 v[156:159], v[24:31], v[186:193], 0
	v_mfma_f32_16x16x128_f8f6f4 v[152:155], v[16:23], v[186:193], 0
	v_mfma_f32_16x16x128_f8f6f4 v[136:139], v[16:23], v[214:221], 0
	v_mfma_f32_16x16x128_f8f6f4 v[144:147], v[24:31], v[214:221], 0
	v_mfma_f32_16x16x128_f8f6f4 v[128:131], v[24:31], v[222:229], 0
	v_mfma_f32_16x16x128_f8f6f4 v[120:123], v[16:23], v[222:229], 0
	v_mfma_f32_16x16x128_f8f6f4 v[104:107], v[16:23], v[230:237], 0
	v_mfma_f32_16x16x128_f8f6f4 v[112:115], v[24:31], v[230:237], 0
	v_mfma_f32_16x16x128_f8f6f4 v[148:151], v[8:15], v[186:193], 0
	v_mfma_f32_16x16x128_f8f6f4 v[140:143], v[0:7], v[186:193], 0
	v_mfma_f32_16x16x128_f8f6f4 v[124:127], v[0:7], v[214:221], 0
	v_mfma_f32_16x16x128_f8f6f4 v[132:135], v[8:15], v[214:221], 0
	v_mfma_f32_16x16x128_f8f6f4 v[116:119], v[8:15], v[222:229], 0
	v_mfma_f32_16x16x128_f8f6f4 v[108:111], v[0:7], v[222:229], 0
	v_mfma_f32_16x16x128_f8f6f4 v[96:99], v[0:7], v[230:237], 0
	v_mfma_f32_16x16x128_f8f6f4 v[100:103], v[8:15], v[230:237], 0
	s_branch .Lc0b_P2_0
.Lc0_P2_1:
	v_mfma_f32_16x16x128_f8f6f4 v[92:95], v[24:31], v[214:221], 0
	v_mfma_f32_16x16x128_f8f6f4 v[88:91], v[16:23], v[214:221], 0
	v_mfma_f32_16x16x128_f8f6f4 v[72:75], v[16:23], v[222:229], 0
	v_mfma_f32_16x16x128_f8f6f4 v[80:83], v[24:31], v[222:229], 0
	s_mov_b32 m0, s37
	v_mfma_f32_16x16x128_f8f6f4 v[64:67], v[24:31], v[230:237], 0
	global_load_lds_dwordx4 v164, s[28:29]
	v_mfma_f32_16x16x128_f8f6f4 v[56:59], v[16:23], v[230:237], 0
	v_mfma_f32_16x16x128_f8f6f4 v[40:43], v[16:23], v[238:245], 0
	v_mfma_f32_16x16x128_f8f6f4 v[48:51], v[24:31], v[238:245], 0
	v_mfma_f32_16x16x128_f8f6f4 v[84:87], v[8:15], v[214:221], 0
	s_mov_b32 m0, s38
	v_mfma_f32_16x16x128_f8f6f4 v[76:79], v[0:7], v[214:221], 0
	global_load_lds_dwordx4 v172, s[28:29]
	v_mfma_f32_16x16x128_f8f6f4 v[60:63], v[0:7], v[222:229], 0
	v_mfma_f32_16x16x128_f8f6f4 v[68:71], v[8:15], v[222:229], 0
	v_mfma_f32_16x16x128_f8f6f4 v[52:55], v[8:15], v[230:237], 0
	v_mfma_f32_16x16x128_f8f6f4 v[44:47], v[0:7], v[230:237], 0
	v_mfma_f32_16x16x128_f8f6f4 v[32:35], v[0:7], v[238:245], 0
	v_mfma_f32_16x16x128_f8f6f4 v[36:39], v[8:15], v[238:245], 0
	s_branch .Lc0b_P2_1

.LBB0_589:
	s_lshl_b32 s4, s80, 10
	s_and_b32 s4, s4, 0x400
	s_add_u32 s27, s38, 0x100
	s_addc_u32 s86, s39, 0
	v_mov_b32_e32 v171, v165
	v_mov_b32_e32 v169, v165
	s_add_u32 s87, s40, 0x100
	v_add_u32_e32 v208, s4, v199
	v_lshl_add_u64 v[174:175], s[18:19], 0, v[168:169]
	v_lshl_add_u64 v[176:177], s[18:19], 0, v[170:171]
	s_addc_u32 s88, s41, 0
	s_mov_b32 s89, -2
	s_mov_b64 s[4:5], 0
	v_add_u32_e32 v252, 0x10000, v197
	v_add_u32_e32 v253, 0x10000, v198
	s_branch .LBB0_591
.LBB0_590:
	s_add_u32 s36, s8, s4
	s_addc_u32 s37, s9, s5
	s_add_u32 s38, s36, 0xe000100
	s_addc_u32 s39, s37, 0
	ds_read_b128 v[24:27], v252
	ds_read_b128 v[28:31], v253
	s_and_b64 s[36:37], s[40:41], exec
	ds_read_b128 v[16:19], v252 offset:2048
	ds_read_b128 v[20:23], v253 offset:2048
	s_cselect_b32 s37, s11, s39
	s_cselect_b32 s36, s10, s38
	s_add_u32 s90, s27, s4
	ds_read_b128 v[8:11], v252 offset:16384
	ds_read_b128 v[12:15], v253 offset:16384
	s_addc_u32 s91, s86, s5
	ds_read_b128 v[0:3], v252 offset:18432
	ds_read_b128 v[4:7], v253 offset:18432
	s_and_b64 s[38:39], s[40:41], exec
	s_cselect_b32 s39, s29, s91
	s_cselect_b32 s38, s28, s90
	s_add_u32 s90, s87, s4
	s_addc_u32 s91, s88, s5
	s_and_b64 s[40:41], s[40:41], exec
	s_cselect_b32 s41, s31, s91
	s_cselect_b32 s40, s30, s90
	s_add_u32 s100, s18, s4
	s_addc_u32 s101, s19, s5
	s_add_i32 m0, s61, 0xc000
	ds_read_b128 v[182:185], v201
	ds_read_b128 v[210:213], v201 offset:2048
	ds_read_b128 v[186:189], v202
	ds_read_b128 v[214:217], v202 offset:2048
	ds_read_b128 v[218:221], v201 offset:4096
	ds_read_b128 v[226:229], v201 offset:6144
	ds_read_b128 v[222:225], v202 offset:4096
	ds_read_b128 v[230:233], v202 offset:6144
	global_load_lds_dwordx4 v170, s[100:101]
	s_add_i32 m0, s61, 0xe000
	s_nop 0
	global_load_lds_dwordx4 v168, s[100:101]
	s_waitcnt vmcnt(8)
	s_waitcnt lgkmcnt(0)
	s_barrier
	s_setprio 1
	s_waitcnt lgkmcnt(0)
	s_cmp_eq_u32 s4, 0
	s_cbranch_scc1 .Lc0_P6_0
	v_mfma_f32_16x16x128_f8f6f4 v[156:159], v[24:31], v[182:189], v[156:159]
	v_mfma_f32_16x16x128_f8f6f4 v[148:151], v[16:23], v[182:189], v[148:151]
	v_mfma_f32_16x16x128_f8f6f4 v[132:135], v[16:23], v[210:217], v[132:135]
	v_mfma_f32_16x16x128_f8f6f4 v[140:143], v[24:31], v[210:217], v[140:143]
	v_mfma_f32_16x16x128_f8f6f4 v[124:127], v[24:31], v[218:225], v[124:127]
	v_mfma_f32_16x16x128_f8f6f4 v[116:119], v[16:23], v[218:225], v[116:119]
	v_mfma_f32_16x16x128_f8f6f4 v[100:103], v[16:23], v[226:233], v[100:103]
	v_mfma_f32_16x16x128_f8f6f4 v[108:111], v[24:31], v[226:233], v[108:111]
	v_mfma_f32_16x16x128_f8f6f4 v[152:155], v[8:15], v[182:189], v[152:155]
	v_mfma_f32_16x16x128_f8f6f4 v[144:147], v[0:7], v[182:189], v[144:147]
	v_mfma_f32_16x16x128_f8f6f4 v[128:131], v[0:7], v[210:217], v[128:131]
	v_mfma_f32_16x16x128_f8f6f4 v[136:139], v[8:15], v[210:217], v[136:139]
	v_mfma_f32_16x16x128_f8f6f4 v[120:123], v[8:15], v[218:225], v[120:123]
	v_mfma_f32_16x16x128_f8f6f4 v[112:115], v[0:7], v[218:225], v[112:115]
	v_mfma_f32_16x16x128_f8f6f4 v[96:99], v[0:7], v[226:233], v[96:99]
	v_mfma_f32_16x16x128_f8f6f4 v[104:107], v[8:15], v[226:233], v[104:107]
.Lc0b_P6_0:
	s_setprio 0
	s_barrier
	s_add_i32 s90, s72, s44
	s_mov_b32 m0, s90
	ds_read_b128 v[210:213], v201 offset:16384
	ds_read_b128 v[218:221], v201 offset:18432
	ds_read_b128 v[214:217], v202 offset:16384
	ds_read_b128 v[222:225], v202 offset:18432
	ds_read_b128 v[226:229], v201 offset:20480
	ds_read_b128 v[234:237], v201 offset:22528
	ds_read_b128 v[230:233], v202 offset:20480
	ds_read_b128 v[238:241], v202 offset:22528
	global_load_lds_dwordx4 v160, s[38:39]
	s_add_i32 m0, s90, 0x2000
	s_add_i32 s98, s74, s44
	global_load_lds_dwordx4 v162, s[38:39]
	s_mov_b32 m0, s98
	s_nop 0
	global_load_lds_dwordx4 v160, s[40:41]
	s_add_i32 m0, s98, 0x2000
	v_mov_b32_e32 v167, v165
	global_load_lds_dwordx4 v162, s[40:41]
	s_waitcnt vmcnt(6)
	s_waitcnt lgkmcnt(0)
	s_barrier
	s_setprio 1
	s_waitcnt lgkmcnt(0)
	s_cmp_eq_u32 s4, 0
	s_cbranch_scc1 .Lc0_P6_1
	v_mfma_f32_16x16x128_f8f6f4 v[92:95], v[24:31], v[210:217], v[92:95]
	v_mfma_f32_16x16x128_f8f6f4 v[84:87], v[16:23], v[210:217], v[84:87]
	v_mfma_f32_16x16x128_f8f6f4 v[68:71], v[16:23], v[218:225], v[68:71]
	v_mfma_f32_16x16x128_f8f6f4 v[76:79], v[24:31], v[218:225], v[76:79]
	s_mov_b32 m0, s61
	v_mfma_f32_16x16x128_f8f6f4 v[60:63], v[24:31], v[226:233], v[60:63]
	global_load_lds_dwordx4 v164, s[36:37]
	v_mfma_f32_16x16x128_f8f6f4 v[52:55], v[16:23], v[226:233], v[52:55]
	v_mfma_f32_16x16x128_f8f6f4 v[36:39], v[16:23], v[234:241], v[36:39]
	v_mfma_f32_16x16x128_f8f6f4 v[44:47], v[24:31], v[234:241], v[44:47]
	v_mfma_f32_16x16x128_f8f6f4 v[88:91], v[8:15], v[210:217], v[88:91]
	s_mov_b32 m0, s62
	v_mfma_f32_16x16x128_f8f6f4 v[80:83], v[0:7], v[210:217], v[80:83]
	global_load_lds_dwordx4 v166, s[36:37]
	v_mfma_f32_16x16x128_f8f6f4 v[64:67], v[0:7], v[218:225], v[64:67]
	v_mfma_f32_16x16x128_f8f6f4 v[72:75], v[8:15], v[218:225], v[72:75]
	v_mfma_f32_16x16x128_f8f6f4 v[56:59], v[8:15], v[226:233], v[56:59]
	v_mfma_f32_16x16x128_f8f6f4 v[48:51], v[0:7], v[226:233], v[48:51]
	v_mfma_f32_16x16x128_f8f6f4 v[32:35], v[0:7], v[234:241], v[32:35]
	v_mfma_f32_16x16x128_f8f6f4 v[40:43], v[8:15], v[234:241], v[40:43]
.Lc0b_P6_1:
	s_setprio 0
	s_barrier
	ds_read_b128 v[0:3], v252 offset:32768
	ds_read_b128 v[4:7], v253 offset:32768
	ds_read_b128 v[8:11], v252 offset:34816
	ds_read_b128 v[12:15], v253 offset:34816
	ds_read_b128 v[16:19], v252 offset:49152
	ds_read_b128 v[20:23], v253 offset:49152
	ds_read_b128 v[24:27], v252 offset:51200
	ds_read_b128 v[28:31], v253 offset:51200
	s_mov_b32 m0, s63
	ds_read_b128 v[210:213], v201 offset:32768
	ds_read_b128 v[218:221], v201 offset:34816
	ds_read_b128 v[214:217], v202 offset:32768
	ds_read_b128 v[222:225], v202 offset:34816
	ds_read_b128 v[226:229], v201 offset:36864
	ds_read_b128 v[234:237], v201 offset:38912
	ds_read_b128 v[230:233], v202 offset:36864
	ds_read_b128 v[238:241], v202 offset:38912
	global_load_lds_dwordx4 v180, s[36:37]
	s_mov_b32 m0, s64
	s_nop 0
	global_load_lds_dwordx4 v178, s[36:37]
	s_waitcnt vmcnt(8)
	s_waitcnt lgkmcnt(0)
	s_barrier
	s_setprio 1
	s_waitcnt lgkmcnt(0)
	v_mfma_f32_16x16x128_f8f6f4 v[156:159], v[0:7], v[210:217], v[156:159]
	v_mfma_f32_16x16x128_f8f6f4 v[148:151], v[8:15], v[210:217], v[148:151]
	v_mfma_f32_16x16x128_f8f6f4 v[132:135], v[8:15], v[218:225], v[132:135]
	v_mfma_f32_16x16x128_f8f6f4 v[140:143], v[0:7], v[218:225], v[140:143]
	v_mfma_f32_16x16x128_f8f6f4 v[124:127], v[0:7], v[226:233], v[124:127]
	v_mfma_f32_16x16x128_f8f6f4 v[116:119], v[8:15], v[226:233], v[116:119]
	v_mfma_f32_16x16x128_f8f6f4 v[100:103], v[8:15], v[234:241], v[100:103]
	v_mfma_f32_16x16x128_f8f6f4 v[108:111], v[0:7], v[234:241], v[108:111]
	v_mfma_f32_16x16x128_f8f6f4 v[152:155], v[16:23], v[210:217], v[152:155]
	v_mfma_f32_16x16x128_f8f6f4 v[144:147], v[24:31], v[210:217], v[144:147]
	v_mfma_f32_16x16x128_f8f6f4 v[128:131], v[24:31], v[218:225], v[128:131]
	v_mfma_f32_16x16x128_f8f6f4 v[136:139], v[16:23], v[218:225], v[136:139]
	v_mfma_f32_16x16x128_f8f6f4 v[120:123], v[16:23], v[226:233], v[120:123]
	v_mfma_f32_16x16x128_f8f6f4 v[112:115], v[24:31], v[226:233], v[112:115]
	v_mfma_f32_16x16x128_f8f6f4 v[96:99], v[24:31], v[234:241], v[96:99]
	v_mfma_f32_16x16x128_f8f6f4 v[104:107], v[16:23], v[234:241], v[104:107]
	s_setprio 0
	s_barrier
	s_add_i32 s99, s44, 0x17f80
	s_mov_b32 m0, s99
	ds_read_b128 v[210:213], v201 offset:49152
	ds_read_b128 v[218:221], v201 offset:51200
	ds_read_b128 v[214:217], v202 offset:49152
	ds_read_b128 v[222:225], v202 offset:51200
	ds_read_b128 v[226:229], v201 offset:53248
	ds_read_b128 v[234:237], v201 offset:55296
	ds_read_b128 v[230:233], v202 offset:53248
	ds_read_b128 v[238:241], v202 offset:55296
	global_load_lds_dwordx4 v160, s[38:39] offset:128
	s_add_i32 m0, s99, 0x2000
	s_add_i32 s99, s44, 0x1bf80
	global_load_lds_dwordx4 v162, s[38:39] offset:128
	s_mov_b32 m0, s99
	s_nop 0
	global_load_lds_dwordx4 v160, s[40:41] offset:128
	s_add_i32 m0, s99, 0x2000
	s_nop 0
	global_load_lds_dwordx4 v162, s[40:41] offset:128
	s_waitcnt vmcnt(6)
	s_waitcnt lgkmcnt(0)
	s_barrier
	s_setprio 1
	s_waitcnt lgkmcnt(0)
	v_mfma_f32_16x16x128_f8f6f4 v[92:95], v[0:7], v[210:217], v[92:95]
	v_mfma_f32_16x16x128_f8f6f4 v[84:87], v[8:15], v[210:217], v[84:87]
	v_mfma_f32_16x16x128_f8f6f4 v[68:71], v[8:15], v[218:225], v[68:71]
	v_mfma_f32_16x16x128_f8f6f4 v[76:79], v[0:7], v[218:225], v[76:79]
	s_add_i32 m0, s65, 0xffffff80
	v_mfma_f32_16x16x128_f8f6f4 v[60:63], v[0:7], v[226:233], v[60:63]
	global_load_lds_dwordx4 v164, s[36:37] offset:128
	v_mfma_f32_16x16x128_f8f6f4 v[52:55], v[8:15], v[226:233], v[52:55]
	v_mfma_f32_16x16x128_f8f6f4 v[36:39], v[8:15], v[234:241], v[36:39]
	v_mfma_f32_16x16x128_f8f6f4 v[44:47], v[0:7], v[234:241], v[44:47]
	v_mfma_f32_16x16x128_f8f6f4 v[88:91], v[16:23], v[210:217], v[88:91]
	s_add_i32 m0, s66, 0xffffff80
	v_mfma_f32_16x16x128_f8f6f4 v[80:83], v[24:31], v[210:217], v[80:83]
	global_load_lds_dwordx4 v166, s[36:37] offset:128
	v_mfma_f32_16x16x128_f8f6f4 v[64:67], v[24:31], v[218:225], v[64:67]
	v_mfma_f32_16x16x128_f8f6f4 v[72:75], v[16:23], v[218:225], v[72:75]
	v_mfma_f32_16x16x128_f8f6f4 v[56:59], v[16:23], v[226:233], v[56:59]
	v_mfma_f32_16x16x128_f8f6f4 v[48:51], v[24:31], v[226:233], v[48:51]
	v_mfma_f32_16x16x128_f8f6f4 v[32:35], v[24:31], v[234:241], v[32:35]
	v_mfma_f32_16x16x128_f8f6f4 v[40:43], v[16:23], v[234:241], v[40:43]
	s_setprio 0
	s_barrier
	s_add_i32 s89, s89, 2
	s_add_u32 s4, s4, 0x100
	s_addc_u32 s5, s5, 0
	s_cmp_gt_u32 s89, 5
	s_cbranch_scc1 .LBB0_593

.Lc0_P6_0:
	v_mfma_f32_16x16x128_f8f6f4 v[156:159], v[24:31], v[182:189], 0
	v_mfma_f32_16x16x128_f8f6f4 v[148:151], v[16:23], v[182:189], 0
	v_mfma_f32_16x16x128_f8f6f4 v[132:135], v[16:23], v[210:217], 0
	v_mfma_f32_16x16x128_f8f6f4 v[140:143], v[24:31], v[210:217], 0
	v_mfma_f32_16x16x128_f8f6f4 v[124:127], v[24:31], v[218:225], 0
	v_mfma_f32_16x16x128_f8f6f4 v[116:119], v[16:23], v[218:225], 0
	v_mfma_f32_16x16x128_f8f6f4 v[100:103], v[16:23], v[226:233], 0
	v_mfma_f32_16x16x128_f8f6f4 v[108:111], v[24:31], v[226:233], 0
	v_mfma_f32_16x16x128_f8f6f4 v[152:155], v[8:15], v[182:189], 0
	v_mfma_f32_16x16x128_f8f6f4 v[144:147], v[0:7], v[182:189], 0
	v_mfma_f32_16x16x128_f8f6f4 v[128:131], v[0:7], v[210:217], 0
	v_mfma_f32_16x16x128_f8f6f4 v[136:139], v[8:15], v[210:217], 0
	v_mfma_f32_16x16x128_f8f6f4 v[120:123], v[8:15], v[218:225], 0
	v_mfma_f32_16x16x128_f8f6f4 v[112:115], v[0:7], v[218:225], 0
	v_mfma_f32_16x16x128_f8f6f4 v[96:99], v[0:7], v[226:233], 0
	v_mfma_f32_16x16x128_f8f6f4 v[104:107], v[8:15], v[226:233], 0
	s_branch .Lc0b_P6_0
.Lc0_P6_1:
	v_mfma_f32_16x16x128_f8f6f4 v[92:95], v[24:31], v[210:217], 0
	v_mfma_f32_16x16x128_f8f6f4 v[84:87], v[16:23], v[210:217], 0
	v_mfma_f32_16x16x128_f8f6f4 v[68:71], v[16:23], v[218:225], 0
	v_mfma_f32_16x16x128_f8f6f4 v[76:79], v[24:31], v[218:225], 0
	s_mov_b32 m0, s61
	v_mfma_f32_16x16x128_f8f6f4 v[60:63], v[24:31], v[226:233], 0
	global_load_lds_dwordx4 v164, s[36:37]
	v_mfma_f32_16x16x128_f8f6f4 v[52:55], v[16:23], v[226:233], 0
	v_mfma_f32_16x16x128_f8f6f4 v[36:39], v[16:23], v[234:241], 0
	v_mfma_f32_16x16x128_f8f6f4 v[44:47], v[24:31], v[234:241], 0
	v_mfma_f32_16x16x128_f8f6f4 v[88:91], v[8:15], v[210:217], 0
	s_mov_b32 m0, s62
	v_mfma_f32_16x16x128_f8f6f4 v[80:83], v[0:7], v[210:217], 0
	global_load_lds_dwordx4 v166, s[36:37]
	v_mfma_f32_16x16x128_f8f6f4 v[64:67], v[0:7], v[218:225], 0
	v_mfma_f32_16x16x128_f8f6f4 v[72:75], v[8:15], v[218:225], 0
	v_mfma_f32_16x16x128_f8f6f4 v[56:59], v[8:15], v[226:233], 0
	v_mfma_f32_16x16x128_f8f6f4 v[48:51], v[0:7], v[226:233], 0
	v_mfma_f32_16x16x128_f8f6f4 v[32:35], v[0:7], v[234:241], 0
	v_mfma_f32_16x16x128_f8f6f4 v[40:43], v[8:15], v[234:241], 0
	s_branch .Lc0b_P6_1

.LBB0_595:
	v_mbcnt_lo_u32_b32 v250, -1, 0
	v_mbcnt_hi_u32_b32 v250, -1, v250
	v_bfe_u32 v250, v250, 4, 1
	v_cmp_eq_u32_e32 vcc, 1, v250
	v_mov_b32_e32 v251, 0xffffc000
	v_mov_b32_e32 v250, -8
	s_nop 0
	v_cndmask_b32_e32 v250, v251, v250, vcc
	v_mov_b32_e32 v251, -1
	s_lshl_b32 s4, s84, 7
	v_mov_b32_e32 v17, v173
	v_mov_b32_e32 v0, v196
	s_or_b32 s4, s4, s69
	s_and_b64 vcc, exec, s[2:3]
	v_lshl_add_u32 v16, v0, 3, s4
	s_lshl_b32 s4, s85, 10
	s_and_b32 s4, s4, 0x400
	s_add_i32 s4, s70, s4
	v_lshl_add_u32 v0, v0, 5, s4
	ds_read_b128 v[12:15], v0
	ds_read_b128 v[4:7], v0 offset:16
	ds_read_b128 v[8:11], v0 offset:512
	ds_read_b128 v[0:3], v0 offset:528
	s_lshl_b32 s4, s83, 8
	s_waitcnt lgkmcnt(0)
	v_pk_fma_f32 v[20:21], v[156:157], s[22:23], v[12:13] op_sel_hi:[1,0,1]
	v_pk_fma_f32 v[26:27], v[158:159], s[22:23], v[14:15] op_sel_hi:[1,0,1]
	v_min_f32_e32 v20, 0x40e00000, v20
	v_min_f32_e32 v21, 0x40e00000, v21
	v_pk_mul_f32 v[22:23], v[20:21], s[24:25] op_sel_hi:[1,0]
	v_min_f32_e32 v26, 0x40e00000, v26
	v_exp_f32_e32 v22, v22
	v_exp_f32_e32 v23, v23
	v_min_f32_e32 v27, 0x40e00000, v27
	v_pk_mul_f32 v[28:29], v[26:27], s[24:25] op_sel_hi:[1,0]
	v_pk_fma_f32 v[24:25], v[152:153], s[22:23], v[8:9] op_sel_hi:[1,0,1]
	v_pk_add_f32 v[22:23], v[22:23], 1.0 op_sel_hi:[1,0]
	v_exp_f32_e32 v28, v28
	v_rcp_f32_e32 v22, v22
	v_rcp_f32_e32 v23, v23
	v_exp_f32_e32 v29, v29
	v_med3_f32 v24, v24, s78, v204
	v_med3_f32 v25, v25, s78, v204
	v_pk_mul_f32 v[20:21], v[20:21], v[22:23]
	v_pk_fma_f32 v[22:23], v[24:25], 4.0, 4.0 op_sel_hi:[1,0,0]
	v_pk_fma_f32 v[24:25], v[154:155], s[22:23], v[10:11] op_sel_hi:[1,0,1]
	v_pk_mul_f32 v[20:21], v[22:23], v[20:21]
	v_pk_add_f32 v[22:23], v[28:29], 1.0 op_sel_hi:[1,0]
	v_med3_f32 v24, v24, s78, v204
	v_rcp_f32_e32 v22, v22
	v_rcp_f32_e32 v23, v23
	v_med3_f32 v25, v25, s78, v204
	v_pk_fma_f32 v[24:25], v[24:25], 4.0, 4.0 op_sel_hi:[1,0,0]
	v_pk_fma_f32 v[30:31], v[150:151], s[22:23], v[6:7] op_sel_hi:[1,0,1]
	v_pk_mul_f32 v[22:23], v[26:27], v[22:23]
	v_min_f32_e32 v30, 0x40e00000, v30
	v_pk_mul_f32 v[22:23], v[24:25], v[22:23]
	v_pk_fma_f32 v[24:25], v[148:149], s[22:23], v[4:5] op_sel_hi:[1,0,1]
	v_min_f32_e32 v31, 0x40e00000, v31
	v_min_f32_e32 v24, 0x40e00000, v24
	v_min_f32_e32 v25, 0x40e00000, v25
	v_pk_mul_f32 v[26:27], v[24:25], s[24:25] op_sel_hi:[1,0]
	v_pk_fma_f32 v[28:29], v[144:145], s[22:23], v[0:1] op_sel_hi:[1,0,1]
	v_exp_f32_e32 v26, v26
	v_exp_f32_e32 v27, v27
	v_pk_mul_f32 v[144:145], v[30:31], s[24:25] op_sel_hi:[1,0]
	v_med3_f32 v28, v28, s78, v204
	v_exp_f32_e32 v144, v144
	v_pk_add_f32 v[26:27], v[26:27], 1.0 op_sel_hi:[1,0]
	v_exp_f32_e32 v145, v145
	v_rcp_f32_e32 v26, v26
	v_rcp_f32_e32 v27, v27
	v_med3_f32 v29, v29, s78, v204
	s_add_i32 s4, s4, s71
	v_add_u32_e32 v18, s4, v17
	v_pk_mul_f32 v[24:25], v[24:25], v[26:27]
	v_pk_fma_f32 v[26:27], v[28:29], 4.0, 4.0 op_sel_hi:[1,0,0]
	v_pk_fma_f32 v[28:29], v[146:147], s[22:23], v[2:3] op_sel_hi:[1,0,1]
	v_pk_mul_f32 v[24:25], v[26:27], v[24:25]
	v_pk_add_f32 v[26:27], v[144:145], 1.0 op_sel_hi:[1,0]
	v_med3_f32 v28, v28, s78, v204
	v_rcp_f32_e32 v26, v26
	v_rcp_f32_e32 v27, v27
	v_med3_f32 v29, v29, s78, v204
	v_ashrrev_i32_e32 v19, 31, v18
	v_ashrrev_i32_e32 v17, 31, v16
	v_pk_mul_f32 v[26:27], v[30:31], v[26:27]
	v_mov_b32_e32 v244, v165
	v_mov_b32_e32 v245, v165
	v_cvt_pk_fp8_f32 v244, v20, v21
	v_cvt_pk_fp8_f32 v245, v24, v25
	v_pk_fma_f32 v[20:21], v[28:29], 4.0, 4.0 op_sel_hi:[1,0,0]
	v_pk_fma_f32 v[24:25], v[136:137], s[22:23], v[8:9] op_sel_hi:[1,0,1]
	v_pk_mul_f32 v[20:21], v[20:21], v[26:27]
	v_cvt_pk_fp8_f32 v244, v22, v23 op_sel:[0,0,1]
	v_cvt_pk_fp8_f32 v245, v20, v21 op_sel:[0,0,1]
	v_lshlrev_b64 v[20:21], 10, v[18:19]
	v_lshl_add_u64 v[20:21], s[14:15], 0, v[20:21]
	v_lshl_add_u64 v[20:21], v[20:21], 0, v[16:17]
	v_pk_fma_f32 v[20:21], v[140:141], s[22:23], v[12:13] op_sel_hi:[1,0,1]
	v_pk_fma_f32 v[26:27], v[142:143], s[22:23], v[14:15] op_sel_hi:[1,0,1]
	v_min_f32_e32 v20, 0x40e00000, v20
	v_min_f32_e32 v21, 0x40e00000, v21
	v_pk_mul_f32 v[22:23], v[20:21], s[24:25] op_sel_hi:[1,0]
	v_min_f32_e32 v26, 0x40e00000, v26
	v_exp_f32_e32 v22, v22
	v_exp_f32_e32 v23, v23
	v_min_f32_e32 v27, 0x40e00000, v27
	v_pk_mul_f32 v[28:29], v[26:27], s[24:25] op_sel_hi:[1,0]
	v_med3_f32 v24, v24, s78, v204
	v_pk_add_f32 v[22:23], v[22:23], 1.0 op_sel_hi:[1,0]
	v_exp_f32_e32 v28, v28
	v_rcp_f32_e32 v22, v22
	v_rcp_f32_e32 v23, v23
	v_exp_f32_e32 v29, v29
	v_med3_f32 v25, v25, s78, v204
	v_pk_fma_f32 v[30:31], v[134:135], s[22:23], v[6:7] op_sel_hi:[1,0,1]
	v_pk_mul_f32 v[20:21], v[20:21], v[22:23]
	v_pk_fma_f32 v[22:23], v[24:25], 4.0, 4.0 op_sel_hi:[1,0,0]
	v_pk_fma_f32 v[24:25], v[138:139], s[22:23], v[10:11] op_sel_hi:[1,0,1]
	v_pk_mul_f32 v[20:21], v[22:23], v[20:21]
	v_pk_add_f32 v[22:23], v[28:29], 1.0 op_sel_hi:[1,0]
	v_med3_f32 v24, v24, s78, v204
	v_rcp_f32_e32 v22, v22
	v_rcp_f32_e32 v23, v23
	v_med3_f32 v25, v25, s78, v204
	v_pk_fma_f32 v[24:25], v[24:25], 4.0, 4.0 op_sel_hi:[1,0,0]
	v_min_f32_e32 v30, 0x40e00000, v30
	v_pk_mul_f32 v[22:23], v[26:27], v[22:23]
	v_min_f32_e32 v31, 0x40e00000, v31
	v_pk_mul_f32 v[22:23], v[24:25], v[22:23]
	v_pk_fma_f32 v[24:25], v[132:133], s[22:23], v[4:5] op_sel_hi:[1,0,1]
	v_pk_fma_f32 v[28:29], v[128:129], s[22:23], v[0:1] op_sel_hi:[1,0,1]
	v_min_f32_e32 v24, 0x40e00000, v24
	v_min_f32_e32 v25, 0x40e00000, v25
	v_pk_mul_f32 v[26:27], v[24:25], s[24:25] op_sel_hi:[1,0]
	v_pk_mul_f32 v[128:129], v[30:31], s[24:25] op_sel_hi:[1,0]
	v_exp_f32_e32 v26, v26
	v_exp_f32_e32 v27, v27
	v_exp_f32_e32 v128, v128
	v_exp_f32_e32 v129, v129
	v_med3_f32 v28, v28, s78, v204
	v_pk_add_f32 v[26:27], v[26:27], 1.0 op_sel_hi:[1,0]
	v_med3_f32 v29, v29, s78, v204
	v_rcp_f32_e32 v26, v26
	v_rcp_f32_e32 v27, v27
	s_mov_b64 s[2:3], -1
	v_pk_mul_f32 v[24:25], v[24:25], v[26:27]
	v_pk_fma_f32 v[26:27], v[28:29], 4.0, 4.0 op_sel_hi:[1,0,0]
	v_pk_fma_f32 v[28:29], v[130:131], s[22:23], v[2:3] op_sel_hi:[1,0,1]
	v_pk_mul_f32 v[24:25], v[26:27], v[24:25]
	v_pk_add_f32 v[26:27], v[128:129], 1.0 op_sel_hi:[1,0]
	v_med3_f32 v28, v28, s78, v204
	v_rcp_f32_e32 v26, v26
	v_rcp_f32_e32 v27, v27
	v_med3_f32 v29, v29, s78, v204
	v_pk_mul_f32 v[26:27], v[30:31], v[26:27]
	v_cvt_pk_fp8_f32 v247, v24, v25
	v_cvt_pk_fp8_f32 v246, v20, v21
	v_pk_fma_f32 v[20:21], v[28:29], 4.0, 4.0 op_sel_hi:[1,0,0]
	v_pk_fma_f32 v[24:25], v[120:121], s[22:23], v[8:9] op_sel_hi:[1,0,1]
	v_pk_mul_f32 v[20:21], v[20:21], v[26:27]
	v_cvt_pk_fp8_f32 v246, v22, v23 op_sel:[0,0,1]
	v_cvt_pk_fp8_f32 v247, v20, v21 op_sel:[0,0,1]
	v_add_u32_e32 v20, 16, v18
	v_ashrrev_i32_e32 v21, 31, v20
	v_lshlrev_b64 v[20:21], 10, v[20:21]
	v_lshl_add_u64 v[20:21], s[14:15], 0, v[20:21]
	v_lshl_add_u64 v[20:21], v[20:21], 0, v[16:17]
	s_nop 1
	v_permlane16_swap_b32_e32 v244, v246
	v_permlane16_swap_b32_e32 v245, v247
	v_lshl_add_u64 v[248:249], v[20:21], 0, v[250:251]
	global_store_dwordx4 v[248:249], v[244:247], off
	s_nop 1
	v_pk_fma_f32 v[20:21], v[124:125], s[22:23], v[12:13] op_sel_hi:[1,0,1]
	v_pk_fma_f32 v[26:27], v[126:127], s[22:23], v[14:15] op_sel_hi:[1,0,1]
	v_min_f32_e32 v20, 0x40e00000, v20
	v_min_f32_e32 v21, 0x40e00000, v21
	v_pk_mul_f32 v[22:23], v[20:21], s[24:25] op_sel_hi:[1,0]
	v_min_f32_e32 v26, 0x40e00000, v26
	v_exp_f32_e32 v22, v22
	v_exp_f32_e32 v23, v23
	v_min_f32_e32 v27, 0x40e00000, v27
	v_pk_mul_f32 v[28:29], v[26:27], s[24:25] op_sel_hi:[1,0]
	v_med3_f32 v24, v24, s78, v204
	v_pk_add_f32 v[22:23], v[22:23], 1.0 op_sel_hi:[1,0]
	v_exp_f32_e32 v28, v28
	v_rcp_f32_e32 v22, v22
	v_rcp_f32_e32 v23, v23
	v_exp_f32_e32 v29, v29
	v_med3_f32 v25, v25, s78, v204
	v_pk_fma_f32 v[30:31], v[118:119], s[22:23], v[6:7] op_sel_hi:[1,0,1]
	v_pk_mul_f32 v[20:21], v[20:21], v[22:23]
	v_pk_fma_f32 v[22:23], v[24:25], 4.0, 4.0 op_sel_hi:[1,0,0]
	v_pk_fma_f32 v[24:25], v[122:123], s[22:23], v[10:11] op_sel_hi:[1,0,1]
	v_pk_mul_f32 v[20:21], v[22:23], v[20:21]
	v_pk_add_f32 v[22:23], v[28:29], 1.0 op_sel_hi:[1,0]
	v_med3_f32 v24, v24, s78, v204
	v_rcp_f32_e32 v22, v22
	v_rcp_f32_e32 v23, v23
	v_med3_f32 v25, v25, s78, v204
	v_pk_fma_f32 v[24:25], v[24:25], 4.0, 4.0 op_sel_hi:[1,0,0]
	v_min_f32_e32 v30, 0x40e00000, v30
	v_pk_mul_f32 v[22:23], v[26:27], v[22:23]
	v_min_f32_e32 v31, 0x40e00000, v31
	v_pk_mul_f32 v[22:23], v[24:25], v[22:23]
	v_pk_fma_f32 v[24:25], v[116:117], s[22:23], v[4:5] op_sel_hi:[1,0,1]
	v_pk_fma_f32 v[28:29], v[112:113], s[22:23], v[0:1] op_sel_hi:[1,0,1]
	v_min_f32_e32 v24, 0x40e00000, v24
	v_min_f32_e32 v25, 0x40e00000, v25
	v_pk_mul_f32 v[26:27], v[24:25], s[24:25] op_sel_hi:[1,0]
	v_pk_mul_f32 v[112:113], v[30:31], s[24:25] op_sel_hi:[1,0]
	v_exp_f32_e32 v26, v26
	v_exp_f32_e32 v27, v27
	v_exp_f32_e32 v112, v112
	v_exp_f32_e32 v113, v113
	v_med3_f32 v28, v28, s78, v204
	v_pk_add_f32 v[26:27], v[26:27], 1.0 op_sel_hi:[1,0]
	v_med3_f32 v29, v29, s78, v204
	v_rcp_f32_e32 v26, v26
	v_rcp_f32_e32 v27, v27
	s_nop 0
	v_pk_mul_f32 v[24:25], v[24:25], v[26:27]
	v_pk_fma_f32 v[26:27], v[28:29], 4.0, 4.0 op_sel_hi:[1,0,0]
	v_pk_fma_f32 v[28:29], v[114:115], s[22:23], v[2:3] op_sel_hi:[1,0,1]
	v_pk_mul_f32 v[24:25], v[26:27], v[24:25]
	v_pk_add_f32 v[26:27], v[112:113], 1.0 op_sel_hi:[1,0]
	v_med3_f32 v28, v28, s78, v204
	v_rcp_f32_e32 v26, v26
	v_rcp_f32_e32 v27, v27
	v_med3_f32 v29, v29, s78, v204
	v_pk_mul_f32 v[26:27], v[30:31], v[26:27]
	v_mov_b32_e32 v245, v165
	v_mov_b32_e32 v244, v165
	v_cvt_pk_fp8_f32 v245, v24, v25
	v_cvt_pk_fp8_f32 v244, v20, v21
	v_pk_fma_f32 v[20:21], v[28:29], 4.0, 4.0 op_sel_hi:[1,0,0]
	v_pk_fma_f32 v[24:25], v[104:105], s[22:23], v[8:9] op_sel_hi:[1,0,1]
	v_pk_mul_f32 v[20:21], v[20:21], v[26:27]
	v_cvt_pk_fp8_f32 v244, v22, v23 op_sel:[0,0,1]
	v_cvt_pk_fp8_f32 v245, v20, v21 op_sel:[0,0,1]
	v_add_u32_e32 v20, 32, v18
	v_ashrrev_i32_e32 v21, 31, v20
	v_lshlrev_b64 v[20:21], 10, v[20:21]
	v_lshl_add_u64 v[20:21], s[14:15], 0, v[20:21]
	v_lshl_add_u64 v[20:21], v[20:21], 0, v[16:17]
	v_pk_fma_f32 v[20:21], v[108:109], s[22:23], v[12:13] op_sel_hi:[1,0,1]
	v_pk_fma_f32 v[26:27], v[110:111], s[22:23], v[14:15] op_sel_hi:[1,0,1]
	v_min_f32_e32 v20, 0x40e00000, v20
	v_min_f32_e32 v21, 0x40e00000, v21
	v_pk_mul_f32 v[22:23], v[20:21], s[24:25] op_sel_hi:[1,0]
	v_min_f32_e32 v26, 0x40e00000, v26
	v_exp_f32_e32 v22, v22
	v_exp_f32_e32 v23, v23
	v_min_f32_e32 v27, 0x40e00000, v27
	v_pk_mul_f32 v[28:29], v[26:27], s[24:25] op_sel_hi:[1,0]
	v_med3_f32 v24, v24, s78, v204
	v_pk_add_f32 v[22:23], v[22:23], 1.0 op_sel_hi:[1,0]
	v_exp_f32_e32 v28, v28
	v_rcp_f32_e32 v22, v22
	v_rcp_f32_e32 v23, v23
	v_exp_f32_e32 v29, v29
	v_med3_f32 v25, v25, s78, v204
	v_pk_fma_f32 v[30:31], v[102:103], s[22:23], v[6:7] op_sel_hi:[1,0,1]
	v_pk_mul_f32 v[20:21], v[20:21], v[22:23]
	v_pk_fma_f32 v[22:23], v[24:25], 4.0, 4.0 op_sel_hi:[1,0,0]
	v_pk_fma_f32 v[24:25], v[106:107], s[22:23], v[10:11] op_sel_hi:[1,0,1]
	v_pk_mul_f32 v[20:21], v[22:23], v[20:21]
	v_pk_add_f32 v[22:23], v[28:29], 1.0 op_sel_hi:[1,0]
	v_med3_f32 v24, v24, s78, v204
	v_rcp_f32_e32 v22, v22
	v_rcp_f32_e32 v23, v23
	v_med3_f32 v25, v25, s78, v204
	v_pk_fma_f32 v[24:25], v[24:25], 4.0, 4.0 op_sel_hi:[1,0,0]
	v_min_f32_e32 v30, 0x40e00000, v30
	v_pk_mul_f32 v[22:23], v[26:27], v[22:23]
	v_min_f32_e32 v31, 0x40e00000, v31
	v_pk_mul_f32 v[22:23], v[24:25], v[22:23]
	v_pk_fma_f32 v[24:25], v[100:101], s[22:23], v[4:5] op_sel_hi:[1,0,1]
	v_pk_fma_f32 v[28:29], v[96:97], s[22:23], v[0:1] op_sel_hi:[1,0,1]
	v_min_f32_e32 v24, 0x40e00000, v24
	v_min_f32_e32 v25, 0x40e00000, v25
	v_pk_mul_f32 v[26:27], v[24:25], s[24:25] op_sel_hi:[1,0]
	v_pk_mul_f32 v[96:97], v[30:31], s[24:25] op_sel_hi:[1,0]
	v_exp_f32_e32 v26, v26
	v_exp_f32_e32 v27, v27
	v_exp_f32_e32 v96, v96
	v_exp_f32_e32 v97, v97
	v_med3_f32 v28, v28, s78, v204
	v_pk_add_f32 v[26:27], v[26:27], 1.0 op_sel_hi:[1,0]
	v_med3_f32 v29, v29, s78, v204
	v_rcp_f32_e32 v26, v26
	v_rcp_f32_e32 v27, v27
	s_nop 0
	v_pk_mul_f32 v[24:25], v[24:25], v[26:27]
	v_pk_fma_f32 v[26:27], v[28:29], 4.0, 4.0 op_sel_hi:[1,0,0]
	v_pk_fma_f32 v[28:29], v[98:99], s[22:23], v[2:3] op_sel_hi:[1,0,1]
	v_pk_mul_f32 v[24:25], v[26:27], v[24:25]
	v_pk_add_f32 v[26:27], v[96:97], 1.0 op_sel_hi:[1,0]
	v_med3_f32 v28, v28, s78, v204
	v_rcp_f32_e32 v26, v26
	v_rcp_f32_e32 v27, v27
	v_med3_f32 v29, v29, s78, v204
	v_pk_mul_f32 v[26:27], v[30:31], v[26:27]
	v_cvt_pk_fp8_f32 v246, v20, v21
	v_cvt_pk_fp8_f32 v247, v24, v25
	v_pk_fma_f32 v[20:21], v[28:29], 4.0, 4.0 op_sel_hi:[1,0,0]
	v_cvt_pk_fp8_f32 v246, v22, v23 op_sel:[0,0,1]
	v_pk_fma_f32 v[22:23], v[92:93], s[22:23], v[12:13] op_sel_hi:[1,0,1]
	v_pk_mul_f32 v[20:21], v[20:21], v[26:27]
	v_min_f32_e32 v22, 0x40e00000, v22
	v_min_f32_e32 v23, 0x40e00000, v23
	v_pk_mul_f32 v[24:25], v[22:23], s[24:25] op_sel_hi:[1,0]
	v_cvt_pk_fp8_f32 v247, v20, v21 op_sel:[0,0,1]
	v_add_u32_e32 v20, 48, v18
	v_exp_f32_e32 v24, v24
	v_exp_f32_e32 v25, v25
	v_ashrrev_i32_e32 v21, 31, v20
	v_lshlrev_b64 v[20:21], 10, v[20:21]
	v_lshl_add_u64 v[20:21], s[14:15], 0, v[20:21]
	v_pk_fma_f32 v[28:29], v[94:95], s[22:23], v[14:15] op_sel_hi:[1,0,1]
	v_lshl_add_u64 v[20:21], v[20:21], 0, v[16:17]
	v_pk_add_f32 v[24:25], v[24:25], 1.0 op_sel_hi:[1,0]
	v_min_f32_e32 v28, 0x40e00000, v28
	v_min_f32_e32 v29, 0x40e00000, v29
	s_nop 1
	v_permlane16_swap_b32_e32 v244, v246
	v_permlane16_swap_b32_e32 v245, v247
	v_lshl_add_u64 v[248:249], v[20:21], 0, v[250:251]
	global_store_dwordx4 v[248:249], v[244:247], off
	s_nop 1
	v_rcp_f32_e32 v24, v24
	v_rcp_f32_e32 v25, v25
	v_pk_mul_f32 v[30:31], v[28:29], s[24:25] op_sel_hi:[1,0]
	v_pk_fma_f32 v[26:27], v[88:89], s[22:23], v[8:9] op_sel_hi:[1,0,1]
	v_exp_f32_e32 v30, v30
	v_exp_f32_e32 v31, v31
	v_med3_f32 v26, v26, s78, v204
	v_med3_f32 v27, v27, s78, v204
	v_pk_mul_f32 v[22:23], v[22:23], v[24:25]
	v_pk_fma_f32 v[24:25], v[26:27], 4.0, 4.0 op_sel_hi:[1,0,0]
	v_pk_fma_f32 v[26:27], v[90:91], s[22:23], v[10:11] op_sel_hi:[1,0,1]
	v_pk_mul_f32 v[22:23], v[24:25], v[22:23]
	v_pk_add_f32 v[24:25], v[30:31], 1.0 op_sel_hi:[1,0]
	v_med3_f32 v26, v26, s78, v204
	v_rcp_f32_e32 v24, v24
	v_rcp_f32_e32 v25, v25
	v_med3_f32 v27, v27, s78, v204
	v_pk_fma_f32 v[26:27], v[26:27], 4.0, 4.0 op_sel_hi:[1,0,0]
	v_pk_fma_f32 v[30:31], v[80:81], s[22:23], v[0:1] op_sel_hi:[1,0,1]
	v_pk_mul_f32 v[24:25], v[28:29], v[24:25]
	v_pk_fma_f32 v[80:81], v[86:87], s[22:23], v[6:7] op_sel_hi:[1,0,1]
	v_pk_mul_f32 v[24:25], v[26:27], v[24:25]
	v_pk_fma_f32 v[26:27], v[84:85], s[22:23], v[4:5] op_sel_hi:[1,0,1]
	v_min_f32_e32 v80, 0x40e00000, v80
	v_min_f32_e32 v26, 0x40e00000, v26
	v_min_f32_e32 v27, 0x40e00000, v27
	v_pk_mul_f32 v[28:29], v[26:27], s[24:25] op_sel_hi:[1,0]
	v_min_f32_e32 v81, 0x40e00000, v81
	v_exp_f32_e32 v28, v28
	v_exp_f32_e32 v29, v29
	v_pk_mul_f32 v[84:85], v[80:81], s[24:25] op_sel_hi:[1,0]
	v_med3_f32 v30, v30, s78, v204
	v_exp_f32_e32 v84, v84
	v_pk_add_f32 v[28:29], v[28:29], 1.0 op_sel_hi:[1,0]
	v_exp_f32_e32 v85, v85
	v_rcp_f32_e32 v28, v28
	v_rcp_f32_e32 v29, v29
	v_med3_f32 v31, v31, s78, v204
	v_add_u32_e32 v20, 0x80, v18
	v_ashrrev_i32_e32 v21, 31, v20
	v_pk_mul_f32 v[26:27], v[26:27], v[28:29]
	v_pk_fma_f32 v[28:29], v[30:31], 4.0, 4.0 op_sel_hi:[1,0,0]
	v_pk_fma_f32 v[30:31], v[82:83], s[22:23], v[2:3] op_sel_hi:[1,0,1]
	v_pk_mul_f32 v[26:27], v[28:29], v[26:27]
	v_pk_add_f32 v[28:29], v[84:85], 1.0 op_sel_hi:[1,0]
	v_med3_f32 v30, v30, s78, v204
	v_rcp_f32_e32 v28, v28
	v_rcp_f32_e32 v29, v29
	v_med3_f32 v31, v31, s78, v204
	v_lshlrev_b64 v[20:21], 10, v[20:21]
	v_lshl_add_u64 v[20:21], s[14:15], 0, v[20:21]
	v_pk_mul_f32 v[28:29], v[80:81], v[28:29]
	v_mov_b32_e32 v244, v165
	v_mov_b32_e32 v245, v165
	v_cvt_pk_fp8_f32 v244, v22, v23
	v_cvt_pk_fp8_f32 v245, v26, v27
	v_pk_fma_f32 v[22:23], v[30:31], 4.0, 4.0 op_sel_hi:[1,0,0]
	v_lshl_add_u64 v[20:21], v[20:21], 0, v[16:17]
	v_pk_mul_f32 v[22:23], v[22:23], v[28:29]
	v_cvt_pk_fp8_f32 v244, v24, v25 op_sel:[0,0,1]
	v_cvt_pk_fp8_f32 v245, v22, v23 op_sel:[0,0,1]
	v_pk_fma_f32 v[26:27], v[78:79], s[22:23], v[14:15] op_sel_hi:[1,0,1]
	v_pk_fma_f32 v[24:25], v[72:73], s[22:23], v[8:9] op_sel_hi:[1,0,1]
	v_min_f32_e32 v26, 0x40e00000, v26
	v_pk_fma_f32 v[20:21], v[76:77], s[22:23], v[12:13] op_sel_hi:[1,0,1]
	v_min_f32_e32 v27, 0x40e00000, v27
	v_min_f32_e32 v20, 0x40e00000, v20
	v_min_f32_e32 v21, 0x40e00000, v21
	v_pk_mul_f32 v[22:23], v[20:21], s[24:25] op_sel_hi:[1,0]
	v_pk_mul_f32 v[28:29], v[26:27], s[24:25] op_sel_hi:[1,0]
	v_exp_f32_e32 v22, v22
	v_exp_f32_e32 v23, v23
	v_exp_f32_e32 v28, v28
	v_exp_f32_e32 v29, v29
	v_med3_f32 v24, v24, s78, v204
	v_pk_add_f32 v[22:23], v[22:23], 1.0 op_sel_hi:[1,0]
	v_med3_f32 v25, v25, s78, v204
	v_rcp_f32_e32 v22, v22
	v_rcp_f32_e32 v23, v23
	v_pk_fma_f32 v[30:31], v[70:71], s[22:23], v[6:7] op_sel_hi:[1,0,1]
	v_pk_mul_f32 v[20:21], v[20:21], v[22:23]
	v_pk_fma_f32 v[22:23], v[24:25], 4.0, 4.0 op_sel_hi:[1,0,0]
	v_pk_fma_f32 v[24:25], v[74:75], s[22:23], v[10:11] op_sel_hi:[1,0,1]
	v_pk_mul_f32 v[20:21], v[22:23], v[20:21]
	v_pk_add_f32 v[22:23], v[28:29], 1.0 op_sel_hi:[1,0]
	v_med3_f32 v24, v24, s78, v204
	v_rcp_f32_e32 v22, v22
	v_rcp_f32_e32 v23, v23
	v_med3_f32 v25, v25, s78, v204
	v_pk_fma_f32 v[24:25], v[24:25], 4.0, 4.0 op_sel_hi:[1,0,0]
	v_min_f32_e32 v30, 0x40e00000, v30
	v_pk_mul_f32 v[22:23], v[26:27], v[22:23]
	v_min_f32_e32 v31, 0x40e00000, v31
	v_pk_mul_f32 v[22:23], v[24:25], v[22:23]
	v_pk_fma_f32 v[24:25], v[68:69], s[22:23], v[4:5] op_sel_hi:[1,0,1]
	v_pk_fma_f32 v[28:29], v[64:65], s[22:23], v[0:1] op_sel_hi:[1,0,1]
	v_min_f32_e32 v24, 0x40e00000, v24
	v_min_f32_e32 v25, 0x40e00000, v25
	v_pk_mul_f32 v[26:27], v[24:25], s[24:25] op_sel_hi:[1,0]
	v_pk_mul_f32 v[64:65], v[30:31], s[24:25] op_sel_hi:[1,0]
	v_exp_f32_e32 v26, v26
	v_exp_f32_e32 v27, v27
	v_exp_f32_e32 v64, v64
	v_exp_f32_e32 v65, v65
	v_med3_f32 v28, v28, s78, v204
	v_pk_add_f32 v[26:27], v[26:27], 1.0 op_sel_hi:[1,0]
	v_med3_f32 v29, v29, s78, v204
	v_rcp_f32_e32 v26, v26
	v_rcp_f32_e32 v27, v27
	s_nop 0
	v_pk_mul_f32 v[24:25], v[24:25], v[26:27]
	v_pk_fma_f32 v[26:27], v[28:29], 4.0, 4.0 op_sel_hi:[1,0,0]
	v_pk_fma_f32 v[28:29], v[66:67], s[22:23], v[2:3] op_sel_hi:[1,0,1]
	v_pk_mul_f32 v[24:25], v[26:27], v[24:25]
	v_pk_add_f32 v[26:27], v[64:65], 1.0 op_sel_hi:[1,0]
	v_med3_f32 v28, v28, s78, v204
	v_rcp_f32_e32 v26, v26
	v_rcp_f32_e32 v27, v27
	v_med3_f32 v29, v29, s78, v204
	v_pk_mul_f32 v[26:27], v[30:31], v[26:27]
	v_cvt_pk_fp8_f32 v247, v24, v25
	v_cvt_pk_fp8_f32 v246, v20, v21
	v_pk_fma_f32 v[20:21], v[28:29], 4.0, 4.0 op_sel_hi:[1,0,0]
	v_pk_fma_f32 v[24:25], v[56:57], s[22:23], v[8:9] op_sel_hi:[1,0,1]
	v_pk_mul_f32 v[20:21], v[20:21], v[26:27]
	v_cvt_pk_fp8_f32 v246, v22, v23 op_sel:[0,0,1]
	v_cvt_pk_fp8_f32 v247, v20, v21 op_sel:[0,0,1]
	v_add_u32_e32 v20, 0x90, v18
	v_ashrrev_i32_e32 v21, 31, v20
	v_lshlrev_b64 v[20:21], 10, v[20:21]
	v_lshl_add_u64 v[20:21], s[14:15], 0, v[20:21]
	v_lshl_add_u64 v[20:21], v[20:21], 0, v[16:17]
	s_nop 1
	v_permlane16_swap_b32_e32 v244, v246
	v_permlane16_swap_b32_e32 v245, v247
	v_lshl_add_u64 v[248:249], v[20:21], 0, v[250:251]
	global_store_dwordx4 v[248:249], v[244:247], off
	s_nop 1
	v_pk_fma_f32 v[20:21], v[60:61], s[22:23], v[12:13] op_sel_hi:[1,0,1]
	v_pk_fma_f32 v[26:27], v[62:63], s[22:23], v[14:15] op_sel_hi:[1,0,1]
	v_min_f32_e32 v20, 0x40e00000, v20
	v_min_f32_e32 v21, 0x40e00000, v21
	v_pk_mul_f32 v[22:23], v[20:21], s[24:25] op_sel_hi:[1,0]
	v_min_f32_e32 v26, 0x40e00000, v26
	v_exp_f32_e32 v22, v22
	v_exp_f32_e32 v23, v23
	v_min_f32_e32 v27, 0x40e00000, v27
	v_pk_mul_f32 v[28:29], v[26:27], s[24:25] op_sel_hi:[1,0]
	v_med3_f32 v24, v24, s78, v204
	v_pk_add_f32 v[22:23], v[22:23], 1.0 op_sel_hi:[1,0]
	v_exp_f32_e32 v28, v28
	v_rcp_f32_e32 v22, v22
	v_rcp_f32_e32 v23, v23
	v_exp_f32_e32 v29, v29
	v_med3_f32 v25, v25, s78, v204
	v_pk_fma_f32 v[30:31], v[54:55], s[22:23], v[6:7] op_sel_hi:[1,0,1]
	v_pk_mul_f32 v[20:21], v[20:21], v[22:23]
	v_pk_fma_f32 v[22:23], v[24:25], 4.0, 4.0 op_sel_hi:[1,0,0]
	v_pk_fma_f32 v[24:25], v[58:59], s[22:23], v[10:11] op_sel_hi:[1,0,1]
	v_pk_mul_f32 v[20:21], v[22:23], v[20:21]
	v_pk_add_f32 v[22:23], v[28:29], 1.0 op_sel_hi:[1,0]
	v_med3_f32 v24, v24, s78, v204
	v_rcp_f32_e32 v22, v22
	v_rcp_f32_e32 v23, v23
	v_med3_f32 v25, v25, s78, v204
	v_pk_fma_f32 v[24:25], v[24:25], 4.0, 4.0 op_sel_hi:[1,0,0]
	v_min_f32_e32 v30, 0x40e00000, v30
	v_pk_mul_f32 v[22:23], v[26:27], v[22:23]
	v_min_f32_e32 v31, 0x40e00000, v31
	v_pk_mul_f32 v[22:23], v[24:25], v[22:23]
	v_pk_fma_f32 v[24:25], v[52:53], s[22:23], v[4:5] op_sel_hi:[1,0,1]
	v_pk_fma_f32 v[28:29], v[48:49], s[22:23], v[0:1] op_sel_hi:[1,0,1]
	v_min_f32_e32 v24, 0x40e00000, v24
	v_min_f32_e32 v25, 0x40e00000, v25
	v_pk_mul_f32 v[26:27], v[24:25], s[24:25] op_sel_hi:[1,0]
	v_pk_mul_f32 v[48:49], v[30:31], s[24:25] op_sel_hi:[1,0]
	v_exp_f32_e32 v26, v26
	v_exp_f32_e32 v27, v27
	v_exp_f32_e32 v48, v48
	v_exp_f32_e32 v49, v49
	v_med3_f32 v28, v28, s78, v204
	v_pk_add_f32 v[26:27], v[26:27], 1.0 op_sel_hi:[1,0]
	v_med3_f32 v29, v29, s78, v204
	v_rcp_f32_e32 v26, v26
	v_rcp_f32_e32 v27, v27
	v_pk_fma_f32 v[12:13], v[44:45], s[22:23], v[12:13] op_sel_hi:[1,0,1]
	v_pk_fma_f32 v[14:15], v[46:47], s[22:23], v[14:15] op_sel_hi:[1,0,1]
	v_min_f32_e32 v12, 0x40e00000, v12
	v_pk_mul_f32 v[24:25], v[24:25], v[26:27]
	v_pk_fma_f32 v[26:27], v[28:29], 4.0, 4.0 op_sel_hi:[1,0,0]
	v_pk_fma_f32 v[28:29], v[50:51], s[22:23], v[2:3] op_sel_hi:[1,0,1]
	v_pk_mul_f32 v[24:25], v[26:27], v[24:25]
	v_pk_add_f32 v[26:27], v[48:49], 1.0 op_sel_hi:[1,0]
	v_med3_f32 v28, v28, s78, v204
	v_rcp_f32_e32 v26, v26
	v_rcp_f32_e32 v27, v27
	v_med3_f32 v29, v29, s78, v204
	v_min_f32_e32 v13, 0x40e00000, v13
	v_min_f32_e32 v14, 0x40e00000, v14
	v_pk_mul_f32 v[26:27], v[30:31], v[26:27]
	v_mov_b32_e32 v245, v165
	v_mov_b32_e32 v244, v165
	v_cvt_pk_fp8_f32 v245, v24, v25
	v_cvt_pk_fp8_f32 v244, v20, v21
	v_pk_fma_f32 v[20:21], v[28:29], 4.0, 4.0 op_sel_hi:[1,0,0]
	v_min_f32_e32 v15, 0x40e00000, v15
	v_pk_mul_f32 v[20:21], v[20:21], v[26:27]
	v_cvt_pk_fp8_f32 v244, v22, v23 op_sel:[0,0,1]
	v_cvt_pk_fp8_f32 v245, v20, v21 op_sel:[0,0,1]
	v_add_u32_e32 v20, 0xa0, v18
	v_ashrrev_i32_e32 v21, 31, v20
	v_lshlrev_b64 v[20:21], 10, v[20:21]
	v_lshl_add_u64 v[20:21], s[14:15], 0, v[20:21]
	v_lshl_add_u64 v[20:21], v[20:21], 0, v[16:17]
	v_pk_mul_f32 v[20:21], v[12:13], s[24:25] op_sel_hi:[1,0]
	v_pk_mul_f32 v[22:23], v[14:15], s[24:25] op_sel_hi:[1,0]
	v_exp_f32_e32 v20, v20
	v_exp_f32_e32 v21, v21
	v_exp_f32_e32 v22, v22
	v_exp_f32_e32 v23, v23
	v_pk_fma_f32 v[8:9], v[40:41], s[22:23], v[8:9] op_sel_hi:[1,0,1]
	v_pk_add_f32 v[20:21], v[20:21], 1.0 op_sel_hi:[1,0]
	v_med3_f32 v8, v8, s78, v204
	v_rcp_f32_e32 v20, v20
	v_rcp_f32_e32 v21, v21
	v_med3_f32 v9, v9, s78, v204
	v_pk_fma_f32 v[8:9], v[8:9], 4.0, 4.0 op_sel_hi:[1,0,0]
	v_pk_fma_f32 v[10:11], v[42:43], s[22:23], v[10:11] op_sel_hi:[1,0,1]
	v_pk_mul_f32 v[12:13], v[12:13], v[20:21]
	v_med3_f32 v10, v10, s78, v204
	v_pk_mul_f32 v[8:9], v[8:9], v[12:13]
	v_pk_add_f32 v[12:13], v[22:23], 1.0 op_sel_hi:[1,0]
	v_med3_f32 v11, v11, s78, v204
	v_rcp_f32_e32 v12, v12
	v_rcp_f32_e32 v13, v13
	v_pk_fma_f32 v[4:5], v[36:37], s[22:23], v[4:5] op_sel_hi:[1,0,1]
	v_pk_fma_f32 v[10:11], v[10:11], 4.0, 4.0 op_sel_hi:[1,0,0]
	v_min_f32_e32 v4, 0x40e00000, v4
	v_pk_mul_f32 v[12:13], v[14:15], v[12:13]
	v_min_f32_e32 v5, 0x40e00000, v5
	v_pk_mul_f32 v[10:11], v[10:11], v[12:13]
	v_pk_mul_f32 v[12:13], v[4:5], s[24:25] op_sel_hi:[1,0]
	v_pk_fma_f32 v[6:7], v[38:39], s[22:23], v[6:7] op_sel_hi:[1,0,1]
	v_exp_f32_e32 v12, v12
	v_exp_f32_e32 v13, v13
	v_min_f32_e32 v6, 0x40e00000, v6
	v_min_f32_e32 v7, 0x40e00000, v7
	v_pk_mul_f32 v[14:15], v[6:7], s[24:25] op_sel_hi:[1,0]
	v_pk_add_f32 v[12:13], v[12:13], 1.0 op_sel_hi:[1,0]
	v_exp_f32_e32 v14, v14
	v_rcp_f32_e32 v12, v12
	v_rcp_f32_e32 v13, v13
	v_exp_f32_e32 v15, v15
	v_pk_fma_f32 v[0:1], v[32:33], s[22:23], v[0:1] op_sel_hi:[1,0,1]
	v_pk_fma_f32 v[2:3], v[34:35], s[22:23], v[2:3] op_sel_hi:[1,0,1]
	v_med3_f32 v0, v0, s78, v204
	v_med3_f32 v1, v1, s78, v204
	v_pk_mul_f32 v[4:5], v[4:5], v[12:13]
	v_pk_fma_f32 v[0:1], v[0:1], 4.0, 4.0 op_sel_hi:[1,0,0]
	v_med3_f32 v2, v2, s78, v204
	v_pk_mul_f32 v[0:1], v[0:1], v[4:5]
	v_pk_add_f32 v[4:5], v[14:15], 1.0 op_sel_hi:[1,0]
	v_med3_f32 v3, v3, s78, v204
	v_rcp_f32_e32 v4, v4
	v_rcp_f32_e32 v5, v5
	s_nop 0
	v_pk_mul_f32 v[4:5], v[6:7], v[4:5]
	v_cvt_pk_fp8_f32 v247, v0, v1
	v_cvt_pk_fp8_f32 v246, v8, v9
	v_pk_fma_f32 v[0:1], v[2:3], 4.0, 4.0 op_sel_hi:[1,0,0]
	v_cvt_pk_fp8_f32 v246, v10, v11 op_sel:[0,0,1]
	v_pk_mul_f32 v[0:1], v[0:1], v[4:5]
	s_nop 0
	v_cvt_pk_fp8_f32 v247, v0, v1 op_sel:[0,0,1]
	v_add_u32_e32 v0, 0xb0, v18
	v_ashrrev_i32_e32 v1, 31, v0
	v_lshlrev_b64 v[0:1], 10, v[0:1]
	v_lshl_add_u64 v[0:1], s[14:15], 0, v[0:1]
	v_lshl_add_u64 v[0:1], v[0:1], 0, v[16:17]
	s_nop 1
	v_permlane16_swap_b32_e32 v244, v246
	v_permlane16_swap_b32_e32 v245, v247
	v_lshl_add_u64 v[248:249], v[0:1], 0, v[250:251]
	global_store_dwordx4 v[248:249], v[244:247], off
	s_nop 1
	s_cbranch_vccnz .LBB0_581
	s_andn2_b64 vcc, exec, s[12:13]
	s_cbranch_vccnz .LBB0_580
	s_barrier
	s_branch .LBB0_580

.LBB0_671:
	s_add_u32 s27, s34, 0x100
	s_addc_u32 s82, s35, 0
	v_mov_b32_e32 v167, v165
	v_mov_b32_e32 v169, v165
	s_add_u32 s83, s38, 0x100
	v_mov_b32_e32 v175, v165
	v_mov_b32_e32 v177, v165
	v_lshl_add_u64 v[178:179], s[16:17], 0, v[168:169]
	v_lshl_add_u64 v[180:181], s[16:17], 0, v[166:167]
	s_addc_u32 s84, s39, 0
	s_mov_b32 s85, -2
	s_mov_b64 s[34:35], 0
	v_add_u32_e32 v252, 0x10000, v205
	v_add_u32_e32 v253, 0x10000, v206
	s_branch .LBB0_673
.LBB0_672:
	s_add_u32 s36, s6, s34
	s_addc_u32 s37, s7, s35
	s_add_u32 s38, s36, 0x12c00100
	s_addc_u32 s39, s37, 0
	ds_read_b128 v[24:27], v252
	ds_read_b128 v[28:31], v253
	s_and_b64 s[36:37], s[40:41], exec
	ds_read_b128 v[16:19], v252 offset:2048
	ds_read_b128 v[20:23], v253 offset:2048
	s_cselect_b32 s37, s9, s39
	s_cselect_b32 s36, s8, s38
	s_add_u32 s86, s27, s34
	ds_read_b128 v[8:11], v252 offset:16384
	ds_read_b128 v[12:15], v253 offset:16384
	s_addc_u32 s87, s82, s35
	ds_read_b128 v[0:3], v252 offset:18432
	ds_read_b128 v[4:7], v253 offset:18432
	s_and_b64 s[38:39], s[40:41], exec
	s_cselect_b32 s39, s29, s87
	s_cselect_b32 s38, s28, s86
	s_add_u32 s86, s83, s34
	s_addc_u32 s87, s84, s35
	s_and_b64 s[40:41], s[40:41], exec
	s_cselect_b32 s41, s31, s87
	s_cselect_b32 s40, s30, s86
	s_add_u32 s100, s16, s34
	s_addc_u32 s101, s17, s35
	s_add_i32 m0, s59, 0xc000
	ds_read_b128 v[186:189], v207
	ds_read_b128 v[216:219], v207 offset:2048
	ds_read_b128 v[190:193], v208
	ds_read_b128 v[220:223], v208 offset:2048
	ds_read_b128 v[224:227], v207 offset:4096
	ds_read_b128 v[232:235], v207 offset:6144
	ds_read_b128 v[228:231], v208 offset:4096
	ds_read_b128 v[236:239], v208 offset:6144
	global_load_lds_dwordx4 v166, s[100:101]
	s_add_i32 m0, s59, 0xe000
	s_nop 0
	global_load_lds_dwordx4 v168, s[100:101]
	s_waitcnt vmcnt(8)
	s_waitcnt lgkmcnt(0)
	s_barrier
	s_setprio 1
	s_waitcnt lgkmcnt(0)
	s_cmp_eq_u32 s34, 0
	s_cbranch_scc1 .Lc0_P7_0
	v_mfma_f32_16x16x128_f8f6f4 v[156:159], v[24:31], v[186:193], v[156:159]
	v_mfma_f32_16x16x128_f8f6f4 v[152:155], v[16:23], v[186:193], v[152:155]
	v_mfma_f32_16x16x128_f8f6f4 v[136:139], v[16:23], v[216:223], v[136:139]
	v_mfma_f32_16x16x128_f8f6f4 v[140:143], v[24:31], v[216:223], v[140:143]
	v_mfma_f32_16x16x128_f8f6f4 v[124:127], v[24:31], v[224:231], v[124:127]
	v_mfma_f32_16x16x128_f8f6f4 v[120:123], v[16:23], v[224:231], v[120:123]
	v_mfma_f32_16x16x128_f8f6f4 v[104:107], v[16:23], v[232:239], v[104:107]
	v_mfma_f32_16x16x128_f8f6f4 v[108:111], v[24:31], v[232:239], v[108:111]
	v_mfma_f32_16x16x128_f8f6f4 v[148:151], v[8:15], v[186:193], v[148:151]
	v_mfma_f32_16x16x128_f8f6f4 v[144:147], v[0:7], v[186:193], v[144:147]
	v_mfma_f32_16x16x128_f8f6f4 v[128:131], v[0:7], v[216:223], v[128:131]
	v_mfma_f32_16x16x128_f8f6f4 v[132:135], v[8:15], v[216:223], v[132:135]
	v_mfma_f32_16x16x128_f8f6f4 v[116:119], v[8:15], v[224:231], v[116:119]
	v_mfma_f32_16x16x128_f8f6f4 v[112:115], v[0:7], v[224:231], v[112:115]
	v_mfma_f32_16x16x128_f8f6f4 v[96:99], v[0:7], v[232:239], v[96:99]
	v_mfma_f32_16x16x128_f8f6f4 v[100:103], v[8:15], v[232:239], v[100:103]
.Lc0b_P7_0:
	s_setprio 0
	s_barrier
	s_add_i32 s86, s69, s42
	s_mov_b32 m0, s86
	ds_read_b128 v[216:219], v207 offset:16384
	ds_read_b128 v[224:227], v207 offset:18432
	ds_read_b128 v[220:223], v208 offset:16384
	ds_read_b128 v[228:231], v208 offset:18432
	ds_read_b128 v[232:235], v207 offset:20480
	ds_read_b128 v[240:243], v207 offset:22528
	ds_read_b128 v[236:239], v208 offset:20480
	ds_read_b128 v[244:247], v208 offset:22528
	global_load_lds_dwordx4 v160, s[38:39]
	s_add_i32 m0, s86, 0x2000
	s_add_i32 s98, s71, s42
	global_load_lds_dwordx4 v162, s[38:39]
	s_mov_b32 m0, s98
	s_nop 0
	global_load_lds_dwordx4 v160, s[40:41]
	s_add_i32 m0, s98, 0x2000
	v_mov_b32_e32 v173, v165
	global_load_lds_dwordx4 v162, s[40:41]
	s_waitcnt vmcnt(6)
	s_waitcnt lgkmcnt(0)
	s_barrier
	s_setprio 1
	s_waitcnt lgkmcnt(0)
	s_cmp_eq_u32 s34, 0
	s_cbranch_scc1 .Lc0_P7_1
	v_mfma_f32_16x16x128_f8f6f4 v[92:95], v[24:31], v[216:223], v[92:95]
	v_mfma_f32_16x16x128_f8f6f4 v[88:91], v[16:23], v[216:223], v[88:91]
	v_mfma_f32_16x16x128_f8f6f4 v[72:75], v[16:23], v[224:231], v[72:75]
	v_mfma_f32_16x16x128_f8f6f4 v[76:79], v[24:31], v[224:231], v[76:79]
	s_mov_b32 m0, s59
	v_mfma_f32_16x16x128_f8f6f4 v[60:63], v[24:31], v[232:239], v[60:63]
	global_load_lds_dwordx4 v164, s[36:37]
	v_mfma_f32_16x16x128_f8f6f4 v[56:59], v[16:23], v[232:239], v[56:59]
	v_mfma_f32_16x16x128_f8f6f4 v[40:43], v[16:23], v[240:247], v[40:43]
	v_mfma_f32_16x16x128_f8f6f4 v[44:47], v[24:31], v[240:247], v[44:47]
	v_mfma_f32_16x16x128_f8f6f4 v[84:87], v[8:15], v[216:223], v[84:87]
	s_mov_b32 m0, s60
	v_mfma_f32_16x16x128_f8f6f4 v[80:83], v[0:7], v[216:223], v[80:83]
	global_load_lds_dwordx4 v172, s[36:37]
	v_mfma_f32_16x16x128_f8f6f4 v[64:67], v[0:7], v[224:231], v[64:67]
	v_mfma_f32_16x16x128_f8f6f4 v[68:71], v[8:15], v[224:231], v[68:71]
	v_mfma_f32_16x16x128_f8f6f4 v[52:55], v[8:15], v[232:239], v[52:55]
	v_mfma_f32_16x16x128_f8f6f4 v[48:51], v[0:7], v[232:239], v[48:51]
	v_mfma_f32_16x16x128_f8f6f4 v[32:35], v[0:7], v[240:247], v[32:35]
	v_mfma_f32_16x16x128_f8f6f4 v[36:39], v[8:15], v[240:247], v[36:39]
.Lc0b_P7_1:
	s_setprio 0
	s_barrier
	ds_read_b128 v[0:3], v252 offset:32768
	ds_read_b128 v[4:7], v253 offset:32768
	ds_read_b128 v[8:11], v252 offset:34816
	ds_read_b128 v[12:15], v253 offset:34816
	ds_read_b128 v[16:19], v252 offset:49152
	ds_read_b128 v[20:23], v253 offset:49152
	ds_read_b128 v[24:27], v252 offset:51200
	ds_read_b128 v[28:31], v253 offset:51200
	s_mov_b32 m0, s61
	ds_read_b128 v[216:219], v207 offset:32768
	ds_read_b128 v[224:227], v207 offset:34816
	ds_read_b128 v[220:223], v208 offset:32768
	ds_read_b128 v[228:231], v208 offset:34816
	ds_read_b128 v[232:235], v207 offset:36864
	ds_read_b128 v[240:243], v207 offset:38912
	ds_read_b128 v[236:239], v208 offset:36864
	ds_read_b128 v[244:247], v208 offset:38912
	global_load_lds_dwordx4 v184, s[36:37]
	s_mov_b32 m0, s62
	s_nop 0
	global_load_lds_dwordx4 v182, s[36:37]
	s_waitcnt vmcnt(8)
	s_waitcnt lgkmcnt(0)
	s_barrier
	s_setprio 1
	s_waitcnt lgkmcnt(0)
	v_mfma_f32_16x16x128_f8f6f4 v[156:159], v[0:7], v[216:223], v[156:159]
	v_mfma_f32_16x16x128_f8f6f4 v[152:155], v[8:15], v[216:223], v[152:155]
	v_mfma_f32_16x16x128_f8f6f4 v[136:139], v[8:15], v[224:231], v[136:139]
	v_mfma_f32_16x16x128_f8f6f4 v[140:143], v[0:7], v[224:231], v[140:143]
	v_mfma_f32_16x16x128_f8f6f4 v[124:127], v[0:7], v[232:239], v[124:127]
	v_mfma_f32_16x16x128_f8f6f4 v[120:123], v[8:15], v[232:239], v[120:123]
	v_mfma_f32_16x16x128_f8f6f4 v[104:107], v[8:15], v[240:247], v[104:107]
	v_mfma_f32_16x16x128_f8f6f4 v[108:111], v[0:7], v[240:247], v[108:111]
	v_mfma_f32_16x16x128_f8f6f4 v[148:151], v[16:23], v[216:223], v[148:151]
	v_mfma_f32_16x16x128_f8f6f4 v[144:147], v[24:31], v[216:223], v[144:147]
	v_mfma_f32_16x16x128_f8f6f4 v[128:131], v[24:31], v[224:231], v[128:131]
	v_mfma_f32_16x16x128_f8f6f4 v[132:135], v[16:23], v[224:231], v[132:135]
	v_mfma_f32_16x16x128_f8f6f4 v[116:119], v[16:23], v[232:239], v[116:119]
	v_mfma_f32_16x16x128_f8f6f4 v[112:115], v[24:31], v[232:239], v[112:115]
	v_mfma_f32_16x16x128_f8f6f4 v[96:99], v[24:31], v[240:247], v[96:99]
	v_mfma_f32_16x16x128_f8f6f4 v[100:103], v[16:23], v[240:247], v[100:103]
	s_setprio 0
	s_barrier
	s_add_i32 s99, s42, 0x17f80
	s_mov_b32 m0, s99
	ds_read_b128 v[216:219], v207 offset:49152
	ds_read_b128 v[224:227], v207 offset:51200
	ds_read_b128 v[220:223], v208 offset:49152
	ds_read_b128 v[228:231], v208 offset:51200
	ds_read_b128 v[232:235], v207 offset:53248
	ds_read_b128 v[240:243], v207 offset:55296
	ds_read_b128 v[236:239], v208 offset:53248
	ds_read_b128 v[244:247], v208 offset:55296
	global_load_lds_dwordx4 v160, s[38:39] offset:128
	s_add_i32 m0, s99, 0x2000
	s_add_i32 s99, s42, 0x1bf80
	global_load_lds_dwordx4 v162, s[38:39] offset:128
	s_mov_b32 m0, s99
	s_nop 0
	global_load_lds_dwordx4 v160, s[40:41] offset:128
	s_add_i32 m0, s99, 0x2000
	s_nop 0
	global_load_lds_dwordx4 v162, s[40:41] offset:128
	s_waitcnt vmcnt(6)
	s_waitcnt lgkmcnt(0)
	s_barrier
	s_setprio 1
	s_waitcnt lgkmcnt(0)
	v_mfma_f32_16x16x128_f8f6f4 v[92:95], v[0:7], v[216:223], v[92:95]
	v_mfma_f32_16x16x128_f8f6f4 v[88:91], v[8:15], v[216:223], v[88:91]
	v_mfma_f32_16x16x128_f8f6f4 v[72:75], v[8:15], v[224:231], v[72:75]
	v_mfma_f32_16x16x128_f8f6f4 v[76:79], v[0:7], v[224:231], v[76:79]
	s_add_i32 m0, s63, 0xffffff80
	v_mfma_f32_16x16x128_f8f6f4 v[60:63], v[0:7], v[232:239], v[60:63]
	global_load_lds_dwordx4 v164, s[36:37] offset:128
	v_mfma_f32_16x16x128_f8f6f4 v[56:59], v[8:15], v[232:239], v[56:59]
	v_mfma_f32_16x16x128_f8f6f4 v[40:43], v[8:15], v[240:247], v[40:43]
	v_mfma_f32_16x16x128_f8f6f4 v[44:47], v[0:7], v[240:247], v[44:47]
	v_mfma_f32_16x16x128_f8f6f4 v[84:87], v[16:23], v[216:223], v[84:87]
	s_add_i32 m0, s64, 0xffffff80
	v_mfma_f32_16x16x128_f8f6f4 v[80:83], v[24:31], v[216:223], v[80:83]
	global_load_lds_dwordx4 v172, s[36:37] offset:128
	v_mfma_f32_16x16x128_f8f6f4 v[64:67], v[24:31], v[224:231], v[64:67]
	v_mfma_f32_16x16x128_f8f6f4 v[68:71], v[16:23], v[224:231], v[68:71]
	v_mfma_f32_16x16x128_f8f6f4 v[52:55], v[16:23], v[232:239], v[52:55]
	v_mfma_f32_16x16x128_f8f6f4 v[48:51], v[24:31], v[232:239], v[48:51]
	v_mfma_f32_16x16x128_f8f6f4 v[32:35], v[24:31], v[240:247], v[32:35]
	v_mfma_f32_16x16x128_f8f6f4 v[36:39], v[16:23], v[240:247], v[36:39]
	s_setprio 0
	s_barrier
	s_add_i32 s85, s85, 2
	s_add_u32 s34, s34, 0x100
	s_addc_u32 s35, s35, 0
	s_cmp_gt_u32 s85, 5
	s_cbranch_scc1 .LBB0_675

.Lc0_P7_0:
	v_mfma_f32_16x16x128_f8f6f4 v[156:159], v[24:31], v[186:193], 0
	v_mfma_f32_16x16x128_f8f6f4 v[152:155], v[16:23], v[186:193], 0
	v_mfma_f32_16x16x128_f8f6f4 v[136:139], v[16:23], v[216:223], 0
	v_mfma_f32_16x16x128_f8f6f4 v[140:143], v[24:31], v[216:223], 0
	v_mfma_f32_16x16x128_f8f6f4 v[124:127], v[24:31], v[224:231], 0
	v_mfma_f32_16x16x128_f8f6f4 v[120:123], v[16:23], v[224:231], 0
	v_mfma_f32_16x16x128_f8f6f4 v[104:107], v[16:23], v[232:239], 0
	v_mfma_f32_16x16x128_f8f6f4 v[108:111], v[24:31], v[232:239], 0
	v_mfma_f32_16x16x128_f8f6f4 v[148:151], v[8:15], v[186:193], 0
	v_mfma_f32_16x16x128_f8f6f4 v[144:147], v[0:7], v[186:193], 0
	v_mfma_f32_16x16x128_f8f6f4 v[128:131], v[0:7], v[216:223], 0
	v_mfma_f32_16x16x128_f8f6f4 v[132:135], v[8:15], v[216:223], 0
	v_mfma_f32_16x16x128_f8f6f4 v[116:119], v[8:15], v[224:231], 0
	v_mfma_f32_16x16x128_f8f6f4 v[112:115], v[0:7], v[224:231], 0
	v_mfma_f32_16x16x128_f8f6f4 v[96:99], v[0:7], v[232:239], 0
	v_mfma_f32_16x16x128_f8f6f4 v[100:103], v[8:15], v[232:239], 0
	s_branch .Lc0b_P7_0
.Lc0_P7_1:
	v_mfma_f32_16x16x128_f8f6f4 v[92:95], v[24:31], v[216:223], 0
	v_mfma_f32_16x16x128_f8f6f4 v[88:91], v[16:23], v[216:223], 0
	v_mfma_f32_16x16x128_f8f6f4 v[72:75], v[16:23], v[224:231], 0
	v_mfma_f32_16x16x128_f8f6f4 v[76:79], v[24:31], v[224:231], 0
	s_mov_b32 m0, s59
	v_mfma_f32_16x16x128_f8f6f4 v[60:63], v[24:31], v[232:239], 0
	global_load_lds_dwordx4 v164, s[36:37]
	v_mfma_f32_16x16x128_f8f6f4 v[56:59], v[16:23], v[232:239], 0
	v_mfma_f32_16x16x128_f8f6f4 v[40:43], v[16:23], v[240:247], 0
	v_mfma_f32_16x16x128_f8f6f4 v[44:47], v[24:31], v[240:247], 0
	v_mfma_f32_16x16x128_f8f6f4 v[84:87], v[8:15], v[216:223], 0
	s_mov_b32 m0, s60
	v_mfma_f32_16x16x128_f8f6f4 v[80:83], v[0:7], v[216:223], 0
	global_load_lds_dwordx4 v172, s[36:37]
	v_mfma_f32_16x16x128_f8f6f4 v[64:67], v[0:7], v[224:231], 0
	v_mfma_f32_16x16x128_f8f6f4 v[68:71], v[8:15], v[224:231], 0
	v_mfma_f32_16x16x128_f8f6f4 v[52:55], v[8:15], v[232:239], 0
	v_mfma_f32_16x16x128_f8f6f4 v[48:51], v[0:7], v[232:239], 0
	v_mfma_f32_16x16x128_f8f6f4 v[32:35], v[0:7], v[240:247], 0
	v_mfma_f32_16x16x128_f8f6f4 v[36:39], v[8:15], v[240:247], 0
	s_branch .Lc0b_P7_1

.LBB0_677:
	v_mbcnt_lo_u32_b32 v250, -1, 0
	v_mbcnt_hi_u32_b32 v250, -1, v250
	v_bfe_u32 v250, v250, 4, 1
	v_mul_u32_u24_e32 v250, 0x78, v250
	v_mov_b32_e32 v251, 0
	s_lshl_b32 s27, s81, 10
	s_and_b32 s27, s27, 0x400
	v_mov_b32_e32 v17, v171
	v_mov_b32_e32 v16, v204
	s_add_i32 s27, s67, s27
	s_and_b64 vcc, exec, s[2:3]
	v_lshl_add_u32 v0, v16, 5, s27
	s_lshl_b32 s27, s80, 8
	s_or_b32 s27, s27, s66
	ds_read_b128 v[12:15], v0
	ds_read_b128 v[8:11], v0 offset:16
	ds_read_b128 v[4:7], v0 offset:512
	ds_read_b128 v[0:3], v0 offset:528
	v_lshl_add_u32 v16, v16, 3, s27
	s_lshl_b32 s27, s79, 8
	s_add_i32 s27, s27, s68
	v_add_u32_e32 v18, s27, v17
	s_waitcnt lgkmcnt(0)
	v_pk_fma_f32 v[22:23], v[158:159], s[22:23], v[14:15] op_sel_hi:[1,0,1]
	v_pk_fma_f32 v[24:25], v[156:157], s[22:23], v[12:13] op_sel_hi:[1,0,1]
	v_ashrrev_i32_e32 v19, 31, v18
	v_pk_mul_f32 v[22:23], v[22:23], s[24:25] op_sel_hi:[1,0]
	v_pk_mul_f32 v[24:25], v[24:25], s[24:25] op_sel_hi:[1,0]
	v_pk_fma_f32 v[28:29], v[152:153], s[22:23], v[8:9] op_sel_hi:[1,0,1]
	v_lshlrev_b64 v[20:21], 10, v[18:19]
	v_pk_mul_f32 v[28:29], v[28:29], s[24:25] op_sel_hi:[1,0]
	v_med3_f32 v19, v24, s75, v210
	v_med3_f32 v24, v25, s75, v210
	v_med3_f32 v25, v22, s75, v210
	v_med3_f32 v30, v23, s75, v210
	v_cvt_pk_fp8_f32 v22, v19, v24
	v_med3_f32 v19, v28, s75, v210
	v_med3_f32 v24, v29, s75, v210
	v_cvt_pk_fp8_f32 v23, v19, v24
	v_pk_fma_f32 v[26:27], v[154:155], s[22:23], v[10:11] op_sel_hi:[1,0,1]
	v_cvt_pk_fp8_f32 v22, v25, v30 op_sel:[0,0,1]
	v_pk_mul_f32 v[26:27], v[26:27], s[24:25] op_sel_hi:[1,0]
	v_pk_fma_f32 v[30:31], v[144:145], s[22:23], v[0:1] op_sel_hi:[1,0,1]
	v_med3_f32 v19, v26, s75, v210
	v_med3_f32 v24, v27, s75, v210
	v_cvt_pk_fp8_f32 v23, v19, v24 op_sel:[0,0,1]
	v_pk_fma_f32 v[24:25], v[150:151], s[22:23], v[6:7] op_sel_hi:[1,0,1]
	v_pk_fma_f32 v[26:27], v[148:149], s[22:23], v[4:5] op_sel_hi:[1,0,1]
	v_pk_mul_f32 v[24:25], v[24:25], s[24:25] op_sel_hi:[1,0]
	v_pk_mul_f32 v[26:27], v[26:27], s[24:25] op_sel_hi:[1,0]
	v_pk_mul_f32 v[30:31], v[30:31], s[24:25] op_sel_hi:[1,0]
	v_med3_f32 v19, v26, s75, v210
	v_med3_f32 v26, v27, s75, v210
	v_med3_f32 v27, v24, s75, v210
	v_med3_f32 v144, v25, s75, v210
	v_cvt_pk_fp8_f32 v24, v19, v26
	v_med3_f32 v19, v30, s75, v210
	v_med3_f32 v26, v31, s75, v210
	v_cvt_pk_fp8_f32 v25, v19, v26
	v_pk_fma_f32 v[28:29], v[146:147], s[22:23], v[2:3] op_sel_hi:[1,0,1]
	v_cvt_pk_fp8_f32 v24, v27, v144 op_sel:[0,0,1]
	v_pk_mul_f32 v[28:29], v[28:29], s[24:25] op_sel_hi:[1,0]
	v_ashrrev_i32_e32 v17, 31, v16
	v_med3_f32 v19, v28, s75, v210
	v_med3_f32 v26, v29, s75, v210
	v_cvt_pk_fp8_f32 v25, v19, v26 op_sel:[0,0,1]
	v_lshl_add_u64 v[20:21], s[12:13], 0, v[20:21]
	v_lshl_add_u64 v[20:21], v[20:21], 0, v[16:17]
	s_nop 1
	v_permlane16_swap_b32_e32 v22, v24
	v_permlane16_swap_b32_e32 v23, v25
	v_lshl_add_u64 v[248:249], v[20:21], 0, v[250:251]
	global_store_dwordx4 v[248:249], v[22:25], off
	s_nop 1
	v_pk_fma_f32 v[22:23], v[142:143], s[22:23], v[14:15] op_sel_hi:[1,0,1]
	v_pk_fma_f32 v[24:25], v[140:141], s[22:23], v[12:13] op_sel_hi:[1,0,1]
	v_pk_mul_f32 v[22:23], v[22:23], s[24:25] op_sel_hi:[1,0]
	v_pk_mul_f32 v[24:25], v[24:25], s[24:25] op_sel_hi:[1,0]
	v_pk_fma_f32 v[28:29], v[136:137], s[22:23], v[8:9] op_sel_hi:[1,0,1]
	v_med3_f32 v19, v24, s75, v210
	v_pk_mul_f32 v[28:29], v[28:29], s[24:25] op_sel_hi:[1,0]
	v_med3_f32 v24, v25, s75, v210
	v_med3_f32 v25, v22, s75, v210
	v_med3_f32 v30, v23, s75, v210
	v_cvt_pk_fp8_f32 v22, v19, v24
	v_med3_f32 v19, v28, s75, v210
	v_med3_f32 v24, v29, s75, v210
	v_cvt_pk_fp8_f32 v23, v19, v24
	v_pk_fma_f32 v[26:27], v[138:139], s[22:23], v[10:11] op_sel_hi:[1,0,1]
	v_cvt_pk_fp8_f32 v22, v25, v30 op_sel:[0,0,1]
	v_pk_mul_f32 v[26:27], v[26:27], s[24:25] op_sel_hi:[1,0]
	v_pk_fma_f32 v[30:31], v[128:129], s[22:23], v[0:1] op_sel_hi:[1,0,1]
	v_med3_f32 v19, v26, s75, v210
	v_med3_f32 v24, v27, s75, v210
	v_cvt_pk_fp8_f32 v23, v19, v24 op_sel:[0,0,1]
	v_pk_fma_f32 v[24:25], v[134:135], s[22:23], v[6:7] op_sel_hi:[1,0,1]
	v_pk_fma_f32 v[26:27], v[132:133], s[22:23], v[4:5] op_sel_hi:[1,0,1]
	v_pk_mul_f32 v[24:25], v[24:25], s[24:25] op_sel_hi:[1,0]
	v_pk_mul_f32 v[26:27], v[26:27], s[24:25] op_sel_hi:[1,0]
	v_pk_mul_f32 v[30:31], v[30:31], s[24:25] op_sel_hi:[1,0]
	v_med3_f32 v19, v26, s75, v210
	v_med3_f32 v26, v27, s75, v210
	v_med3_f32 v27, v24, s75, v210
	v_med3_f32 v128, v25, s75, v210
	v_cvt_pk_fp8_f32 v24, v19, v26
	v_med3_f32 v19, v30, s75, v210
	v_med3_f32 v26, v31, s75, v210
	v_cvt_pk_fp8_f32 v25, v19, v26
	v_pk_fma_f32 v[28:29], v[130:131], s[22:23], v[2:3] op_sel_hi:[1,0,1]
	v_add_u32_e32 v20, 16, v18
	v_pk_mul_f32 v[28:29], v[28:29], s[24:25] op_sel_hi:[1,0]
	v_ashrrev_i32_e32 v21, 31, v20
	v_med3_f32 v19, v28, s75, v210
	v_med3_f32 v26, v29, s75, v210
	v_lshlrev_b64 v[20:21], 10, v[20:21]
	v_cvt_pk_fp8_f32 v24, v27, v128 op_sel:[0,0,1]
	v_cvt_pk_fp8_f32 v25, v19, v26 op_sel:[0,0,1]
	v_lshl_add_u64 v[20:21], s[12:13], 0, v[20:21]
	v_lshl_add_u64 v[20:21], v[20:21], 0, v[16:17]
	s_nop 1
	v_permlane16_swap_b32_e32 v22, v24
	v_permlane16_swap_b32_e32 v23, v25
	v_lshl_add_u64 v[248:249], v[20:21], 0, v[250:251]
	global_store_dwordx4 v[248:249], v[22:25], off
	s_nop 1
	v_pk_fma_f32 v[22:23], v[126:127], s[22:23], v[14:15] op_sel_hi:[1,0,1]
	v_pk_fma_f32 v[24:25], v[124:125], s[22:23], v[12:13] op_sel_hi:[1,0,1]
	v_pk_mul_f32 v[22:23], v[22:23], s[24:25] op_sel_hi:[1,0]
	v_pk_mul_f32 v[24:25], v[24:25], s[24:25] op_sel_hi:[1,0]
	v_pk_fma_f32 v[28:29], v[120:121], s[22:23], v[8:9] op_sel_hi:[1,0,1]
	v_med3_f32 v19, v24, s75, v210
	v_pk_mul_f32 v[28:29], v[28:29], s[24:25] op_sel_hi:[1,0]
	v_med3_f32 v24, v25, s75, v210
	v_med3_f32 v25, v22, s75, v210
	v_med3_f32 v30, v23, s75, v210
	v_cvt_pk_fp8_f32 v22, v19, v24
	v_med3_f32 v19, v28, s75, v210
	v_med3_f32 v24, v29, s75, v210
	v_cvt_pk_fp8_f32 v23, v19, v24
	v_pk_fma_f32 v[26:27], v[122:123], s[22:23], v[10:11] op_sel_hi:[1,0,1]
	v_cvt_pk_fp8_f32 v22, v25, v30 op_sel:[0,0,1]
	v_pk_mul_f32 v[26:27], v[26:27], s[24:25] op_sel_hi:[1,0]
	v_pk_fma_f32 v[30:31], v[112:113], s[22:23], v[0:1] op_sel_hi:[1,0,1]
	v_med3_f32 v19, v26, s75, v210
	v_med3_f32 v24, v27, s75, v210
	v_cvt_pk_fp8_f32 v23, v19, v24 op_sel:[0,0,1]
	v_pk_fma_f32 v[24:25], v[118:119], s[22:23], v[6:7] op_sel_hi:[1,0,1]
	v_pk_fma_f32 v[26:27], v[116:117], s[22:23], v[4:5] op_sel_hi:[1,0,1]
	v_pk_mul_f32 v[24:25], v[24:25], s[24:25] op_sel_hi:[1,0]
	v_pk_mul_f32 v[26:27], v[26:27], s[24:25] op_sel_hi:[1,0]
	v_pk_mul_f32 v[30:31], v[30:31], s[24:25] op_sel_hi:[1,0]
	v_med3_f32 v19, v26, s75, v210
	v_med3_f32 v26, v27, s75, v210
	v_med3_f32 v27, v24, s75, v210
	v_med3_f32 v112, v25, s75, v210
	v_cvt_pk_fp8_f32 v24, v19, v26
	v_med3_f32 v19, v30, s75, v210
	v_med3_f32 v26, v31, s75, v210
	v_cvt_pk_fp8_f32 v25, v19, v26
	v_pk_fma_f32 v[28:29], v[114:115], s[22:23], v[2:3] op_sel_hi:[1,0,1]
	v_add_u32_e32 v20, 32, v18
	v_pk_mul_f32 v[28:29], v[28:29], s[24:25] op_sel_hi:[1,0]
	v_ashrrev_i32_e32 v21, 31, v20
	v_med3_f32 v19, v28, s75, v210
	v_med3_f32 v26, v29, s75, v210
	v_lshlrev_b64 v[20:21], 10, v[20:21]
	v_cvt_pk_fp8_f32 v24, v27, v112 op_sel:[0,0,1]
	v_cvt_pk_fp8_f32 v25, v19, v26 op_sel:[0,0,1]
	v_lshl_add_u64 v[20:21], s[12:13], 0, v[20:21]
	v_lshl_add_u64 v[20:21], v[20:21], 0, v[16:17]
	s_nop 1
	v_permlane16_swap_b32_e32 v22, v24
	v_permlane16_swap_b32_e32 v23, v25
	v_lshl_add_u64 v[248:249], v[20:21], 0, v[250:251]
	global_store_dwordx4 v[248:249], v[22:25], off
	s_nop 1
	v_pk_fma_f32 v[22:23], v[110:111], s[22:23], v[14:15] op_sel_hi:[1,0,1]
	v_pk_fma_f32 v[24:25], v[108:109], s[22:23], v[12:13] op_sel_hi:[1,0,1]
	v_pk_mul_f32 v[22:23], v[22:23], s[24:25] op_sel_hi:[1,0]
	v_pk_mul_f32 v[24:25], v[24:25], s[24:25] op_sel_hi:[1,0]
	v_pk_fma_f32 v[28:29], v[104:105], s[22:23], v[8:9] op_sel_hi:[1,0,1]
	v_med3_f32 v19, v24, s75, v210
	v_pk_mul_f32 v[28:29], v[28:29], s[24:25] op_sel_hi:[1,0]
	v_med3_f32 v24, v25, s75, v210
	v_med3_f32 v25, v22, s75, v210
	v_med3_f32 v30, v23, s75, v210
	v_cvt_pk_fp8_f32 v22, v19, v24
	v_med3_f32 v19, v28, s75, v210
	v_med3_f32 v24, v29, s75, v210
	v_cvt_pk_fp8_f32 v23, v19, v24
	v_pk_fma_f32 v[26:27], v[106:107], s[22:23], v[10:11] op_sel_hi:[1,0,1]
	v_cvt_pk_fp8_f32 v22, v25, v30 op_sel:[0,0,1]
	v_pk_mul_f32 v[26:27], v[26:27], s[24:25] op_sel_hi:[1,0]
	v_pk_fma_f32 v[30:31], v[96:97], s[22:23], v[0:1] op_sel_hi:[1,0,1]
	v_med3_f32 v19, v26, s75, v210
	v_med3_f32 v24, v27, s75, v210
	v_cvt_pk_fp8_f32 v23, v19, v24 op_sel:[0,0,1]
	v_pk_fma_f32 v[24:25], v[102:103], s[22:23], v[6:7] op_sel_hi:[1,0,1]
	v_pk_fma_f32 v[26:27], v[100:101], s[22:23], v[4:5] op_sel_hi:[1,0,1]
	v_pk_mul_f32 v[24:25], v[24:25], s[24:25] op_sel_hi:[1,0]
	v_pk_mul_f32 v[26:27], v[26:27], s[24:25] op_sel_hi:[1,0]
	v_pk_mul_f32 v[30:31], v[30:31], s[24:25] op_sel_hi:[1,0]
	v_med3_f32 v19, v26, s75, v210
	v_med3_f32 v26, v27, s75, v210
	v_med3_f32 v27, v24, s75, v210
	v_med3_f32 v96, v25, s75, v210
	v_cvt_pk_fp8_f32 v24, v19, v26
	v_med3_f32 v19, v30, s75, v210
	v_med3_f32 v26, v31, s75, v210
	v_cvt_pk_fp8_f32 v25, v19, v26
	v_pk_fma_f32 v[28:29], v[98:99], s[22:23], v[2:3] op_sel_hi:[1,0,1]
	v_add_u32_e32 v20, 48, v18
	v_pk_mul_f32 v[28:29], v[28:29], s[24:25] op_sel_hi:[1,0]
	v_ashrrev_i32_e32 v21, 31, v20
	v_med3_f32 v19, v28, s75, v210
	v_med3_f32 v26, v29, s75, v210
	v_lshlrev_b64 v[20:21], 10, v[20:21]
	v_cvt_pk_fp8_f32 v24, v27, v96 op_sel:[0,0,1]
	v_cvt_pk_fp8_f32 v25, v19, v26 op_sel:[0,0,1]
	v_lshl_add_u64 v[20:21], s[12:13], 0, v[20:21]
	v_lshl_add_u64 v[20:21], v[20:21], 0, v[16:17]
	s_nop 1
	v_permlane16_swap_b32_e32 v22, v24
	v_permlane16_swap_b32_e32 v23, v25
	v_lshl_add_u64 v[248:249], v[20:21], 0, v[250:251]
	global_store_dwordx4 v[248:249], v[22:25], off
	s_nop 1
	v_pk_fma_f32 v[22:23], v[94:95], s[22:23], v[14:15] op_sel_hi:[1,0,1]
	v_pk_fma_f32 v[24:25], v[92:93], s[22:23], v[12:13] op_sel_hi:[1,0,1]
	v_pk_mul_f32 v[22:23], v[22:23], s[24:25] op_sel_hi:[1,0]
	v_pk_mul_f32 v[24:25], v[24:25], s[24:25] op_sel_hi:[1,0]
	v_pk_fma_f32 v[28:29], v[88:89], s[22:23], v[8:9] op_sel_hi:[1,0,1]
	v_med3_f32 v19, v24, s75, v210
	v_pk_mul_f32 v[28:29], v[28:29], s[24:25] op_sel_hi:[1,0]
	v_med3_f32 v24, v25, s75, v210
	v_med3_f32 v25, v22, s75, v210
	v_med3_f32 v30, v23, s75, v210
	v_cvt_pk_fp8_f32 v22, v19, v24
	v_med3_f32 v19, v28, s75, v210
	v_med3_f32 v24, v29, s75, v210
	v_cvt_pk_fp8_f32 v23, v19, v24
	v_pk_fma_f32 v[26:27], v[90:91], s[22:23], v[10:11] op_sel_hi:[1,0,1]
	v_cvt_pk_fp8_f32 v22, v25, v30 op_sel:[0,0,1]
	v_pk_mul_f32 v[26:27], v[26:27], s[24:25] op_sel_hi:[1,0]
	v_pk_fma_f32 v[30:31], v[80:81], s[22:23], v[0:1] op_sel_hi:[1,0,1]
	v_med3_f32 v19, v26, s75, v210
	v_med3_f32 v24, v27, s75, v210
	v_cvt_pk_fp8_f32 v23, v19, v24 op_sel:[0,0,1]
	v_pk_fma_f32 v[24:25], v[86:87], s[22:23], v[6:7] op_sel_hi:[1,0,1]
	v_pk_fma_f32 v[26:27], v[84:85], s[22:23], v[4:5] op_sel_hi:[1,0,1]
	v_pk_mul_f32 v[24:25], v[24:25], s[24:25] op_sel_hi:[1,0]
	v_pk_mul_f32 v[26:27], v[26:27], s[24:25] op_sel_hi:[1,0]
	v_pk_mul_f32 v[30:31], v[30:31], s[24:25] op_sel_hi:[1,0]
	v_med3_f32 v19, v26, s75, v210
	v_med3_f32 v26, v27, s75, v210
	v_med3_f32 v27, v24, s75, v210
	v_med3_f32 v80, v25, s75, v210
	v_cvt_pk_fp8_f32 v24, v19, v26
	v_med3_f32 v19, v30, s75, v210
	v_med3_f32 v26, v31, s75, v210
	v_cvt_pk_fp8_f32 v25, v19, v26
	v_pk_fma_f32 v[28:29], v[82:83], s[22:23], v[2:3] op_sel_hi:[1,0,1]
	v_add_u32_e32 v20, 0x80, v18
	v_pk_mul_f32 v[28:29], v[28:29], s[24:25] op_sel_hi:[1,0]
	v_ashrrev_i32_e32 v21, 31, v20
	v_med3_f32 v19, v28, s75, v210
	v_med3_f32 v26, v29, s75, v210
	v_lshlrev_b64 v[20:21], 10, v[20:21]
	v_cvt_pk_fp8_f32 v24, v27, v80 op_sel:[0,0,1]
	v_cvt_pk_fp8_f32 v25, v19, v26 op_sel:[0,0,1]
	v_lshl_add_u64 v[20:21], s[12:13], 0, v[20:21]
	v_lshl_add_u64 v[20:21], v[20:21], 0, v[16:17]
	s_nop 1
	v_permlane16_swap_b32_e32 v22, v24
	v_permlane16_swap_b32_e32 v23, v25
	v_lshl_add_u64 v[248:249], v[20:21], 0, v[250:251]
	global_store_dwordx4 v[248:249], v[22:25], off
	s_nop 1
	v_pk_fma_f32 v[22:23], v[78:79], s[22:23], v[14:15] op_sel_hi:[1,0,1]
	v_pk_fma_f32 v[24:25], v[76:77], s[22:23], v[12:13] op_sel_hi:[1,0,1]
	v_pk_mul_f32 v[22:23], v[22:23], s[24:25] op_sel_hi:[1,0]
	v_pk_mul_f32 v[24:25], v[24:25], s[24:25] op_sel_hi:[1,0]
	v_pk_fma_f32 v[28:29], v[72:73], s[22:23], v[8:9] op_sel_hi:[1,0,1]
	v_med3_f32 v19, v24, s75, v210
	v_pk_mul_f32 v[28:29], v[28:29], s[24:25] op_sel_hi:[1,0]
	v_med3_f32 v24, v25, s75, v210
	v_med3_f32 v25, v22, s75, v210
	v_med3_f32 v30, v23, s75, v210
	v_cvt_pk_fp8_f32 v22, v19, v24
	v_med3_f32 v19, v28, s75, v210
	v_med3_f32 v24, v29, s75, v210
	v_cvt_pk_fp8_f32 v23, v19, v24
	v_pk_fma_f32 v[26:27], v[74:75], s[22:23], v[10:11] op_sel_hi:[1,0,1]
	v_cvt_pk_fp8_f32 v22, v25, v30 op_sel:[0,0,1]
	v_pk_mul_f32 v[26:27], v[26:27], s[24:25] op_sel_hi:[1,0]
	v_pk_fma_f32 v[30:31], v[64:65], s[22:23], v[0:1] op_sel_hi:[1,0,1]
	v_med3_f32 v19, v26, s75, v210
	v_med3_f32 v24, v27, s75, v210
	v_cvt_pk_fp8_f32 v23, v19, v24 op_sel:[0,0,1]
	v_pk_fma_f32 v[24:25], v[70:71], s[22:23], v[6:7] op_sel_hi:[1,0,1]
	v_pk_fma_f32 v[26:27], v[68:69], s[22:23], v[4:5] op_sel_hi:[1,0,1]
	v_pk_mul_f32 v[24:25], v[24:25], s[24:25] op_sel_hi:[1,0]
	v_pk_mul_f32 v[26:27], v[26:27], s[24:25] op_sel_hi:[1,0]
	v_pk_mul_f32 v[30:31], v[30:31], s[24:25] op_sel_hi:[1,0]
	v_med3_f32 v19, v26, s75, v210
	v_med3_f32 v26, v27, s75, v210
	v_med3_f32 v27, v24, s75, v210
	v_med3_f32 v64, v25, s75, v210
	v_cvt_pk_fp8_f32 v24, v19, v26
	v_med3_f32 v19, v30, s75, v210
	v_med3_f32 v26, v31, s75, v210
	v_cvt_pk_fp8_f32 v25, v19, v26
	v_pk_fma_f32 v[28:29], v[66:67], s[22:23], v[2:3] op_sel_hi:[1,0,1]
	v_add_u32_e32 v20, 0x90, v18
	v_pk_mul_f32 v[28:29], v[28:29], s[24:25] op_sel_hi:[1,0]
	v_ashrrev_i32_e32 v21, 31, v20
	v_med3_f32 v19, v28, s75, v210
	v_med3_f32 v26, v29, s75, v210
	v_lshlrev_b64 v[20:21], 10, v[20:21]
	v_cvt_pk_fp8_f32 v24, v27, v64 op_sel:[0,0,1]
	v_cvt_pk_fp8_f32 v25, v19, v26 op_sel:[0,0,1]
	v_lshl_add_u64 v[20:21], s[12:13], 0, v[20:21]
	v_lshl_add_u64 v[20:21], v[20:21], 0, v[16:17]
	s_nop 1
	v_permlane16_swap_b32_e32 v22, v24
	v_permlane16_swap_b32_e32 v23, v25
	v_lshl_add_u64 v[248:249], v[20:21], 0, v[250:251]
	global_store_dwordx4 v[248:249], v[22:25], off
	s_nop 1
	v_pk_fma_f32 v[22:23], v[62:63], s[22:23], v[14:15] op_sel_hi:[1,0,1]
	v_pk_fma_f32 v[24:25], v[60:61], s[22:23], v[12:13] op_sel_hi:[1,0,1]
	v_pk_mul_f32 v[22:23], v[22:23], s[24:25] op_sel_hi:[1,0]
	v_pk_mul_f32 v[24:25], v[24:25], s[24:25] op_sel_hi:[1,0]
	v_pk_fma_f32 v[28:29], v[56:57], s[22:23], v[8:9] op_sel_hi:[1,0,1]
	v_med3_f32 v19, v24, s75, v210
	v_pk_mul_f32 v[28:29], v[28:29], s[24:25] op_sel_hi:[1,0]
	v_med3_f32 v24, v25, s75, v210
	v_med3_f32 v25, v22, s75, v210
	v_med3_f32 v30, v23, s75, v210
	v_cvt_pk_fp8_f32 v22, v19, v24
	v_med3_f32 v19, v28, s75, v210
	v_med3_f32 v24, v29, s75, v210
	v_cvt_pk_fp8_f32 v23, v19, v24
	v_pk_fma_f32 v[26:27], v[58:59], s[22:23], v[10:11] op_sel_hi:[1,0,1]
	v_cvt_pk_fp8_f32 v22, v25, v30 op_sel:[0,0,1]
	v_pk_mul_f32 v[26:27], v[26:27], s[24:25] op_sel_hi:[1,0]
	v_pk_fma_f32 v[30:31], v[48:49], s[22:23], v[0:1] op_sel_hi:[1,0,1]
	v_med3_f32 v19, v26, s75, v210
	v_med3_f32 v24, v27, s75, v210
	v_cvt_pk_fp8_f32 v23, v19, v24 op_sel:[0,0,1]
	v_pk_fma_f32 v[24:25], v[54:55], s[22:23], v[6:7] op_sel_hi:[1,0,1]
	v_pk_fma_f32 v[26:27], v[52:53], s[22:23], v[4:5] op_sel_hi:[1,0,1]
	v_pk_mul_f32 v[24:25], v[24:25], s[24:25] op_sel_hi:[1,0]
	v_pk_mul_f32 v[26:27], v[26:27], s[24:25] op_sel_hi:[1,0]
	v_pk_mul_f32 v[30:31], v[30:31], s[24:25] op_sel_hi:[1,0]
	v_med3_f32 v19, v26, s75, v210
	v_med3_f32 v26, v27, s75, v210
	v_med3_f32 v27, v24, s75, v210
	v_med3_f32 v48, v25, s75, v210
	v_cvt_pk_fp8_f32 v24, v19, v26
	v_med3_f32 v19, v30, s75, v210
	v_med3_f32 v26, v31, s75, v210
	v_cvt_pk_fp8_f32 v25, v19, v26
	v_pk_fma_f32 v[28:29], v[50:51], s[22:23], v[2:3] op_sel_hi:[1,0,1]
	v_add_u32_e32 v20, 0xa0, v18
	v_pk_mul_f32 v[28:29], v[28:29], s[24:25] op_sel_hi:[1,0]
	v_ashrrev_i32_e32 v21, 31, v20
	v_med3_f32 v19, v28, s75, v210
	v_med3_f32 v26, v29, s75, v210
	v_lshlrev_b64 v[20:21], 10, v[20:21]
	v_cvt_pk_fp8_f32 v24, v27, v48 op_sel:[0,0,1]
	v_cvt_pk_fp8_f32 v25, v19, v26 op_sel:[0,0,1]
	v_lshl_add_u64 v[20:21], s[12:13], 0, v[20:21]
	v_pk_fma_f32 v[12:13], v[44:45], s[22:23], v[12:13] op_sel_hi:[1,0,1]
	v_lshl_add_u64 v[20:21], v[20:21], 0, v[16:17]
	v_pk_mul_f32 v[12:13], v[12:13], s[24:25] op_sel_hi:[1,0]
	v_pk_fma_f32 v[8:9], v[40:41], s[22:23], v[8:9] op_sel_hi:[1,0,1]
	s_nop 1
	v_permlane16_swap_b32_e32 v22, v24
	v_permlane16_swap_b32_e32 v23, v25
	v_lshl_add_u64 v[248:249], v[20:21], 0, v[250:251]
	global_store_dwordx4 v[248:249], v[22:25], off
	s_nop 1
	v_pk_mul_f32 v[8:9], v[8:9], s[24:25] op_sel_hi:[1,0]
	v_med3_f32 v20, v12, s75, v210
	v_med3_f32 v13, v13, s75, v210
	v_cvt_pk_fp8_f32 v12, v20, v13
	v_med3_f32 v8, v8, s75, v210
	v_med3_f32 v9, v9, s75, v210
	v_cvt_pk_fp8_f32 v13, v8, v9
	v_pk_fma_f32 v[10:11], v[42:43], s[22:23], v[10:11] op_sel_hi:[1,0,1]
	v_pk_fma_f32 v[4:5], v[36:37], s[22:23], v[4:5] op_sel_hi:[1,0,1]
	v_pk_mul_f32 v[10:11], v[10:11], s[24:25] op_sel_hi:[1,0]
	v_pk_mul_f32 v[4:5], v[4:5], s[24:25] op_sel_hi:[1,0]
	v_med3_f32 v8, v10, s75, v210
	v_med3_f32 v9, v11, s75, v210
	v_pk_fma_f32 v[0:1], v[32:33], s[22:23], v[0:1] op_sel_hi:[1,0,1]
	v_cvt_pk_fp8_f32 v13, v8, v9 op_sel:[0,0,1]
	v_pk_mul_f32 v[0:1], v[0:1], s[24:25] op_sel_hi:[1,0]
	v_med3_f32 v8, v4, s75, v210
	v_med3_f32 v5, v5, s75, v210
	v_cvt_pk_fp8_f32 v4, v8, v5
	v_med3_f32 v0, v0, s75, v210
	v_med3_f32 v1, v1, s75, v210
	v_pk_fma_f32 v[14:15], v[46:47], s[22:23], v[14:15] op_sel_hi:[1,0,1]
	v_cvt_pk_fp8_f32 v5, v0, v1
	v_pk_mul_f32 v[14:15], v[14:15], s[24:25] op_sel_hi:[1,0]
	v_pk_fma_f32 v[6:7], v[38:39], s[22:23], v[6:7] op_sel_hi:[1,0,1]
	v_pk_fma_f32 v[2:3], v[34:35], s[22:23], v[2:3] op_sel_hi:[1,0,1]
	v_add_u32_e32 v18, 0xb0, v18
	v_med3_f32 v14, v14, s75, v210
	v_med3_f32 v15, v15, s75, v210
	v_pk_mul_f32 v[6:7], v[6:7], s[24:25] op_sel_hi:[1,0]
	v_pk_mul_f32 v[2:3], v[2:3], s[24:25] op_sel_hi:[1,0]
	v_ashrrev_i32_e32 v19, 31, v18
	v_cvt_pk_fp8_f32 v12, v14, v15 op_sel:[0,0,1]
	v_med3_f32 v6, v6, s75, v210
	v_med3_f32 v7, v7, s75, v210
	v_med3_f32 v0, v2, s75, v210
	v_med3_f32 v1, v3, s75, v210
	v_lshlrev_b64 v[18:19], 10, v[18:19]
	v_cvt_pk_fp8_f32 v4, v6, v7 op_sel:[0,0,1]
	v_cvt_pk_fp8_f32 v5, v0, v1 op_sel:[0,0,1]
	v_lshl_add_u64 v[0:1], s[12:13], 0, v[18:19]
	v_lshl_add_u64 v[0:1], v[0:1], 0, v[16:17]
	s_mov_b64 s[2:3], -1
	global_store_dwordx2 v[0:1], v[12:13], off
	global_store_dwordx2 v[0:1], v[4:5], off offset:128
	s_cbranch_vccnz .LBB0_664
	s_andn2_b64 vcc, exec, s[10:11]
	s_cbranch_vccnz .LBB0_663
	s_barrier
	s_branch .LBB0_663

.LBB0_816:
	s_add_u32 s56, s26, 0x100
	s_addc_u32 s57, s27, 0
	v_mov_b32_e32 v169, v165
	v_mov_b32_e32 v171, v165
	s_add_u32 s58, s28, 0x100
	v_mov_b32_e32 v175, v165
	v_mov_b32_e32 v177, v165
	v_lshl_add_u64 v[178:179], s[14:15], 0, v[170:171]
	v_lshl_add_u64 v[180:181], s[14:15], 0, v[168:169]
	s_addc_u32 s59, s29, 0
	s_mov_b32 s60, -2
	s_mov_b64 s[26:27], 0
	v_add_u32_e32 v252, 0x10000, v173
	v_add_u32_e32 v253, 0x10000, v206
	s_branch .LBB0_818
.LBB0_817:
	s_add_u32 s28, s10, s26
	s_addc_u32 s29, s11, s27
	s_add_u32 s30, s28, 0x38000100
	s_addc_u32 s31, s29, 0
	ds_read_b128 v[24:27], v252
	ds_read_b128 v[28:31], v253
	s_and_b64 s[28:29], s[34:35], exec
	ds_read_b128 v[16:19], v252 offset:2048
	ds_read_b128 v[20:23], v253 offset:2048
	s_cselect_b32 s29, s1, s31
	s_cselect_b32 s28, s0, s30
	s_add_u32 s61, s56, s26
	ds_read_b128 v[8:11], v252 offset:16384
	ds_read_b128 v[12:15], v253 offset:16384
	s_addc_u32 s62, s57, s27
	ds_read_b128 v[0:3], v252 offset:18432
	ds_read_b128 v[4:7], v253 offset:18432
	s_and_b64 s[30:31], s[34:35], exec
	s_cselect_b32 s31, s23, s62
	s_cselect_b32 s30, s22, s61
	s_add_u32 s61, s58, s26
	s_addc_u32 s62, s59, s27
	s_and_b64 s[34:35], s[34:35], exec
	s_cselect_b32 s35, s25, s62
	s_cselect_b32 s34, s24, s61
	s_add_u32 s100, s14, s26
	s_addc_u32 s101, s15, s27
	s_add_i32 m0, s37, 0xc000
	ds_read_b128 v[186:189], v207
	ds_read_b128 v[216:219], v207 offset:2048
	ds_read_b128 v[190:193], v208
	ds_read_b128 v[220:223], v208 offset:2048
	ds_read_b128 v[224:227], v207 offset:4096
	ds_read_b128 v[232:235], v207 offset:6144
	ds_read_b128 v[228:231], v208 offset:4096
	ds_read_b128 v[236:239], v208 offset:6144
	global_load_lds_dwordx4 v168, s[100:101]
	s_add_i32 m0, s37, 0xe000
	s_nop 0
	global_load_lds_dwordx4 v170, s[100:101]
	s_waitcnt vmcnt(8)
	s_waitcnt lgkmcnt(0)
	s_barrier
	s_setprio 1
	s_waitcnt lgkmcnt(0)
	s_cmp_eq_u32 s26, 0
	s_cbranch_scc1 .Lc0_P9a_0
	v_mfma_f32_16x16x128_f8f6f4 v[156:159], v[24:31], v[186:193], v[156:159]
	v_mfma_f32_16x16x128_f8f6f4 v[152:155], v[16:23], v[186:193], v[152:155]
	v_mfma_f32_16x16x128_f8f6f4 v[136:139], v[16:23], v[216:223], v[136:139]
	v_mfma_f32_16x16x128_f8f6f4 v[140:143], v[24:31], v[216:223], v[140:143]
	v_mfma_f32_16x16x128_f8f6f4 v[124:127], v[24:31], v[224:231], v[124:127]
	v_mfma_f32_16x16x128_f8f6f4 v[120:123], v[16:23], v[224:231], v[120:123]
	v_mfma_f32_16x16x128_f8f6f4 v[104:107], v[16:23], v[232:239], v[104:107]
	v_mfma_f32_16x16x128_f8f6f4 v[108:111], v[24:31], v[232:239], v[108:111]
	v_mfma_f32_16x16x128_f8f6f4 v[148:151], v[8:15], v[186:193], v[148:151]
	v_mfma_f32_16x16x128_f8f6f4 v[144:147], v[0:7], v[186:193], v[144:147]
	v_mfma_f32_16x16x128_f8f6f4 v[128:131], v[0:7], v[216:223], v[128:131]
	v_mfma_f32_16x16x128_f8f6f4 v[132:135], v[8:15], v[216:223], v[132:135]
	v_mfma_f32_16x16x128_f8f6f4 v[116:119], v[8:15], v[224:231], v[116:119]
	v_mfma_f32_16x16x128_f8f6f4 v[112:115], v[0:7], v[224:231], v[112:115]
	v_mfma_f32_16x16x128_f8f6f4 v[96:99], v[0:7], v[232:239], v[96:99]
	v_mfma_f32_16x16x128_f8f6f4 v[100:103], v[8:15], v[232:239], v[100:103]
.Lc0b_P9a_0:
	s_setprio 0
	s_barrier
	s_add_i32 s61, s44, s36
	s_mov_b32 m0, s61
	ds_read_b128 v[216:219], v207 offset:16384
	ds_read_b128 v[224:227], v207 offset:18432
	ds_read_b128 v[220:223], v208 offset:16384
	ds_read_b128 v[228:231], v208 offset:18432
	ds_read_b128 v[232:235], v207 offset:20480
	ds_read_b128 v[240:243], v207 offset:22528
	ds_read_b128 v[236:239], v208 offset:20480
	ds_read_b128 v[244:247], v208 offset:22528
	global_load_lds_dwordx4 v160, s[30:31]
	s_add_i32 m0, s61, 0x2000
	s_add_i32 s98, s46, s36
	global_load_lds_dwordx4 v162, s[30:31]
	s_mov_b32 m0, s98
	s_nop 0
	global_load_lds_dwordx4 v160, s[34:35]
	s_add_i32 m0, s98, 0x2000
	v_mov_b32_e32 v167, v165
	global_load_lds_dwordx4 v162, s[34:35]
	s_waitcnt vmcnt(6)
	s_waitcnt lgkmcnt(0)
	s_barrier
	s_setprio 1
	s_waitcnt lgkmcnt(0)
	s_cmp_eq_u32 s26, 0
	s_cbranch_scc1 .Lc0_P9a_1
	v_mfma_f32_16x16x128_f8f6f4 v[92:95], v[24:31], v[216:223], v[92:95]
	v_mfma_f32_16x16x128_f8f6f4 v[88:91], v[16:23], v[216:223], v[88:91]
	v_mfma_f32_16x16x128_f8f6f4 v[72:75], v[16:23], v[224:231], v[72:75]
	v_mfma_f32_16x16x128_f8f6f4 v[76:79], v[24:31], v[224:231], v[76:79]
	s_mov_b32 m0, s37
	v_mfma_f32_16x16x128_f8f6f4 v[60:63], v[24:31], v[232:239], v[60:63]
	global_load_lds_dwordx4 v164, s[28:29]
	v_mfma_f32_16x16x128_f8f6f4 v[56:59], v[16:23], v[232:239], v[56:59]
	v_mfma_f32_16x16x128_f8f6f4 v[40:43], v[16:23], v[240:247], v[40:43]
	v_mfma_f32_16x16x128_f8f6f4 v[44:47], v[24:31], v[240:247], v[44:47]
	v_mfma_f32_16x16x128_f8f6f4 v[84:87], v[8:15], v[216:223], v[84:87]
	s_mov_b32 m0, s38
	v_mfma_f32_16x16x128_f8f6f4 v[80:83], v[0:7], v[216:223], v[80:83]
	global_load_lds_dwordx4 v166, s[28:29]
	v_mfma_f32_16x16x128_f8f6f4 v[64:67], v[0:7], v[224:231], v[64:67]
	v_mfma_f32_16x16x128_f8f6f4 v[68:71], v[8:15], v[224:231], v[68:71]
	v_mfma_f32_16x16x128_f8f6f4 v[52:55], v[8:15], v[232:239], v[52:55]
	v_mfma_f32_16x16x128_f8f6f4 v[48:51], v[0:7], v[232:239], v[48:51]
	v_mfma_f32_16x16x128_f8f6f4 v[32:35], v[0:7], v[240:247], v[32:35]
	v_mfma_f32_16x16x128_f8f6f4 v[36:39], v[8:15], v[240:247], v[36:39]
.Lc0b_P9a_1:
	s_setprio 0
	s_barrier
	ds_read_b128 v[0:3], v252 offset:32768
	ds_read_b128 v[4:7], v253 offset:32768
	ds_read_b128 v[8:11], v252 offset:34816
	ds_read_b128 v[12:15], v253 offset:34816
	ds_read_b128 v[16:19], v252 offset:49152
	ds_read_b128 v[20:23], v253 offset:49152
	ds_read_b128 v[24:27], v252 offset:51200
	ds_read_b128 v[28:31], v253 offset:51200
	s_mov_b32 m0, s39
	ds_read_b128 v[216:219], v207 offset:32768
	ds_read_b128 v[224:227], v207 offset:34816
	ds_read_b128 v[220:223], v208 offset:32768
	ds_read_b128 v[228:231], v208 offset:34816
	ds_read_b128 v[232:235], v207 offset:36864
	ds_read_b128 v[240:243], v207 offset:38912
	ds_read_b128 v[236:239], v208 offset:36864
	ds_read_b128 v[244:247], v208 offset:38912
	global_load_lds_dwordx4 v184, s[28:29]
	s_mov_b32 m0, s40
	s_nop 0
	global_load_lds_dwordx4 v182, s[28:29]
	s_waitcnt vmcnt(8)
	s_waitcnt lgkmcnt(0)
	s_barrier
	s_setprio 1
	s_waitcnt lgkmcnt(0)
	v_mfma_f32_16x16x128_f8f6f4 v[156:159], v[0:7], v[216:223], v[156:159]
	v_mfma_f32_16x16x128_f8f6f4 v[152:155], v[8:15], v[216:223], v[152:155]
	v_mfma_f32_16x16x128_f8f6f4 v[136:139], v[8:15], v[224:231], v[136:139]
	v_mfma_f32_16x16x128_f8f6f4 v[140:143], v[0:7], v[224:231], v[140:143]
	v_mfma_f32_16x16x128_f8f6f4 v[124:127], v[0:7], v[232:239], v[124:127]
	v_mfma_f32_16x16x128_f8f6f4 v[120:123], v[8:15], v[232:239], v[120:123]
	v_mfma_f32_16x16x128_f8f6f4 v[104:107], v[8:15], v[240:247], v[104:107]
	v_mfma_f32_16x16x128_f8f6f4 v[108:111], v[0:7], v[240:247], v[108:111]
	v_mfma_f32_16x16x128_f8f6f4 v[148:151], v[16:23], v[216:223], v[148:151]
	v_mfma_f32_16x16x128_f8f6f4 v[144:147], v[24:31], v[216:223], v[144:147]
	v_mfma_f32_16x16x128_f8f6f4 v[128:131], v[24:31], v[224:231], v[128:131]
	v_mfma_f32_16x16x128_f8f6f4 v[132:135], v[16:23], v[224:231], v[132:135]
	v_mfma_f32_16x16x128_f8f6f4 v[116:119], v[16:23], v[232:239], v[116:119]
	v_mfma_f32_16x16x128_f8f6f4 v[112:115], v[24:31], v[232:239], v[112:115]
	v_mfma_f32_16x16x128_f8f6f4 v[96:99], v[24:31], v[240:247], v[96:99]
	v_mfma_f32_16x16x128_f8f6f4 v[100:103], v[16:23], v[240:247], v[100:103]
	s_setprio 0
	s_barrier
	s_add_i32 s99, s36, 0x17f80
	s_mov_b32 m0, s99
	ds_read_b128 v[216:219], v207 offset:49152
	ds_read_b128 v[224:227], v207 offset:51200
	ds_read_b128 v[220:223], v208 offset:49152
	ds_read_b128 v[228:231], v208 offset:51200
	ds_read_b128 v[232:235], v207 offset:53248
	ds_read_b128 v[240:243], v207 offset:55296
	ds_read_b128 v[236:239], v208 offset:53248
	ds_read_b128 v[244:247], v208 offset:55296
	global_load_lds_dwordx4 v160, s[30:31] offset:128
	s_add_i32 m0, s99, 0x2000
	s_add_i32 s99, s36, 0x1bf80
	global_load_lds_dwordx4 v162, s[30:31] offset:128
	s_mov_b32 m0, s99
	s_nop 0
	global_load_lds_dwordx4 v160, s[34:35] offset:128
	s_add_i32 m0, s99, 0x2000
	s_nop 0
	global_load_lds_dwordx4 v162, s[34:35] offset:128
	s_waitcnt vmcnt(6)
	s_waitcnt lgkmcnt(0)
	s_barrier
	s_setprio 1
	s_waitcnt lgkmcnt(0)
	v_mfma_f32_16x16x128_f8f6f4 v[92:95], v[0:7], v[216:223], v[92:95]
	v_mfma_f32_16x16x128_f8f6f4 v[88:91], v[8:15], v[216:223], v[88:91]
	v_mfma_f32_16x16x128_f8f6f4 v[72:75], v[8:15], v[224:231], v[72:75]
	v_mfma_f32_16x16x128_f8f6f4 v[76:79], v[0:7], v[224:231], v[76:79]
	s_add_i32 m0, s41, 0xffffff80
	v_mfma_f32_16x16x128_f8f6f4 v[60:63], v[0:7], v[232:239], v[60:63]
	global_load_lds_dwordx4 v164, s[28:29] offset:128
	v_mfma_f32_16x16x128_f8f6f4 v[56:59], v[8:15], v[232:239], v[56:59]
	v_mfma_f32_16x16x128_f8f6f4 v[40:43], v[8:15], v[240:247], v[40:43]
	v_mfma_f32_16x16x128_f8f6f4 v[44:47], v[0:7], v[240:247], v[44:47]
	v_mfma_f32_16x16x128_f8f6f4 v[84:87], v[16:23], v[216:223], v[84:87]
	s_add_i32 m0, s42, 0xffffff80
	v_mfma_f32_16x16x128_f8f6f4 v[80:83], v[24:31], v[216:223], v[80:83]
	global_load_lds_dwordx4 v166, s[28:29] offset:128
	v_mfma_f32_16x16x128_f8f6f4 v[64:67], v[24:31], v[224:231], v[64:67]
	v_mfma_f32_16x16x128_f8f6f4 v[68:71], v[16:23], v[224:231], v[68:71]
	v_mfma_f32_16x16x128_f8f6f4 v[52:55], v[16:23], v[232:239], v[52:55]
	v_mfma_f32_16x16x128_f8f6f4 v[48:51], v[24:31], v[232:239], v[48:51]
	v_mfma_f32_16x16x128_f8f6f4 v[32:35], v[24:31], v[240:247], v[32:35]
	v_mfma_f32_16x16x128_f8f6f4 v[36:39], v[16:23], v[240:247], v[36:39]
	s_setprio 0
	s_barrier
	s_add_i32 s60, s60, 2
	s_add_u32 s26, s26, 0x100
	s_addc_u32 s27, s27, 0
	s_cmp_gt_u32 s60, 5
	s_cbranch_scc1 .LBB0_820

.Lc0_P9a_1:
	v_mfma_f32_16x16x128_f8f6f4 v[92:95], v[24:31], v[216:223], 0
	v_mfma_f32_16x16x128_f8f6f4 v[88:91], v[16:23], v[216:223], 0
	v_mfma_f32_16x16x128_f8f6f4 v[72:75], v[16:23], v[224:231], 0
	v_mfma_f32_16x16x128_f8f6f4 v[76:79], v[24:31], v[224:231], 0
	s_mov_b32 m0, s37
	v_mfma_f32_16x16x128_f8f6f4 v[60:63], v[24:31], v[232:239], 0
	global_load_lds_dwordx4 v164, s[28:29]
	v_mfma_f32_16x16x128_f8f6f4 v[56:59], v[16:23], v[232:239], 0
	v_mfma_f32_16x16x128_f8f6f4 v[40:43], v[16:23], v[240:247], 0
	v_mfma_f32_16x16x128_f8f6f4 v[44:47], v[24:31], v[240:247], 0
	v_mfma_f32_16x16x128_f8f6f4 v[84:87], v[8:15], v[216:223], 0
	s_mov_b32 m0, s38
	v_mfma_f32_16x16x128_f8f6f4 v[80:83], v[0:7], v[216:223], 0
	global_load_lds_dwordx4 v166, s[28:29]
	v_mfma_f32_16x16x128_f8f6f4 v[64:67], v[0:7], v[224:231], 0
	v_mfma_f32_16x16x128_f8f6f4 v[68:71], v[8:15], v[224:231], 0
	v_mfma_f32_16x16x128_f8f6f4 v[52:55], v[8:15], v[232:239], 0
	v_mfma_f32_16x16x128_f8f6f4 v[48:51], v[0:7], v[232:239], 0
	v_mfma_f32_16x16x128_f8f6f4 v[32:35], v[0:7], v[240:247], 0
	v_mfma_f32_16x16x128_f8f6f4 v[36:39], v[8:15], v[240:247], 0
	s_branch .Lc0b_P9a_1

.LBB0_822:
	v_mbcnt_lo_u32_b32 v250, -1, 0
	v_mbcnt_hi_u32_b32 v250, -1, v250
	v_bfe_u32 v250, v250, 4, 1
	v_mul_u32_u24_e32 v250, 0x78, v250
	v_mov_b32_e32 v251, 0
	s_lshl_b32 s26, s55, 8
	v_mov_b32_e32 v0, v199
	v_mov_b32_e32 v1, v198
	s_add_i32 s26, s26, s43
	v_pk_mul_f32 v[6:7], v[158:159], s[20:21] op_sel_hi:[1,0]
	v_add_u32_e32 v2, s26, v1
	v_ashrrev_i32_e32 v3, 31, v2
	v_pk_mul_f32 v[8:9], v[156:157], s[20:21] op_sel_hi:[1,0]
	v_lshlrev_b64 v[4:5], 12, v[2:3]
	v_pk_mul_f32 v[12:13], v[152:153], s[20:21] op_sel_hi:[1,0]
	v_med3_f32 v3, v8, s50, v210
	v_med3_f32 v8, v9, s50, v210
	v_med3_f32 v9, v6, s50, v210
	v_med3_f32 v14, v7, s50, v210
	v_cvt_pk_fp8_f32 v6, v3, v8
	v_med3_f32 v3, v12, s50, v210
	v_med3_f32 v8, v13, s50, v210
	v_cvt_pk_fp8_f32 v7, v3, v8
	v_pk_mul_f32 v[10:11], v[154:155], s[20:21] op_sel_hi:[1,0]
	v_cvt_pk_fp8_f32 v6, v9, v14 op_sel:[0,0,1]
	v_med3_f32 v3, v10, s50, v210
	v_med3_f32 v8, v11, s50, v210
	v_cvt_pk_fp8_f32 v7, v3, v8 op_sel:[0,0,1]
	v_pk_mul_f32 v[8:9], v[150:151], s[20:21] op_sel_hi:[1,0]
	v_pk_mul_f32 v[10:11], v[148:149], s[20:21] op_sel_hi:[1,0]
	v_pk_mul_f32 v[14:15], v[144:145], s[20:21] op_sel_hi:[1,0]
	v_med3_f32 v3, v10, s50, v210
	v_med3_f32 v10, v11, s50, v210
	v_med3_f32 v11, v8, s50, v210
	v_med3_f32 v16, v9, s50, v210
	v_cvt_pk_fp8_f32 v8, v3, v10
	v_med3_f32 v3, v14, s50, v210
	v_med3_f32 v10, v15, s50, v210
	v_cvt_pk_fp8_f32 v9, v3, v10
	s_lshl_b32 s26, s54, 8
	v_pk_mul_f32 v[12:13], v[146:147], s[20:21] op_sel_hi:[1,0]
	s_ashr_i32 s27, s26, 31
	v_lshl_add_u64 v[4:5], s[6:7], 0, v[4:5]
	v_med3_f32 v3, v12, s50, v210
	v_med3_f32 v10, v13, s50, v210
	v_lshlrev_b32_e32 v0, 3, v0
	v_lshl_add_u64 v[4:5], v[4:5], 0, s[26:27]
	v_cvt_pk_fp8_f32 v8, v11, v16 op_sel:[0,0,1]
	v_cvt_pk_fp8_f32 v9, v3, v10 op_sel:[0,0,1]
	v_ashrrev_i32_e32 v1, 31, v0
	v_lshl_add_u64 v[4:5], v[4:5], 0, s[16:17]
	v_lshl_add_u64 v[4:5], v[4:5], 0, v[0:1]
	s_nop 1
	v_permlane16_swap_b32_e32 v6, v8
	v_permlane16_swap_b32_e32 v7, v9
	v_lshl_add_u64 v[248:249], v[4:5], 0, v[250:251]
	global_store_dwordx4 v[248:249], v[6:9], off
	s_nop 1
	v_pk_mul_f32 v[6:7], v[142:143], s[20:21] op_sel_hi:[1,0]
	v_pk_mul_f32 v[8:9], v[140:141], s[20:21] op_sel_hi:[1,0]
	v_pk_mul_f32 v[12:13], v[136:137], s[20:21] op_sel_hi:[1,0]
	v_med3_f32 v3, v8, s50, v210
	v_med3_f32 v8, v9, s50, v210
	v_med3_f32 v9, v6, s50, v210
	v_med3_f32 v14, v7, s50, v210
	v_cvt_pk_fp8_f32 v6, v3, v8
	v_med3_f32 v3, v12, s50, v210
	v_med3_f32 v8, v13, s50, v210
	v_cvt_pk_fp8_f32 v7, v3, v8
	v_pk_mul_f32 v[10:11], v[138:139], s[20:21] op_sel_hi:[1,0]
	v_cvt_pk_fp8_f32 v6, v9, v14 op_sel:[0,0,1]
	v_med3_f32 v3, v10, s50, v210
	v_med3_f32 v8, v11, s50, v210
	v_cvt_pk_fp8_f32 v7, v3, v8 op_sel:[0,0,1]
	v_pk_mul_f32 v[8:9], v[134:135], s[20:21] op_sel_hi:[1,0]
	v_pk_mul_f32 v[10:11], v[132:133], s[20:21] op_sel_hi:[1,0]
	v_pk_mul_f32 v[14:15], v[128:129], s[20:21] op_sel_hi:[1,0]
	v_med3_f32 v3, v10, s50, v210
	v_med3_f32 v10, v11, s50, v210
	v_med3_f32 v11, v8, s50, v210
	v_med3_f32 v16, v9, s50, v210
	v_cvt_pk_fp8_f32 v8, v3, v10
	v_med3_f32 v3, v14, s50, v210
	v_med3_f32 v10, v15, s50, v210
	v_add_u32_e32 v4, 16, v2
	v_cvt_pk_fp8_f32 v9, v3, v10
	v_ashrrev_i32_e32 v5, 31, v4
	v_lshlrev_b64 v[4:5], 12, v[4:5]
	v_pk_mul_f32 v[12:13], v[130:131], s[20:21] op_sel_hi:[1,0]
	v_lshl_add_u64 v[4:5], s[6:7], 0, v[4:5]
	v_med3_f32 v3, v12, s50, v210
	v_med3_f32 v10, v13, s50, v210
	v_lshl_add_u64 v[4:5], v[4:5], 0, s[26:27]
	v_cvt_pk_fp8_f32 v8, v11, v16 op_sel:[0,0,1]
	v_cvt_pk_fp8_f32 v9, v3, v10 op_sel:[0,0,1]
	v_lshl_add_u64 v[4:5], v[4:5], 0, s[16:17]
	v_lshl_add_u64 v[4:5], v[4:5], 0, v[0:1]
	s_nop 1
	v_permlane16_swap_b32_e32 v6, v8
	v_permlane16_swap_b32_e32 v7, v9
	v_lshl_add_u64 v[248:249], v[4:5], 0, v[250:251]
	global_store_dwordx4 v[248:249], v[6:9], off
	s_nop 1
	v_pk_mul_f32 v[6:7], v[126:127], s[20:21] op_sel_hi:[1,0]
	v_pk_mul_f32 v[8:9], v[124:125], s[20:21] op_sel_hi:[1,0]
	v_pk_mul_f32 v[12:13], v[120:121], s[20:21] op_sel_hi:[1,0]
	v_med3_f32 v3, v8, s50, v210
	v_med3_f32 v8, v9, s50, v210
	v_med3_f32 v9, v6, s50, v210
	v_med3_f32 v14, v7, s50, v210
	v_cvt_pk_fp8_f32 v6, v3, v8
	v_med3_f32 v3, v12, s50, v210
	v_med3_f32 v8, v13, s50, v210
	v_cvt_pk_fp8_f32 v7, v3, v8
	v_pk_mul_f32 v[10:11], v[122:123], s[20:21] op_sel_hi:[1,0]
	v_cvt_pk_fp8_f32 v6, v9, v14 op_sel:[0,0,1]
	v_med3_f32 v3, v10, s50, v210
	v_med3_f32 v8, v11, s50, v210
	v_cvt_pk_fp8_f32 v7, v3, v8 op_sel:[0,0,1]
	v_pk_mul_f32 v[8:9], v[118:119], s[20:21] op_sel_hi:[1,0]
	v_pk_mul_f32 v[10:11], v[116:117], s[20:21] op_sel_hi:[1,0]
	v_pk_mul_f32 v[14:15], v[112:113], s[20:21] op_sel_hi:[1,0]
	v_med3_f32 v3, v10, s50, v210
	v_med3_f32 v10, v11, s50, v210
	v_med3_f32 v11, v8, s50, v210
	v_med3_f32 v16, v9, s50, v210
	v_cvt_pk_fp8_f32 v8, v3, v10
	v_med3_f32 v3, v14, s50, v210
	v_med3_f32 v10, v15, s50, v210
	v_add_u32_e32 v4, 32, v2
	v_cvt_pk_fp8_f32 v9, v3, v10
	v_ashrrev_i32_e32 v5, 31, v4
	v_lshlrev_b64 v[4:5], 12, v[4:5]
	v_pk_mul_f32 v[12:13], v[114:115], s[20:21] op_sel_hi:[1,0]
	v_lshl_add_u64 v[4:5], s[6:7], 0, v[4:5]
	v_med3_f32 v3, v12, s50, v210
	v_med3_f32 v10, v13, s50, v210
	v_lshl_add_u64 v[4:5], v[4:5], 0, s[26:27]
	v_cvt_pk_fp8_f32 v8, v11, v16 op_sel:[0,0,1]
	v_cvt_pk_fp8_f32 v9, v3, v10 op_sel:[0,0,1]
	v_lshl_add_u64 v[4:5], v[4:5], 0, s[16:17]
	v_lshl_add_u64 v[4:5], v[4:5], 0, v[0:1]
	s_nop 1
	v_permlane16_swap_b32_e32 v6, v8
	v_permlane16_swap_b32_e32 v7, v9
	v_lshl_add_u64 v[248:249], v[4:5], 0, v[250:251]
	global_store_dwordx4 v[248:249], v[6:9], off
	s_nop 1
	v_pk_mul_f32 v[6:7], v[110:111], s[20:21] op_sel_hi:[1,0]
	v_pk_mul_f32 v[8:9], v[108:109], s[20:21] op_sel_hi:[1,0]
	v_pk_mul_f32 v[12:13], v[104:105], s[20:21] op_sel_hi:[1,0]
	v_med3_f32 v3, v8, s50, v210
	v_med3_f32 v8, v9, s50, v210
	v_med3_f32 v9, v6, s50, v210
	v_med3_f32 v14, v7, s50, v210
	v_cvt_pk_fp8_f32 v6, v3, v8
	v_med3_f32 v3, v12, s50, v210
	v_med3_f32 v8, v13, s50, v210
	v_cvt_pk_fp8_f32 v7, v3, v8
	v_pk_mul_f32 v[10:11], v[106:107], s[20:21] op_sel_hi:[1,0]
	v_cvt_pk_fp8_f32 v6, v9, v14 op_sel:[0,0,1]
	v_med3_f32 v3, v10, s50, v210
	v_med3_f32 v8, v11, s50, v210
	v_cvt_pk_fp8_f32 v7, v3, v8 op_sel:[0,0,1]
	v_pk_mul_f32 v[8:9], v[102:103], s[20:21] op_sel_hi:[1,0]
	v_pk_mul_f32 v[10:11], v[100:101], s[20:21] op_sel_hi:[1,0]
	v_pk_mul_f32 v[14:15], v[96:97], s[20:21] op_sel_hi:[1,0]
	v_med3_f32 v3, v10, s50, v210
	v_med3_f32 v10, v11, s50, v210
	v_med3_f32 v11, v8, s50, v210
	v_med3_f32 v16, v9, s50, v210
	v_cvt_pk_fp8_f32 v8, v3, v10
	v_med3_f32 v3, v14, s50, v210
	v_med3_f32 v10, v15, s50, v210
	v_add_u32_e32 v4, 48, v2
	v_cvt_pk_fp8_f32 v9, v3, v10
	v_ashrrev_i32_e32 v5, 31, v4
	v_lshlrev_b64 v[4:5], 12, v[4:5]
	v_pk_mul_f32 v[12:13], v[98:99], s[20:21] op_sel_hi:[1,0]
	v_lshl_add_u64 v[4:5], s[6:7], 0, v[4:5]
	v_med3_f32 v3, v12, s50, v210
	v_med3_f32 v10, v13, s50, v210
	v_lshl_add_u64 v[4:5], v[4:5], 0, s[26:27]
	v_cvt_pk_fp8_f32 v8, v11, v16 op_sel:[0,0,1]
	v_cvt_pk_fp8_f32 v9, v3, v10 op_sel:[0,0,1]
	v_lshl_add_u64 v[4:5], v[4:5], 0, s[16:17]
	v_lshl_add_u64 v[4:5], v[4:5], 0, v[0:1]
	s_nop 1
	v_permlane16_swap_b32_e32 v6, v8
	v_permlane16_swap_b32_e32 v7, v9
	v_lshl_add_u64 v[248:249], v[4:5], 0, v[250:251]
	global_store_dwordx4 v[248:249], v[6:9], off
	s_nop 1
	v_pk_mul_f32 v[6:7], v[94:95], s[20:21] op_sel_hi:[1,0]
	v_pk_mul_f32 v[8:9], v[92:93], s[20:21] op_sel_hi:[1,0]
	v_pk_mul_f32 v[12:13], v[88:89], s[20:21] op_sel_hi:[1,0]
	v_med3_f32 v3, v8, s50, v210
	v_med3_f32 v8, v9, s50, v210
	v_med3_f32 v9, v6, s50, v210
	v_med3_f32 v14, v7, s50, v210
	v_cvt_pk_fp8_f32 v6, v3, v8
	v_med3_f32 v3, v12, s50, v210
	v_med3_f32 v8, v13, s50, v210
	v_cvt_pk_fp8_f32 v7, v3, v8
	v_pk_mul_f32 v[10:11], v[90:91], s[20:21] op_sel_hi:[1,0]
	v_cvt_pk_fp8_f32 v6, v9, v14 op_sel:[0,0,1]
	v_med3_f32 v3, v10, s50, v210
	v_med3_f32 v8, v11, s50, v210
	v_cvt_pk_fp8_f32 v7, v3, v8 op_sel:[0,0,1]
	v_pk_mul_f32 v[8:9], v[86:87], s[20:21] op_sel_hi:[1,0]
	v_pk_mul_f32 v[10:11], v[84:85], s[20:21] op_sel_hi:[1,0]
	v_pk_mul_f32 v[14:15], v[80:81], s[20:21] op_sel_hi:[1,0]
	v_med3_f32 v3, v10, s50, v210
	v_med3_f32 v10, v11, s50, v210
	v_med3_f32 v11, v8, s50, v210
	v_med3_f32 v16, v9, s50, v210
	v_cvt_pk_fp8_f32 v8, v3, v10
	v_med3_f32 v3, v14, s50, v210
	v_med3_f32 v10, v15, s50, v210
	v_add_u32_e32 v4, 0x80, v2
	v_cvt_pk_fp8_f32 v9, v3, v10
	v_ashrrev_i32_e32 v5, 31, v4
	v_lshlrev_b64 v[4:5], 12, v[4:5]
	v_pk_mul_f32 v[12:13], v[82:83], s[20:21] op_sel_hi:[1,0]
	v_lshl_add_u64 v[4:5], s[6:7], 0, v[4:5]
	v_med3_f32 v3, v12, s50, v210
	v_med3_f32 v10, v13, s50, v210
	v_lshl_add_u64 v[4:5], v[4:5], 0, s[26:27]
	v_cvt_pk_fp8_f32 v8, v11, v16 op_sel:[0,0,1]
	v_cvt_pk_fp8_f32 v9, v3, v10 op_sel:[0,0,1]
	v_lshl_add_u64 v[4:5], v[4:5], 0, s[16:17]
	v_lshl_add_u64 v[4:5], v[4:5], 0, v[0:1]
	s_nop 1
	v_permlane16_swap_b32_e32 v6, v8
	v_permlane16_swap_b32_e32 v7, v9
	v_lshl_add_u64 v[248:249], v[4:5], 0, v[250:251]
	global_store_dwordx4 v[248:249], v[6:9], off
	s_nop 1
	v_pk_mul_f32 v[6:7], v[78:79], s[20:21] op_sel_hi:[1,0]
	v_pk_mul_f32 v[8:9], v[76:77], s[20:21] op_sel_hi:[1,0]
	v_pk_mul_f32 v[12:13], v[72:73], s[20:21] op_sel_hi:[1,0]
	v_med3_f32 v3, v8, s50, v210
	v_med3_f32 v8, v9, s50, v210
	v_med3_f32 v9, v6, s50, v210
	v_med3_f32 v14, v7, s50, v210
	v_cvt_pk_fp8_f32 v6, v3, v8
	v_med3_f32 v3, v12, s50, v210
	v_med3_f32 v8, v13, s50, v210
	v_cvt_pk_fp8_f32 v7, v3, v8
	v_pk_mul_f32 v[10:11], v[74:75], s[20:21] op_sel_hi:[1,0]
	v_cvt_pk_fp8_f32 v6, v9, v14 op_sel:[0,0,1]
	v_med3_f32 v3, v10, s50, v210
	v_med3_f32 v8, v11, s50, v210
	v_cvt_pk_fp8_f32 v7, v3, v8 op_sel:[0,0,1]
	v_pk_mul_f32 v[8:9], v[70:71], s[20:21] op_sel_hi:[1,0]
	v_pk_mul_f32 v[10:11], v[68:69], s[20:21] op_sel_hi:[1,0]
	v_pk_mul_f32 v[14:15], v[64:65], s[20:21] op_sel_hi:[1,0]
	v_med3_f32 v3, v10, s50, v210
	v_med3_f32 v10, v11, s50, v210
	v_med3_f32 v11, v8, s50, v210
	v_med3_f32 v16, v9, s50, v210
	v_cvt_pk_fp8_f32 v8, v3, v10
	v_med3_f32 v3, v14, s50, v210
	v_med3_f32 v10, v15, s50, v210
	v_add_u32_e32 v4, 0x90, v2
	v_cvt_pk_fp8_f32 v9, v3, v10
	v_ashrrev_i32_e32 v5, 31, v4
	v_lshlrev_b64 v[4:5], 12, v[4:5]
	v_pk_mul_f32 v[12:13], v[66:67], s[20:21] op_sel_hi:[1,0]
	v_lshl_add_u64 v[4:5], s[6:7], 0, v[4:5]
	v_med3_f32 v3, v12, s50, v210
	v_med3_f32 v10, v13, s50, v210
	v_lshl_add_u64 v[4:5], v[4:5], 0, s[26:27]
	v_cvt_pk_fp8_f32 v8, v11, v16 op_sel:[0,0,1]
	v_cvt_pk_fp8_f32 v9, v3, v10 op_sel:[0,0,1]
	v_lshl_add_u64 v[4:5], v[4:5], 0, s[16:17]
	v_lshl_add_u64 v[4:5], v[4:5], 0, v[0:1]
	s_nop 1
	v_permlane16_swap_b32_e32 v6, v8
	v_permlane16_swap_b32_e32 v7, v9
	v_lshl_add_u64 v[248:249], v[4:5], 0, v[250:251]
	global_store_dwordx4 v[248:249], v[6:9], off
	s_nop 1
	v_pk_mul_f32 v[6:7], v[62:63], s[20:21] op_sel_hi:[1,0]
	v_pk_mul_f32 v[8:9], v[60:61], s[20:21] op_sel_hi:[1,0]
	v_pk_mul_f32 v[12:13], v[56:57], s[20:21] op_sel_hi:[1,0]
	v_med3_f32 v3, v8, s50, v210
	v_med3_f32 v8, v9, s50, v210
	v_med3_f32 v9, v6, s50, v210
	v_med3_f32 v14, v7, s50, v210
	v_cvt_pk_fp8_f32 v6, v3, v8
	v_med3_f32 v3, v12, s50, v210
	v_med3_f32 v8, v13, s50, v210
	v_cvt_pk_fp8_f32 v7, v3, v8
	v_pk_mul_f32 v[10:11], v[58:59], s[20:21] op_sel_hi:[1,0]
	v_cvt_pk_fp8_f32 v6, v9, v14 op_sel:[0,0,1]
	v_med3_f32 v3, v10, s50, v210
	v_med3_f32 v8, v11, s50, v210
	v_cvt_pk_fp8_f32 v7, v3, v8 op_sel:[0,0,1]
	v_pk_mul_f32 v[8:9], v[54:55], s[20:21] op_sel_hi:[1,0]
	v_pk_mul_f32 v[10:11], v[52:53], s[20:21] op_sel_hi:[1,0]
	v_pk_mul_f32 v[14:15], v[48:49], s[20:21] op_sel_hi:[1,0]
	v_med3_f32 v3, v10, s50, v210
	v_med3_f32 v10, v11, s50, v210
	v_med3_f32 v11, v8, s50, v210
	v_med3_f32 v16, v9, s50, v210
	v_cvt_pk_fp8_f32 v8, v3, v10
	v_med3_f32 v3, v14, s50, v210
	v_med3_f32 v10, v15, s50, v210
	v_add_u32_e32 v4, 0xa0, v2
	v_cvt_pk_fp8_f32 v9, v3, v10
	v_ashrrev_i32_e32 v5, 31, v4
	v_lshlrev_b64 v[4:5], 12, v[4:5]
	v_pk_mul_f32 v[12:13], v[50:51], s[20:21] op_sel_hi:[1,0]
	v_lshl_add_u64 v[4:5], s[6:7], 0, v[4:5]
	v_med3_f32 v3, v12, s50, v210
	v_med3_f32 v10, v13, s50, v210
	v_lshl_add_u64 v[4:5], v[4:5], 0, s[26:27]
	v_cvt_pk_fp8_f32 v8, v11, v16 op_sel:[0,0,1]
	v_cvt_pk_fp8_f32 v9, v3, v10 op_sel:[0,0,1]
	v_lshl_add_u64 v[4:5], v[4:5], 0, s[16:17]
	v_lshl_add_u64 v[4:5], v[4:5], 0, v[0:1]
	s_nop 1
	v_permlane16_swap_b32_e32 v6, v8
	v_permlane16_swap_b32_e32 v7, v9
	v_lshl_add_u64 v[248:249], v[4:5], 0, v[250:251]
	global_store_dwordx4 v[248:249], v[6:9], off
	s_nop 1
	v_pk_mul_f32 v[4:5], v[46:47], s[20:21] op_sel_hi:[1,0]
	v_pk_mul_f32 v[6:7], v[44:45], s[20:21] op_sel_hi:[1,0]
	v_pk_mul_f32 v[10:11], v[40:41], s[20:21] op_sel_hi:[1,0]
	v_med3_f32 v6, v6, s50, v210
	v_med3_f32 v7, v7, s50, v210
	v_med3_f32 v12, v4, s50, v210
	v_med3_f32 v13, v5, s50, v210
	v_cvt_pk_fp8_f32 v4, v6, v7
	v_med3_f32 v6, v10, s50, v210
	v_med3_f32 v7, v11, s50, v210
	v_cvt_pk_fp8_f32 v5, v6, v7
	v_pk_mul_f32 v[8:9], v[42:43], s[20:21] op_sel_hi:[1,0]
	v_cvt_pk_fp8_f32 v4, v12, v13 op_sel:[0,0,1]
	v_med3_f32 v6, v8, s50, v210
	v_med3_f32 v7, v9, s50, v210
	v_cvt_pk_fp8_f32 v5, v6, v7 op_sel:[0,0,1]
	v_pk_mul_f32 v[6:7], v[38:39], s[20:21] op_sel_hi:[1,0]
	v_pk_mul_f32 v[8:9], v[36:37], s[20:21] op_sel_hi:[1,0]
	v_pk_mul_f32 v[12:13], v[32:33], s[20:21] op_sel_hi:[1,0]
	v_med3_f32 v8, v8, s50, v210
	v_med3_f32 v9, v9, s50, v210
	v_med3_f32 v14, v6, s50, v210
	v_med3_f32 v15, v7, s50, v210
	v_cvt_pk_fp8_f32 v6, v8, v9
	v_med3_f32 v8, v12, s50, v210
	v_med3_f32 v9, v13, s50, v210
	v_add_u32_e32 v2, 0xb0, v2
	v_cvt_pk_fp8_f32 v7, v8, v9
	v_ashrrev_i32_e32 v3, 31, v2
	v_lshlrev_b64 v[2:3], 12, v[2:3]
	v_pk_mul_f32 v[10:11], v[34:35], s[20:21] op_sel_hi:[1,0]
	v_lshl_add_u64 v[2:3], s[6:7], 0, v[2:3]
	v_med3_f32 v8, v10, s50, v210
	v_med3_f32 v9, v11, s50, v210
	v_lshl_add_u64 v[2:3], v[2:3], 0, s[26:27]
	v_cvt_pk_fp8_f32 v6, v14, v15 op_sel:[0,0,1]
	v_cvt_pk_fp8_f32 v7, v8, v9 op_sel:[0,0,1]
	v_lshl_add_u64 v[2:3], v[2:3], 0, s[16:17]
	v_lshl_add_u64 v[0:1], v[2:3], 0, v[0:1]
	s_and_b64 vcc, exec, s[2:3]
	s_mov_b64 s[2:3], -1
	s_nop 1
	v_permlane16_swap_b32_e32 v4, v6
	v_permlane16_swap_b32_e32 v5, v7
	v_lshl_add_u64 v[248:249], v[0:1], 0, v[250:251]
	global_store_dwordx4 v[248:249], v[4:7], off
	s_nop 1
	s_cbranch_vccnz .LBB0_811
	s_andn2_b64 vcc, exec, s[4:5]
	s_cbranch_vccnz .LBB0_810
	s_barrier
	s_branch .LBB0_810

.LBB0_1548:
	s_add_u32 s58, s24, 0x100
	s_addc_u32 s59, s25, 0
	v_mov_b32_e32 v169, v165
	v_mov_b32_e32 v171, v165
	s_add_u32 s60, s26, 0x100
	v_mov_b32_e32 v175, v165
	v_mov_b32_e32 v177, v165
	v_lshl_add_u64 v[178:179], s[14:15], 0, v[170:171]
	v_lshl_add_u64 v[180:181], s[14:15], 0, v[168:169]
	s_addc_u32 s61, s27, 0
	s_mov_b32 s62, -2
	s_mov_b64 s[24:25], 0
	s_waitcnt vmcnt(0)
	v_add_u32_e32 v252, 0x10000, v204
	v_add_u32_e32 v253, 0x10000, v205
	s_branch .LBB0_1550
.LBB0_1549:
	s_add_u32 s26, s4, s24
	s_addc_u32 s27, s5, s25
	s_add_u32 s28, s26, 0x28000100
	s_addc_u32 s29, s27, 0
	ds_read_b128 v[24:27], v252
	ds_read_b128 v[28:31], v253
	s_and_b64 s[26:27], s[30:31], exec
	ds_read_b128 v[16:19], v252 offset:2048
	ds_read_b128 v[20:23], v253 offset:2048
	s_cselect_b32 s27, s7, s29
	s_cselect_b32 s26, s6, s28
	s_add_u32 s63, s58, s24
	ds_read_b128 v[8:11], v252 offset:16384
	ds_read_b128 v[12:15], v253 offset:16384
	s_addc_u32 s64, s59, s25
	ds_read_b128 v[0:3], v252 offset:18432
	ds_read_b128 v[4:7], v253 offset:18432
	s_and_b64 s[28:29], s[30:31], exec
	s_cselect_b32 s29, s21, s64
	s_cselect_b32 s28, s20, s63
	s_add_u32 s63, s60, s24
	s_addc_u32 s64, s61, s25
	s_and_b64 s[30:31], s[30:31], exec
	s_cselect_b32 s31, s23, s64
	s_cselect_b32 s30, s22, s63
	s_add_u32 s100, s14, s24
	s_addc_u32 s101, s15, s25
	s_add_i32 m0, s35, 0xc000
	ds_read_b128 v[186:189], v206
	ds_read_b128 v[214:217], v206 offset:2048
	ds_read_b128 v[190:193], v207
	ds_read_b128 v[218:221], v207 offset:2048
	ds_read_b128 v[222:225], v206 offset:4096
	ds_read_b128 v[230:233], v206 offset:6144
	ds_read_b128 v[226:229], v207 offset:4096
	ds_read_b128 v[234:237], v207 offset:6144
	global_load_lds_dwordx4 v168, s[100:101]
	s_add_i32 m0, s35, 0xe000
	s_nop 0
	global_load_lds_dwordx4 v170, s[100:101]
	s_waitcnt vmcnt(8)
	s_waitcnt lgkmcnt(0)
	s_barrier
	s_setprio 1
	s_waitcnt lgkmcnt(0)
	s_cmp_eq_u32 s24, 0
	s_cbranch_scc1 .Lc0_P12_0
	v_mfma_f32_16x16x128_f8f6f4 v[156:159], v[24:31], v[186:193], v[156:159]
	v_mfma_f32_16x16x128_f8f6f4 v[152:155], v[16:23], v[186:193], v[152:155]
	v_mfma_f32_16x16x128_f8f6f4 v[136:139], v[16:23], v[214:221], v[136:139]
	v_mfma_f32_16x16x128_f8f6f4 v[144:147], v[24:31], v[214:221], v[144:147]
	v_mfma_f32_16x16x128_f8f6f4 v[124:127], v[24:31], v[222:229], v[124:127]
	v_mfma_f32_16x16x128_f8f6f4 v[120:123], v[16:23], v[222:229], v[120:123]
	v_mfma_f32_16x16x128_f8f6f4 v[104:107], v[16:23], v[230:237], v[104:107]
	v_mfma_f32_16x16x128_f8f6f4 v[112:115], v[24:31], v[230:237], v[112:115]
	v_mfma_f32_16x16x128_f8f6f4 v[148:151], v[8:15], v[186:193], v[148:151]
	v_mfma_f32_16x16x128_f8f6f4 v[140:143], v[0:7], v[186:193], v[140:143]
	v_mfma_f32_16x16x128_f8f6f4 v[128:131], v[0:7], v[214:221], v[128:131]
	v_mfma_f32_16x16x128_f8f6f4 v[132:135], v[8:15], v[214:221], v[132:135]
	v_mfma_f32_16x16x128_f8f6f4 v[116:119], v[8:15], v[222:229], v[116:119]
	v_mfma_f32_16x16x128_f8f6f4 v[108:111], v[0:7], v[222:229], v[108:111]
	v_mfma_f32_16x16x128_f8f6f4 v[96:99], v[0:7], v[230:237], v[96:99]
	v_mfma_f32_16x16x128_f8f6f4 v[100:103], v[8:15], v[230:237], v[100:103]
.Lc0b_P12_0:
	s_setprio 0
	s_barrier
	s_add_i32 s63, s46, s34
	s_mov_b32 m0, s63
	ds_read_b128 v[214:217], v206 offset:16384
	ds_read_b128 v[222:225], v206 offset:18432
	ds_read_b128 v[218:221], v207 offset:16384
	ds_read_b128 v[226:229], v207 offset:18432
	ds_read_b128 v[230:233], v206 offset:20480
	ds_read_b128 v[238:241], v206 offset:22528
	ds_read_b128 v[234:237], v207 offset:20480
	ds_read_b128 v[242:245], v207 offset:22528
	global_load_lds_dwordx4 v160, s[28:29]
	s_add_i32 m0, s63, 0x2000
	s_add_i32 s98, s48, s34
	global_load_lds_dwordx4 v162, s[28:29]
	s_mov_b32 m0, s98
	s_nop 0
	global_load_lds_dwordx4 v160, s[30:31]
	s_add_i32 m0, s98, 0x2000
	v_mov_b32_e32 v167, v165
	global_load_lds_dwordx4 v162, s[30:31]
	s_waitcnt vmcnt(6)
	s_waitcnt lgkmcnt(0)
	s_barrier
	s_setprio 1
	s_waitcnt lgkmcnt(0)
	s_cmp_eq_u32 s24, 0
	s_cbranch_scc1 .Lc0_P12_1
	v_mfma_f32_16x16x128_f8f6f4 v[92:95], v[24:31], v[214:221], v[92:95]
	v_mfma_f32_16x16x128_f8f6f4 v[88:91], v[16:23], v[214:221], v[88:91]
	v_mfma_f32_16x16x128_f8f6f4 v[72:75], v[16:23], v[222:229], v[72:75]
	v_mfma_f32_16x16x128_f8f6f4 v[80:83], v[24:31], v[222:229], v[80:83]
	s_mov_b32 m0, s35
	v_mfma_f32_16x16x128_f8f6f4 v[60:63], v[24:31], v[230:237], v[60:63]
	global_load_lds_dwordx4 v164, s[26:27]
	v_mfma_f32_16x16x128_f8f6f4 v[56:59], v[16:23], v[230:237], v[56:59]
	v_mfma_f32_16x16x128_f8f6f4 v[40:43], v[16:23], v[238:245], v[40:43]
	v_mfma_f32_16x16x128_f8f6f4 v[48:51], v[24:31], v[238:245], v[48:51]
	v_mfma_f32_16x16x128_f8f6f4 v[84:87], v[8:15], v[214:221], v[84:87]
	s_mov_b32 m0, s36
	v_mfma_f32_16x16x128_f8f6f4 v[76:79], v[0:7], v[214:221], v[76:79]
	global_load_lds_dwordx4 v166, s[26:27]
	v_mfma_f32_16x16x128_f8f6f4 v[64:67], v[0:7], v[222:229], v[64:67]
	v_mfma_f32_16x16x128_f8f6f4 v[68:71], v[8:15], v[222:229], v[68:71]
	v_mfma_f32_16x16x128_f8f6f4 v[52:55], v[8:15], v[230:237], v[52:55]
	v_mfma_f32_16x16x128_f8f6f4 v[44:47], v[0:7], v[230:237], v[44:47]
	v_mfma_f32_16x16x128_f8f6f4 v[32:35], v[0:7], v[238:245], v[32:35]
	v_mfma_f32_16x16x128_f8f6f4 v[36:39], v[8:15], v[238:245], v[36:39]
.Lc0b_P12_1:
	s_setprio 0
	s_barrier
	ds_read_b128 v[0:3], v252 offset:32768
	ds_read_b128 v[4:7], v253 offset:32768
	ds_read_b128 v[8:11], v252 offset:34816
	ds_read_b128 v[12:15], v253 offset:34816
	ds_read_b128 v[16:19], v252 offset:49152
	ds_read_b128 v[20:23], v253 offset:49152
	ds_read_b128 v[24:27], v252 offset:51200
	ds_read_b128 v[28:31], v253 offset:51200
	s_mov_b32 m0, s37
	ds_read_b128 v[214:217], v206 offset:32768
	ds_read_b128 v[222:225], v206 offset:34816
	ds_read_b128 v[218:221], v207 offset:32768
	ds_read_b128 v[226:229], v207 offset:34816
	ds_read_b128 v[230:233], v206 offset:36864
	ds_read_b128 v[238:241], v206 offset:38912
	ds_read_b128 v[234:237], v207 offset:36864
	ds_read_b128 v[242:245], v207 offset:38912
	global_load_lds_dwordx4 v184, s[26:27]
	s_mov_b32 m0, s38
	s_nop 0
	global_load_lds_dwordx4 v182, s[26:27]
	s_waitcnt vmcnt(8)
	s_waitcnt lgkmcnt(0)
	s_barrier
	s_setprio 1
	s_waitcnt lgkmcnt(0)
	v_mfma_f32_16x16x128_f8f6f4 v[156:159], v[0:7], v[214:221], v[156:159]
	v_mfma_f32_16x16x128_f8f6f4 v[152:155], v[8:15], v[214:221], v[152:155]
	v_mfma_f32_16x16x128_f8f6f4 v[136:139], v[8:15], v[222:229], v[136:139]
	v_mfma_f32_16x16x128_f8f6f4 v[144:147], v[0:7], v[222:229], v[144:147]
	v_mfma_f32_16x16x128_f8f6f4 v[124:127], v[0:7], v[230:237], v[124:127]
	v_mfma_f32_16x16x128_f8f6f4 v[120:123], v[8:15], v[230:237], v[120:123]
	v_mfma_f32_16x16x128_f8f6f4 v[104:107], v[8:15], v[238:245], v[104:107]
	v_mfma_f32_16x16x128_f8f6f4 v[112:115], v[0:7], v[238:245], v[112:115]
	v_mfma_f32_16x16x128_f8f6f4 v[148:151], v[16:23], v[214:221], v[148:151]
	v_mfma_f32_16x16x128_f8f6f4 v[140:143], v[24:31], v[214:221], v[140:143]
	v_mfma_f32_16x16x128_f8f6f4 v[128:131], v[24:31], v[222:229], v[128:131]
	v_mfma_f32_16x16x128_f8f6f4 v[132:135], v[16:23], v[222:229], v[132:135]
	v_mfma_f32_16x16x128_f8f6f4 v[116:119], v[16:23], v[230:237], v[116:119]
	v_mfma_f32_16x16x128_f8f6f4 v[108:111], v[24:31], v[230:237], v[108:111]
	v_mfma_f32_16x16x128_f8f6f4 v[96:99], v[24:31], v[238:245], v[96:99]
	v_mfma_f32_16x16x128_f8f6f4 v[100:103], v[16:23], v[238:245], v[100:103]
	s_setprio 0
	s_barrier
	s_add_i32 s99, s34, 0x17f80
	s_mov_b32 m0, s99
	ds_read_b128 v[214:217], v206 offset:49152
	ds_read_b128 v[222:225], v206 offset:51200
	ds_read_b128 v[218:221], v207 offset:49152
	ds_read_b128 v[226:229], v207 offset:51200
	ds_read_b128 v[230:233], v206 offset:53248
	ds_read_b128 v[238:241], v206 offset:55296
	ds_read_b128 v[234:237], v207 offset:53248
	ds_read_b128 v[242:245], v207 offset:55296
	global_load_lds_dwordx4 v160, s[28:29] offset:128
	s_add_i32 m0, s99, 0x2000
	s_add_i32 s99, s34, 0x1bf80
	global_load_lds_dwordx4 v162, s[28:29] offset:128
	s_mov_b32 m0, s99
	s_nop 0
	global_load_lds_dwordx4 v160, s[30:31] offset:128
	s_add_i32 m0, s99, 0x2000
	s_nop 0
	global_load_lds_dwordx4 v162, s[30:31] offset:128
	s_waitcnt vmcnt(6)
	s_waitcnt lgkmcnt(0)
	s_barrier
	s_setprio 1
	s_waitcnt lgkmcnt(0)
	v_mfma_f32_16x16x128_f8f6f4 v[92:95], v[0:7], v[214:221], v[92:95]
	v_mfma_f32_16x16x128_f8f6f4 v[88:91], v[8:15], v[214:221], v[88:91]
	v_mfma_f32_16x16x128_f8f6f4 v[72:75], v[8:15], v[222:229], v[72:75]
	v_mfma_f32_16x16x128_f8f6f4 v[80:83], v[0:7], v[222:229], v[80:83]
	s_add_i32 m0, s41, 0xffffff80
	v_mfma_f32_16x16x128_f8f6f4 v[60:63], v[0:7], v[230:237], v[60:63]
	global_load_lds_dwordx4 v164, s[26:27] offset:128
	v_mfma_f32_16x16x128_f8f6f4 v[56:59], v[8:15], v[230:237], v[56:59]
	v_mfma_f32_16x16x128_f8f6f4 v[40:43], v[8:15], v[238:245], v[40:43]
	v_mfma_f32_16x16x128_f8f6f4 v[48:51], v[0:7], v[238:245], v[48:51]
	v_mfma_f32_16x16x128_f8f6f4 v[84:87], v[16:23], v[214:221], v[84:87]
	s_add_i32 m0, s42, 0xffffff80
	v_mfma_f32_16x16x128_f8f6f4 v[76:79], v[24:31], v[214:221], v[76:79]
	global_load_lds_dwordx4 v166, s[26:27] offset:128
	v_mfma_f32_16x16x128_f8f6f4 v[64:67], v[24:31], v[222:229], v[64:67]
	v_mfma_f32_16x16x128_f8f6f4 v[68:71], v[16:23], v[222:229], v[68:71]
	v_mfma_f32_16x16x128_f8f6f4 v[52:55], v[16:23], v[230:237], v[52:55]
	v_mfma_f32_16x16x128_f8f6f4 v[44:47], v[24:31], v[230:237], v[44:47]
	v_mfma_f32_16x16x128_f8f6f4 v[32:35], v[24:31], v[238:245], v[32:35]
	v_mfma_f32_16x16x128_f8f6f4 v[36:39], v[16:23], v[238:245], v[36:39]
	s_setprio 0
	s_barrier
	s_add_i32 s62, s62, 2
	s_add_u32 s24, s24, 0x100
	s_addc_u32 s25, s25, 0
	s_cmp_gt_u32 s62, 29
	s_cbranch_scc1 .LBB0_1552

.Lc0_P12_0:
	v_mfma_f32_16x16x128_f8f6f4 v[156:159], v[24:31], v[186:193], 0
	v_mfma_f32_16x16x128_f8f6f4 v[152:155], v[16:23], v[186:193], 0
	v_mfma_f32_16x16x128_f8f6f4 v[136:139], v[16:23], v[214:221], 0
	v_mfma_f32_16x16x128_f8f6f4 v[144:147], v[24:31], v[214:221], 0
	v_mfma_f32_16x16x128_f8f6f4 v[124:127], v[24:31], v[222:229], 0
	v_mfma_f32_16x16x128_f8f6f4 v[120:123], v[16:23], v[222:229], 0
	v_mfma_f32_16x16x128_f8f6f4 v[104:107], v[16:23], v[230:237], 0
	v_mfma_f32_16x16x128_f8f6f4 v[112:115], v[24:31], v[230:237], 0
	v_mfma_f32_16x16x128_f8f6f4 v[148:151], v[8:15], v[186:193], 0
	v_mfma_f32_16x16x128_f8f6f4 v[140:143], v[0:7], v[186:193], 0
	v_mfma_f32_16x16x128_f8f6f4 v[128:131], v[0:7], v[214:221], 0
	v_mfma_f32_16x16x128_f8f6f4 v[132:135], v[8:15], v[214:221], 0
	v_mfma_f32_16x16x128_f8f6f4 v[116:119], v[8:15], v[222:229], 0
	v_mfma_f32_16x16x128_f8f6f4 v[108:111], v[0:7], v[222:229], 0
	v_mfma_f32_16x16x128_f8f6f4 v[96:99], v[0:7], v[230:237], 0
	v_mfma_f32_16x16x128_f8f6f4 v[100:103], v[8:15], v[230:237], 0
	s_branch .Lc0b_P12_0
.Lc0_P12_1:
	v_mfma_f32_16x16x128_f8f6f4 v[92:95], v[24:31], v[214:221], 0
	v_mfma_f32_16x16x128_f8f6f4 v[88:91], v[16:23], v[214:221], 0
	v_mfma_f32_16x16x128_f8f6f4 v[72:75], v[16:23], v[222:229], 0
	v_mfma_f32_16x16x128_f8f6f4 v[80:83], v[24:31], v[222:229], 0
	s_mov_b32 m0, s35
	v_mfma_f32_16x16x128_f8f6f4 v[60:63], v[24:31], v[230:237], 0
	global_load_lds_dwordx4 v164, s[26:27]
	v_mfma_f32_16x16x128_f8f6f4 v[56:59], v[16:23], v[230:237], 0
	v_mfma_f32_16x16x128_f8f6f4 v[40:43], v[16:23], v[238:245], 0
	v_mfma_f32_16x16x128_f8f6f4 v[48:51], v[24:31], v[238:245], 0
	v_mfma_f32_16x16x128_f8f6f4 v[84:87], v[8:15], v[214:221], 0
	s_mov_b32 m0, s36
	v_mfma_f32_16x16x128_f8f6f4 v[76:79], v[0:7], v[214:221], 0
	global_load_lds_dwordx4 v166, s[26:27]
	v_mfma_f32_16x16x128_f8f6f4 v[64:67], v[0:7], v[222:229], 0
	v_mfma_f32_16x16x128_f8f6f4 v[68:71], v[8:15], v[222:229], 0
	v_mfma_f32_16x16x128_f8f6f4 v[52:55], v[8:15], v[230:237], 0
	v_mfma_f32_16x16x128_f8f6f4 v[44:47], v[0:7], v[230:237], 0
	v_mfma_f32_16x16x128_f8f6f4 v[32:35], v[0:7], v[238:245], 0
	v_mfma_f32_16x16x128_f8f6f4 v[36:39], v[8:15], v[238:245], 0
	s_branch .Lc0b_P12_1

.LBB0_1714:
	v_mbcnt_lo_u32_b32 v250, -1, 0
	v_mbcnt_hi_u32_b32 v250, -1, v250
	v_bfe_u32 v250, v250, 4, 1
	v_cmp_eq_u32_e32 vcc, 1, v250
	v_mov_b32_e32 v251, 0xffffc000
	v_mov_b32_e32 v250, -8
	s_nop 0
	v_cndmask_b32_e32 v250, v251, v250, vcc
	v_mov_b32_e32 v251, -1
	s_lshl_b32 s4, s84, 7
	v_mov_b32_e32 v0, v196
	v_mov_b32_e32 v17, v173
	s_or_b32 s4, s4, s69
	s_and_b64 vcc, exec, s[2:3]
	v_lshl_add_u32 v16, v0, 3, s4
	s_lshl_b32 s4, s85, 10
	s_and_b32 s4, s4, 0x400
	s_add_i32 s4, s70, s4
	v_lshl_add_u32 v0, v0, 5, s4
	ds_read_b128 v[12:15], v0
	ds_read_b128 v[4:7], v0 offset:16
	ds_read_b128 v[8:11], v0 offset:512
	ds_read_b128 v[0:3], v0 offset:528
	s_lshl_b32 s4, s83, 8
	s_waitcnt lgkmcnt(0)
	v_pk_fma_f32 v[20:21], v[156:157], s[22:23], v[12:13] op_sel_hi:[1,0,1]
	v_pk_fma_f32 v[26:27], v[158:159], s[22:23], v[14:15] op_sel_hi:[1,0,1]
	v_min_f32_e32 v20, 0x40e00000, v20
	v_min_f32_e32 v21, 0x40e00000, v21
	v_pk_mul_f32 v[22:23], v[20:21], s[24:25] op_sel_hi:[1,0]
	v_min_f32_e32 v26, 0x40e00000, v26
	v_exp_f32_e32 v22, v22
	v_exp_f32_e32 v23, v23
	v_min_f32_e32 v27, 0x40e00000, v27
	v_pk_mul_f32 v[28:29], v[26:27], s[24:25] op_sel_hi:[1,0]
	v_pk_fma_f32 v[24:25], v[152:153], s[22:23], v[8:9] op_sel_hi:[1,0,1]
	v_pk_add_f32 v[22:23], v[22:23], 1.0 op_sel_hi:[1,0]
	v_exp_f32_e32 v28, v28
	v_rcp_f32_e32 v22, v22
	v_rcp_f32_e32 v23, v23
	v_exp_f32_e32 v29, v29
	v_med3_f32 v24, v24, s78, v204
	v_med3_f32 v25, v25, s78, v204
	v_pk_mul_f32 v[20:21], v[20:21], v[22:23]
	v_pk_fma_f32 v[22:23], v[24:25], 4.0, 4.0 op_sel_hi:[1,0,0]
	v_pk_fma_f32 v[24:25], v[154:155], s[22:23], v[10:11] op_sel_hi:[1,0,1]
	v_pk_mul_f32 v[20:21], v[22:23], v[20:21]
	v_pk_add_f32 v[22:23], v[28:29], 1.0 op_sel_hi:[1,0]
	v_med3_f32 v24, v24, s78, v204
	v_rcp_f32_e32 v22, v22
	v_rcp_f32_e32 v23, v23
	v_med3_f32 v25, v25, s78, v204
	v_pk_fma_f32 v[24:25], v[24:25], 4.0, 4.0 op_sel_hi:[1,0,0]
	v_pk_fma_f32 v[30:31], v[150:151], s[22:23], v[6:7] op_sel_hi:[1,0,1]
	v_pk_mul_f32 v[22:23], v[26:27], v[22:23]
	v_min_f32_e32 v30, 0x40e00000, v30
	v_pk_mul_f32 v[22:23], v[24:25], v[22:23]
	v_pk_fma_f32 v[24:25], v[148:149], s[22:23], v[4:5] op_sel_hi:[1,0,1]
	v_min_f32_e32 v31, 0x40e00000, v31
	v_min_f32_e32 v24, 0x40e00000, v24
	v_min_f32_e32 v25, 0x40e00000, v25
	v_pk_mul_f32 v[26:27], v[24:25], s[24:25] op_sel_hi:[1,0]
	v_pk_fma_f32 v[28:29], v[144:145], s[22:23], v[0:1] op_sel_hi:[1,0,1]
	v_exp_f32_e32 v26, v26
	v_exp_f32_e32 v27, v27
	v_pk_mul_f32 v[144:145], v[30:31], s[24:25] op_sel_hi:[1,0]
	v_med3_f32 v28, v28, s78, v204
	v_exp_f32_e32 v144, v144
	v_pk_add_f32 v[26:27], v[26:27], 1.0 op_sel_hi:[1,0]
	v_exp_f32_e32 v145, v145
	v_rcp_f32_e32 v26, v26
	v_rcp_f32_e32 v27, v27
	v_med3_f32 v29, v29, s78, v204
	s_add_i32 s4, s4, s71
	v_add_u32_e32 v18, s4, v17
	v_pk_mul_f32 v[24:25], v[24:25], v[26:27]
	v_pk_fma_f32 v[26:27], v[28:29], 4.0, 4.0 op_sel_hi:[1,0,0]
	v_pk_fma_f32 v[28:29], v[146:147], s[22:23], v[2:3] op_sel_hi:[1,0,1]
	v_pk_mul_f32 v[24:25], v[26:27], v[24:25]
	v_pk_add_f32 v[26:27], v[144:145], 1.0 op_sel_hi:[1,0]
	v_med3_f32 v28, v28, s78, v204
	v_rcp_f32_e32 v26, v26
	v_rcp_f32_e32 v27, v27
	v_med3_f32 v29, v29, s78, v204
	v_ashrrev_i32_e32 v19, 31, v18
	v_ashrrev_i32_e32 v17, 31, v16
	v_pk_mul_f32 v[26:27], v[30:31], v[26:27]
	v_mov_b32_e32 v244, v165
	v_mov_b32_e32 v245, v165
	v_cvt_pk_fp8_f32 v244, v20, v21
	v_cvt_pk_fp8_f32 v245, v24, v25
	v_pk_fma_f32 v[20:21], v[28:29], 4.0, 4.0 op_sel_hi:[1,0,0]
	v_pk_fma_f32 v[24:25], v[136:137], s[22:23], v[8:9] op_sel_hi:[1,0,1]
	v_pk_mul_f32 v[20:21], v[20:21], v[26:27]
	v_cvt_pk_fp8_f32 v244, v22, v23 op_sel:[0,0,1]
	v_cvt_pk_fp8_f32 v245, v20, v21 op_sel:[0,0,1]
	v_lshlrev_b64 v[20:21], 10, v[18:19]
	v_lshl_add_u64 v[20:21], s[14:15], 0, v[20:21]
	v_lshl_add_u64 v[20:21], v[20:21], 0, v[16:17]
	v_pk_fma_f32 v[20:21], v[140:141], s[22:23], v[12:13] op_sel_hi:[1,0,1]
	v_pk_fma_f32 v[26:27], v[142:143], s[22:23], v[14:15] op_sel_hi:[1,0,1]
	v_min_f32_e32 v20, 0x40e00000, v20
	v_min_f32_e32 v21, 0x40e00000, v21
	v_pk_mul_f32 v[22:23], v[20:21], s[24:25] op_sel_hi:[1,0]
	v_min_f32_e32 v26, 0x40e00000, v26
	v_exp_f32_e32 v22, v22
	v_exp_f32_e32 v23, v23
	v_min_f32_e32 v27, 0x40e00000, v27
	v_pk_mul_f32 v[28:29], v[26:27], s[24:25] op_sel_hi:[1,0]
	v_med3_f32 v24, v24, s78, v204
	v_pk_add_f32 v[22:23], v[22:23], 1.0 op_sel_hi:[1,0]
	v_exp_f32_e32 v28, v28
	v_rcp_f32_e32 v22, v22
	v_rcp_f32_e32 v23, v23
	v_exp_f32_e32 v29, v29
	v_med3_f32 v25, v25, s78, v204
	v_pk_fma_f32 v[30:31], v[134:135], s[22:23], v[6:7] op_sel_hi:[1,0,1]
	v_pk_mul_f32 v[20:21], v[20:21], v[22:23]
	v_pk_fma_f32 v[22:23], v[24:25], 4.0, 4.0 op_sel_hi:[1,0,0]
	v_pk_fma_f32 v[24:25], v[138:139], s[22:23], v[10:11] op_sel_hi:[1,0,1]
	v_pk_mul_f32 v[20:21], v[22:23], v[20:21]
	v_pk_add_f32 v[22:23], v[28:29], 1.0 op_sel_hi:[1,0]
	v_med3_f32 v24, v24, s78, v204
	v_rcp_f32_e32 v22, v22
	v_rcp_f32_e32 v23, v23
	v_med3_f32 v25, v25, s78, v204
	v_pk_fma_f32 v[24:25], v[24:25], 4.0, 4.0 op_sel_hi:[1,0,0]
	v_min_f32_e32 v30, 0x40e00000, v30
	v_pk_mul_f32 v[22:23], v[26:27], v[22:23]
	v_min_f32_e32 v31, 0x40e00000, v31
	v_pk_mul_f32 v[22:23], v[24:25], v[22:23]
	v_pk_fma_f32 v[24:25], v[132:133], s[22:23], v[4:5] op_sel_hi:[1,0,1]
	v_pk_fma_f32 v[28:29], v[128:129], s[22:23], v[0:1] op_sel_hi:[1,0,1]
	v_min_f32_e32 v24, 0x40e00000, v24
	v_min_f32_e32 v25, 0x40e00000, v25
	v_pk_mul_f32 v[26:27], v[24:25], s[24:25] op_sel_hi:[1,0]
	v_pk_mul_f32 v[128:129], v[30:31], s[24:25] op_sel_hi:[1,0]
	v_exp_f32_e32 v26, v26
	v_exp_f32_e32 v27, v27
	v_exp_f32_e32 v128, v128
	v_exp_f32_e32 v129, v129
	v_med3_f32 v28, v28, s78, v204
	v_pk_add_f32 v[26:27], v[26:27], 1.0 op_sel_hi:[1,0]
	v_med3_f32 v29, v29, s78, v204
	v_rcp_f32_e32 v26, v26
	v_rcp_f32_e32 v27, v27
	s_mov_b64 s[2:3], -1
	v_pk_mul_f32 v[24:25], v[24:25], v[26:27]
	v_pk_fma_f32 v[26:27], v[28:29], 4.0, 4.0 op_sel_hi:[1,0,0]
	v_pk_fma_f32 v[28:29], v[130:131], s[22:23], v[2:3] op_sel_hi:[1,0,1]
	v_pk_mul_f32 v[24:25], v[26:27], v[24:25]
	v_pk_add_f32 v[26:27], v[128:129], 1.0 op_sel_hi:[1,0]
	v_med3_f32 v28, v28, s78, v204
	v_rcp_f32_e32 v26, v26
	v_rcp_f32_e32 v27, v27
	v_med3_f32 v29, v29, s78, v204
	v_pk_mul_f32 v[26:27], v[30:31], v[26:27]
	v_cvt_pk_fp8_f32 v247, v24, v25
	v_cvt_pk_fp8_f32 v246, v20, v21
	v_pk_fma_f32 v[20:21], v[28:29], 4.0, 4.0 op_sel_hi:[1,0,0]
	v_pk_fma_f32 v[24:25], v[120:121], s[22:23], v[8:9] op_sel_hi:[1,0,1]
	v_pk_mul_f32 v[20:21], v[20:21], v[26:27]
	v_cvt_pk_fp8_f32 v246, v22, v23 op_sel:[0,0,1]
	v_cvt_pk_fp8_f32 v247, v20, v21 op_sel:[0,0,1]
	v_add_u32_e32 v20, 16, v18
	v_ashrrev_i32_e32 v21, 31, v20
	v_lshlrev_b64 v[20:21], 10, v[20:21]
	v_lshl_add_u64 v[20:21], s[14:15], 0, v[20:21]
	v_lshl_add_u64 v[20:21], v[20:21], 0, v[16:17]
	s_nop 1
	v_permlane16_swap_b32_e32 v244, v246
	v_permlane16_swap_b32_e32 v245, v247
	v_lshl_add_u64 v[248:249], v[20:21], 0, v[250:251]
	global_store_dwordx4 v[248:249], v[244:247], off
	s_nop 1
	v_pk_fma_f32 v[20:21], v[124:125], s[22:23], v[12:13] op_sel_hi:[1,0,1]
	v_pk_fma_f32 v[26:27], v[126:127], s[22:23], v[14:15] op_sel_hi:[1,0,1]
	v_min_f32_e32 v20, 0x40e00000, v20
	v_min_f32_e32 v21, 0x40e00000, v21
	v_pk_mul_f32 v[22:23], v[20:21], s[24:25] op_sel_hi:[1,0]
	v_min_f32_e32 v26, 0x40e00000, v26
	v_exp_f32_e32 v22, v22
	v_exp_f32_e32 v23, v23
	v_min_f32_e32 v27, 0x40e00000, v27
	v_pk_mul_f32 v[28:29], v[26:27], s[24:25] op_sel_hi:[1,0]
	v_med3_f32 v24, v24, s78, v204
	v_pk_add_f32 v[22:23], v[22:23], 1.0 op_sel_hi:[1,0]
	v_exp_f32_e32 v28, v28
	v_rcp_f32_e32 v22, v22
	v_rcp_f32_e32 v23, v23
	v_exp_f32_e32 v29, v29
	v_med3_f32 v25, v25, s78, v204
	v_pk_fma_f32 v[30:31], v[118:119], s[22:23], v[6:7] op_sel_hi:[1,0,1]
	v_pk_mul_f32 v[20:21], v[20:21], v[22:23]
	v_pk_fma_f32 v[22:23], v[24:25], 4.0, 4.0 op_sel_hi:[1,0,0]
	v_pk_fma_f32 v[24:25], v[122:123], s[22:23], v[10:11] op_sel_hi:[1,0,1]
	v_pk_mul_f32 v[20:21], v[22:23], v[20:21]
	v_pk_add_f32 v[22:23], v[28:29], 1.0 op_sel_hi:[1,0]
	v_med3_f32 v24, v24, s78, v204
	v_rcp_f32_e32 v22, v22
	v_rcp_f32_e32 v23, v23
	v_med3_f32 v25, v25, s78, v204
	v_pk_fma_f32 v[24:25], v[24:25], 4.0, 4.0 op_sel_hi:[1,0,0]
	v_min_f32_e32 v30, 0x40e00000, v30
	v_pk_mul_f32 v[22:23], v[26:27], v[22:23]
	v_min_f32_e32 v31, 0x40e00000, v31
	v_pk_mul_f32 v[22:23], v[24:25], v[22:23]
	v_pk_fma_f32 v[24:25], v[116:117], s[22:23], v[4:5] op_sel_hi:[1,0,1]
	v_pk_fma_f32 v[28:29], v[112:113], s[22:23], v[0:1] op_sel_hi:[1,0,1]
	v_min_f32_e32 v24, 0x40e00000, v24
	v_min_f32_e32 v25, 0x40e00000, v25
	v_pk_mul_f32 v[26:27], v[24:25], s[24:25] op_sel_hi:[1,0]
	v_pk_mul_f32 v[112:113], v[30:31], s[24:25] op_sel_hi:[1,0]
	v_exp_f32_e32 v26, v26
	v_exp_f32_e32 v27, v27
	v_exp_f32_e32 v112, v112
	v_exp_f32_e32 v113, v113
	v_med3_f32 v28, v28, s78, v204
	v_pk_add_f32 v[26:27], v[26:27], 1.0 op_sel_hi:[1,0]
	v_med3_f32 v29, v29, s78, v204
	v_rcp_f32_e32 v26, v26
	v_rcp_f32_e32 v27, v27
	s_nop 0
	v_pk_mul_f32 v[24:25], v[24:25], v[26:27]
	v_pk_fma_f32 v[26:27], v[28:29], 4.0, 4.0 op_sel_hi:[1,0,0]
	v_pk_fma_f32 v[28:29], v[114:115], s[22:23], v[2:3] op_sel_hi:[1,0,1]
	v_pk_mul_f32 v[24:25], v[26:27], v[24:25]
	v_pk_add_f32 v[26:27], v[112:113], 1.0 op_sel_hi:[1,0]
	v_med3_f32 v28, v28, s78, v204
	v_rcp_f32_e32 v26, v26
	v_rcp_f32_e32 v27, v27
	v_med3_f32 v29, v29, s78, v204
	v_pk_mul_f32 v[26:27], v[30:31], v[26:27]
	v_mov_b32_e32 v245, v165
	v_mov_b32_e32 v244, v165
	v_cvt_pk_fp8_f32 v245, v24, v25
	v_cvt_pk_fp8_f32 v244, v20, v21
	v_pk_fma_f32 v[20:21], v[28:29], 4.0, 4.0 op_sel_hi:[1,0,0]
	v_pk_fma_f32 v[24:25], v[104:105], s[22:23], v[8:9] op_sel_hi:[1,0,1]
	v_pk_mul_f32 v[20:21], v[20:21], v[26:27]
	v_cvt_pk_fp8_f32 v244, v22, v23 op_sel:[0,0,1]
	v_cvt_pk_fp8_f32 v245, v20, v21 op_sel:[0,0,1]
	v_add_u32_e32 v20, 32, v18
	v_ashrrev_i32_e32 v21, 31, v20
	v_lshlrev_b64 v[20:21], 10, v[20:21]
	v_lshl_add_u64 v[20:21], s[14:15], 0, v[20:21]
	v_lshl_add_u64 v[20:21], v[20:21], 0, v[16:17]
	v_pk_fma_f32 v[20:21], v[108:109], s[22:23], v[12:13] op_sel_hi:[1,0,1]
	v_pk_fma_f32 v[26:27], v[110:111], s[22:23], v[14:15] op_sel_hi:[1,0,1]
	v_min_f32_e32 v20, 0x40e00000, v20
	v_min_f32_e32 v21, 0x40e00000, v21
	v_pk_mul_f32 v[22:23], v[20:21], s[24:25] op_sel_hi:[1,0]
	v_min_f32_e32 v26, 0x40e00000, v26
	v_exp_f32_e32 v22, v22
	v_exp_f32_e32 v23, v23
	v_min_f32_e32 v27, 0x40e00000, v27
	v_pk_mul_f32 v[28:29], v[26:27], s[24:25] op_sel_hi:[1,0]
	v_med3_f32 v24, v24, s78, v204
	v_pk_add_f32 v[22:23], v[22:23], 1.0 op_sel_hi:[1,0]
	v_exp_f32_e32 v28, v28
	v_rcp_f32_e32 v22, v22
	v_rcp_f32_e32 v23, v23
	v_exp_f32_e32 v29, v29
	v_med3_f32 v25, v25, s78, v204
	v_pk_fma_f32 v[30:31], v[102:103], s[22:23], v[6:7] op_sel_hi:[1,0,1]
	v_pk_mul_f32 v[20:21], v[20:21], v[22:23]
	v_pk_fma_f32 v[22:23], v[24:25], 4.0, 4.0 op_sel_hi:[1,0,0]
	v_pk_fma_f32 v[24:25], v[106:107], s[22:23], v[10:11] op_sel_hi:[1,0,1]
	v_pk_mul_f32 v[20:21], v[22:23], v[20:21]
	v_pk_add_f32 v[22:23], v[28:29], 1.0 op_sel_hi:[1,0]
	v_med3_f32 v24, v24, s78, v204
	v_rcp_f32_e32 v22, v22
	v_rcp_f32_e32 v23, v23
	v_med3_f32 v25, v25, s78, v204
	v_pk_fma_f32 v[24:25], v[24:25], 4.0, 4.0 op_sel_hi:[1,0,0]
	v_min_f32_e32 v30, 0x40e00000, v30
	v_pk_mul_f32 v[22:23], v[26:27], v[22:23]
	v_min_f32_e32 v31, 0x40e00000, v31
	v_pk_mul_f32 v[22:23], v[24:25], v[22:23]
	v_pk_fma_f32 v[24:25], v[100:101], s[22:23], v[4:5] op_sel_hi:[1,0,1]
	v_pk_fma_f32 v[28:29], v[96:97], s[22:23], v[0:1] op_sel_hi:[1,0,1]
	v_min_f32_e32 v24, 0x40e00000, v24
	v_min_f32_e32 v25, 0x40e00000, v25
	v_pk_mul_f32 v[26:27], v[24:25], s[24:25] op_sel_hi:[1,0]
	v_pk_mul_f32 v[96:97], v[30:31], s[24:25] op_sel_hi:[1,0]
	v_exp_f32_e32 v26, v26
	v_exp_f32_e32 v27, v27
	v_exp_f32_e32 v96, v96
	v_exp_f32_e32 v97, v97
	v_med3_f32 v28, v28, s78, v204
	v_pk_add_f32 v[26:27], v[26:27], 1.0 op_sel_hi:[1,0]
	v_med3_f32 v29, v29, s78, v204
	v_rcp_f32_e32 v26, v26
	v_rcp_f32_e32 v27, v27
	s_nop 0
	v_pk_mul_f32 v[24:25], v[24:25], v[26:27]
	v_pk_fma_f32 v[26:27], v[28:29], 4.0, 4.0 op_sel_hi:[1,0,0]
	v_pk_fma_f32 v[28:29], v[98:99], s[22:23], v[2:3] op_sel_hi:[1,0,1]
	v_pk_mul_f32 v[24:25], v[26:27], v[24:25]
	v_pk_add_f32 v[26:27], v[96:97], 1.0 op_sel_hi:[1,0]
	v_med3_f32 v28, v28, s78, v204
	v_rcp_f32_e32 v26, v26
	v_rcp_f32_e32 v27, v27
	v_med3_f32 v29, v29, s78, v204
	v_pk_mul_f32 v[26:27], v[30:31], v[26:27]
	v_cvt_pk_fp8_f32 v246, v20, v21
	v_cvt_pk_fp8_f32 v247, v24, v25
	v_pk_fma_f32 v[20:21], v[28:29], 4.0, 4.0 op_sel_hi:[1,0,0]
	v_cvt_pk_fp8_f32 v246, v22, v23 op_sel:[0,0,1]
	v_pk_fma_f32 v[22:23], v[92:93], s[22:23], v[12:13] op_sel_hi:[1,0,1]
	v_pk_mul_f32 v[20:21], v[20:21], v[26:27]
	v_min_f32_e32 v22, 0x40e00000, v22
	v_min_f32_e32 v23, 0x40e00000, v23
	v_pk_mul_f32 v[24:25], v[22:23], s[24:25] op_sel_hi:[1,0]
	v_cvt_pk_fp8_f32 v247, v20, v21 op_sel:[0,0,1]
	v_add_u32_e32 v20, 48, v18
	v_exp_f32_e32 v24, v24
	v_exp_f32_e32 v25, v25
	v_ashrrev_i32_e32 v21, 31, v20
	v_lshlrev_b64 v[20:21], 10, v[20:21]
	v_lshl_add_u64 v[20:21], s[14:15], 0, v[20:21]
	v_pk_fma_f32 v[28:29], v[94:95], s[22:23], v[14:15] op_sel_hi:[1,0,1]
	v_lshl_add_u64 v[20:21], v[20:21], 0, v[16:17]
	v_pk_add_f32 v[24:25], v[24:25], 1.0 op_sel_hi:[1,0]
	v_min_f32_e32 v28, 0x40e00000, v28
	v_min_f32_e32 v29, 0x40e00000, v29
	s_nop 1
	v_permlane16_swap_b32_e32 v244, v246
	v_permlane16_swap_b32_e32 v245, v247
	v_lshl_add_u64 v[248:249], v[20:21], 0, v[250:251]
	global_store_dwordx4 v[248:249], v[244:247], off
	s_nop 1
	v_rcp_f32_e32 v24, v24
	v_rcp_f32_e32 v25, v25
	v_pk_mul_f32 v[30:31], v[28:29], s[24:25] op_sel_hi:[1,0]
	v_pk_fma_f32 v[26:27], v[88:89], s[22:23], v[8:9] op_sel_hi:[1,0,1]
	v_exp_f32_e32 v30, v30
	v_exp_f32_e32 v31, v31
	v_med3_f32 v26, v26, s78, v204
	v_med3_f32 v27, v27, s78, v204
	v_pk_mul_f32 v[22:23], v[22:23], v[24:25]
	v_pk_fma_f32 v[24:25], v[26:27], 4.0, 4.0 op_sel_hi:[1,0,0]
	v_pk_fma_f32 v[26:27], v[90:91], s[22:23], v[10:11] op_sel_hi:[1,0,1]
	v_pk_mul_f32 v[22:23], v[24:25], v[22:23]
	v_pk_add_f32 v[24:25], v[30:31], 1.0 op_sel_hi:[1,0]
	v_med3_f32 v26, v26, s78, v204
	v_rcp_f32_e32 v24, v24
	v_rcp_f32_e32 v25, v25
	v_med3_f32 v27, v27, s78, v204
	v_pk_fma_f32 v[26:27], v[26:27], 4.0, 4.0 op_sel_hi:[1,0,0]
	v_pk_fma_f32 v[30:31], v[80:81], s[22:23], v[0:1] op_sel_hi:[1,0,1]
	v_pk_mul_f32 v[24:25], v[28:29], v[24:25]
	v_pk_fma_f32 v[80:81], v[86:87], s[22:23], v[6:7] op_sel_hi:[1,0,1]
	v_pk_mul_f32 v[24:25], v[26:27], v[24:25]
	v_pk_fma_f32 v[26:27], v[84:85], s[22:23], v[4:5] op_sel_hi:[1,0,1]
	v_min_f32_e32 v80, 0x40e00000, v80
	v_min_f32_e32 v26, 0x40e00000, v26
	v_min_f32_e32 v27, 0x40e00000, v27
	v_pk_mul_f32 v[28:29], v[26:27], s[24:25] op_sel_hi:[1,0]
	v_min_f32_e32 v81, 0x40e00000, v81
	v_exp_f32_e32 v28, v28
	v_exp_f32_e32 v29, v29
	v_pk_mul_f32 v[84:85], v[80:81], s[24:25] op_sel_hi:[1,0]
	v_med3_f32 v30, v30, s78, v204
	v_exp_f32_e32 v84, v84
	v_pk_add_f32 v[28:29], v[28:29], 1.0 op_sel_hi:[1,0]
	v_exp_f32_e32 v85, v85
	v_rcp_f32_e32 v28, v28
	v_rcp_f32_e32 v29, v29
	v_med3_f32 v31, v31, s78, v204
	v_add_u32_e32 v20, 0x80, v18
	v_ashrrev_i32_e32 v21, 31, v20
	v_pk_mul_f32 v[26:27], v[26:27], v[28:29]
	v_pk_fma_f32 v[28:29], v[30:31], 4.0, 4.0 op_sel_hi:[1,0,0]
	v_pk_fma_f32 v[30:31], v[82:83], s[22:23], v[2:3] op_sel_hi:[1,0,1]
	v_pk_mul_f32 v[26:27], v[28:29], v[26:27]
	v_pk_add_f32 v[28:29], v[84:85], 1.0 op_sel_hi:[1,0]
	v_med3_f32 v30, v30, s78, v204
	v_rcp_f32_e32 v28, v28
	v_rcp_f32_e32 v29, v29
	v_med3_f32 v31, v31, s78, v204
	v_lshlrev_b64 v[20:21], 10, v[20:21]
	v_lshl_add_u64 v[20:21], s[14:15], 0, v[20:21]
	v_pk_mul_f32 v[28:29], v[80:81], v[28:29]
	v_mov_b32_e32 v244, v165
	v_mov_b32_e32 v245, v165
	v_cvt_pk_fp8_f32 v244, v22, v23
	v_cvt_pk_fp8_f32 v245, v26, v27
	v_pk_fma_f32 v[22:23], v[30:31], 4.0, 4.0 op_sel_hi:[1,0,0]
	v_lshl_add_u64 v[20:21], v[20:21], 0, v[16:17]
	v_pk_mul_f32 v[22:23], v[22:23], v[28:29]
	v_cvt_pk_fp8_f32 v244, v24, v25 op_sel:[0,0,1]
	v_cvt_pk_fp8_f32 v245, v22, v23 op_sel:[0,0,1]
	v_pk_fma_f32 v[26:27], v[78:79], s[22:23], v[14:15] op_sel_hi:[1,0,1]
	v_pk_fma_f32 v[24:25], v[72:73], s[22:23], v[8:9] op_sel_hi:[1,0,1]
	v_min_f32_e32 v26, 0x40e00000, v26
	v_pk_fma_f32 v[20:21], v[76:77], s[22:23], v[12:13] op_sel_hi:[1,0,1]
	v_min_f32_e32 v27, 0x40e00000, v27
	v_min_f32_e32 v20, 0x40e00000, v20
	v_min_f32_e32 v21, 0x40e00000, v21
	v_pk_mul_f32 v[22:23], v[20:21], s[24:25] op_sel_hi:[1,0]
	v_pk_mul_f32 v[28:29], v[26:27], s[24:25] op_sel_hi:[1,0]
	v_exp_f32_e32 v22, v22
	v_exp_f32_e32 v23, v23
	v_exp_f32_e32 v28, v28
	v_exp_f32_e32 v29, v29
	v_med3_f32 v24, v24, s78, v204
	v_pk_add_f32 v[22:23], v[22:23], 1.0 op_sel_hi:[1,0]
	v_med3_f32 v25, v25, s78, v204
	v_rcp_f32_e32 v22, v22
	v_rcp_f32_e32 v23, v23
	v_pk_fma_f32 v[30:31], v[70:71], s[22:23], v[6:7] op_sel_hi:[1,0,1]
	v_pk_mul_f32 v[20:21], v[20:21], v[22:23]
	v_pk_fma_f32 v[22:23], v[24:25], 4.0, 4.0 op_sel_hi:[1,0,0]
	v_pk_fma_f32 v[24:25], v[74:75], s[22:23], v[10:11] op_sel_hi:[1,0,1]
	v_pk_mul_f32 v[20:21], v[22:23], v[20:21]
	v_pk_add_f32 v[22:23], v[28:29], 1.0 op_sel_hi:[1,0]
	v_med3_f32 v24, v24, s78, v204
	v_rcp_f32_e32 v22, v22
	v_rcp_f32_e32 v23, v23
	v_med3_f32 v25, v25, s78, v204
	v_pk_fma_f32 v[24:25], v[24:25], 4.0, 4.0 op_sel_hi:[1,0,0]
	v_min_f32_e32 v30, 0x40e00000, v30
	v_pk_mul_f32 v[22:23], v[26:27], v[22:23]
	v_min_f32_e32 v31, 0x40e00000, v31
	v_pk_mul_f32 v[22:23], v[24:25], v[22:23]
	v_pk_fma_f32 v[24:25], v[68:69], s[22:23], v[4:5] op_sel_hi:[1,0,1]
	v_pk_fma_f32 v[28:29], v[64:65], s[22:23], v[0:1] op_sel_hi:[1,0,1]
	v_min_f32_e32 v24, 0x40e00000, v24
	v_min_f32_e32 v25, 0x40e00000, v25
	v_pk_mul_f32 v[26:27], v[24:25], s[24:25] op_sel_hi:[1,0]
	v_pk_mul_f32 v[64:65], v[30:31], s[24:25] op_sel_hi:[1,0]
	v_exp_f32_e32 v26, v26
	v_exp_f32_e32 v27, v27
	v_exp_f32_e32 v64, v64
	v_exp_f32_e32 v65, v65
	v_med3_f32 v28, v28, s78, v204
	v_pk_add_f32 v[26:27], v[26:27], 1.0 op_sel_hi:[1,0]
	v_med3_f32 v29, v29, s78, v204
	v_rcp_f32_e32 v26, v26
	v_rcp_f32_e32 v27, v27
	s_nop 0
	v_pk_mul_f32 v[24:25], v[24:25], v[26:27]
	v_pk_fma_f32 v[26:27], v[28:29], 4.0, 4.0 op_sel_hi:[1,0,0]
	v_pk_fma_f32 v[28:29], v[66:67], s[22:23], v[2:3] op_sel_hi:[1,0,1]
	v_pk_mul_f32 v[24:25], v[26:27], v[24:25]
	v_pk_add_f32 v[26:27], v[64:65], 1.0 op_sel_hi:[1,0]
	v_med3_f32 v28, v28, s78, v204
	v_rcp_f32_e32 v26, v26
	v_rcp_f32_e32 v27, v27
	v_med3_f32 v29, v29, s78, v204
	v_pk_mul_f32 v[26:27], v[30:31], v[26:27]
	v_cvt_pk_fp8_f32 v247, v24, v25
	v_cvt_pk_fp8_f32 v246, v20, v21
	v_pk_fma_f32 v[20:21], v[28:29], 4.0, 4.0 op_sel_hi:[1,0,0]
	v_pk_fma_f32 v[24:25], v[56:57], s[22:23], v[8:9] op_sel_hi:[1,0,1]
	v_pk_mul_f32 v[20:21], v[20:21], v[26:27]
	v_cvt_pk_fp8_f32 v246, v22, v23 op_sel:[0,0,1]
	v_cvt_pk_fp8_f32 v247, v20, v21 op_sel:[0,0,1]
	v_add_u32_e32 v20, 0x90, v18
	v_ashrrev_i32_e32 v21, 31, v20
	v_lshlrev_b64 v[20:21], 10, v[20:21]
	v_lshl_add_u64 v[20:21], s[14:15], 0, v[20:21]
	v_lshl_add_u64 v[20:21], v[20:21], 0, v[16:17]
	s_nop 1
	v_permlane16_swap_b32_e32 v244, v246
	v_permlane16_swap_b32_e32 v245, v247
	v_lshl_add_u64 v[248:249], v[20:21], 0, v[250:251]
	global_store_dwordx4 v[248:249], v[244:247], off
	s_nop 1
	v_pk_fma_f32 v[20:21], v[60:61], s[22:23], v[12:13] op_sel_hi:[1,0,1]
	v_pk_fma_f32 v[26:27], v[62:63], s[22:23], v[14:15] op_sel_hi:[1,0,1]
	v_min_f32_e32 v20, 0x40e00000, v20
	v_min_f32_e32 v21, 0x40e00000, v21
	v_pk_mul_f32 v[22:23], v[20:21], s[24:25] op_sel_hi:[1,0]
	v_min_f32_e32 v26, 0x40e00000, v26
	v_exp_f32_e32 v22, v22
	v_exp_f32_e32 v23, v23
	v_min_f32_e32 v27, 0x40e00000, v27
	v_pk_mul_f32 v[28:29], v[26:27], s[24:25] op_sel_hi:[1,0]
	v_med3_f32 v24, v24, s78, v204
	v_pk_add_f32 v[22:23], v[22:23], 1.0 op_sel_hi:[1,0]
	v_exp_f32_e32 v28, v28
	v_rcp_f32_e32 v22, v22
	v_rcp_f32_e32 v23, v23
	v_exp_f32_e32 v29, v29
	v_med3_f32 v25, v25, s78, v204
	v_pk_fma_f32 v[30:31], v[54:55], s[22:23], v[6:7] op_sel_hi:[1,0,1]
	v_pk_mul_f32 v[20:21], v[20:21], v[22:23]
	v_pk_fma_f32 v[22:23], v[24:25], 4.0, 4.0 op_sel_hi:[1,0,0]
	v_pk_fma_f32 v[24:25], v[58:59], s[22:23], v[10:11] op_sel_hi:[1,0,1]
	v_pk_mul_f32 v[20:21], v[22:23], v[20:21]
	v_pk_add_f32 v[22:23], v[28:29], 1.0 op_sel_hi:[1,0]
	v_med3_f32 v24, v24, s78, v204
	v_rcp_f32_e32 v22, v22
	v_rcp_f32_e32 v23, v23
	v_med3_f32 v25, v25, s78, v204
	v_pk_fma_f32 v[24:25], v[24:25], 4.0, 4.0 op_sel_hi:[1,0,0]
	v_min_f32_e32 v30, 0x40e00000, v30
	v_pk_mul_f32 v[22:23], v[26:27], v[22:23]
	v_min_f32_e32 v31, 0x40e00000, v31
	v_pk_mul_f32 v[22:23], v[24:25], v[22:23]
	v_pk_fma_f32 v[24:25], v[52:53], s[22:23], v[4:5] op_sel_hi:[1,0,1]
	v_pk_fma_f32 v[28:29], v[48:49], s[22:23], v[0:1] op_sel_hi:[1,0,1]
	v_min_f32_e32 v24, 0x40e00000, v24
	v_min_f32_e32 v25, 0x40e00000, v25
	v_pk_mul_f32 v[26:27], v[24:25], s[24:25] op_sel_hi:[1,0]
	v_pk_mul_f32 v[48:49], v[30:31], s[24:25] op_sel_hi:[1,0]
	v_exp_f32_e32 v26, v26
	v_exp_f32_e32 v27, v27
	v_exp_f32_e32 v48, v48
	v_exp_f32_e32 v49, v49
	v_med3_f32 v28, v28, s78, v204
	v_pk_add_f32 v[26:27], v[26:27], 1.0 op_sel_hi:[1,0]
	v_med3_f32 v29, v29, s78, v204
	v_rcp_f32_e32 v26, v26
	v_rcp_f32_e32 v27, v27
	v_pk_fma_f32 v[12:13], v[44:45], s[22:23], v[12:13] op_sel_hi:[1,0,1]
	v_pk_fma_f32 v[14:15], v[46:47], s[22:23], v[14:15] op_sel_hi:[1,0,1]
	v_min_f32_e32 v12, 0x40e00000, v12
	v_pk_mul_f32 v[24:25], v[24:25], v[26:27]
	v_pk_fma_f32 v[26:27], v[28:29], 4.0, 4.0 op_sel_hi:[1,0,0]
	v_pk_fma_f32 v[28:29], v[50:51], s[22:23], v[2:3] op_sel_hi:[1,0,1]
	v_pk_mul_f32 v[24:25], v[26:27], v[24:25]
	v_pk_add_f32 v[26:27], v[48:49], 1.0 op_sel_hi:[1,0]
	v_med3_f32 v28, v28, s78, v204
	v_rcp_f32_e32 v26, v26
	v_rcp_f32_e32 v27, v27
	v_med3_f32 v29, v29, s78, v204
	v_min_f32_e32 v13, 0x40e00000, v13
	v_min_f32_e32 v14, 0x40e00000, v14
	v_pk_mul_f32 v[26:27], v[30:31], v[26:27]
	v_mov_b32_e32 v245, v165
	v_mov_b32_e32 v244, v165
	v_cvt_pk_fp8_f32 v245, v24, v25
	v_cvt_pk_fp8_f32 v244, v20, v21
	v_pk_fma_f32 v[20:21], v[28:29], 4.0, 4.0 op_sel_hi:[1,0,0]
	v_min_f32_e32 v15, 0x40e00000, v15
	v_pk_mul_f32 v[20:21], v[20:21], v[26:27]
	v_cvt_pk_fp8_f32 v244, v22, v23 op_sel:[0,0,1]
	v_cvt_pk_fp8_f32 v245, v20, v21 op_sel:[0,0,1]
	v_add_u32_e32 v20, 0xa0, v18
	v_ashrrev_i32_e32 v21, 31, v20
	v_lshlrev_b64 v[20:21], 10, v[20:21]
	v_lshl_add_u64 v[20:21], s[14:15], 0, v[20:21]
	v_lshl_add_u64 v[20:21], v[20:21], 0, v[16:17]
	v_pk_mul_f32 v[20:21], v[12:13], s[24:25] op_sel_hi:[1,0]
	v_pk_mul_f32 v[22:23], v[14:15], s[24:25] op_sel_hi:[1,0]
	v_exp_f32_e32 v20, v20
	v_exp_f32_e32 v21, v21
	v_exp_f32_e32 v22, v22
	v_exp_f32_e32 v23, v23
	v_pk_fma_f32 v[8:9], v[40:41], s[22:23], v[8:9] op_sel_hi:[1,0,1]
	v_pk_add_f32 v[20:21], v[20:21], 1.0 op_sel_hi:[1,0]
	v_med3_f32 v8, v8, s78, v204
	v_rcp_f32_e32 v20, v20
	v_rcp_f32_e32 v21, v21
	v_med3_f32 v9, v9, s78, v204
	v_pk_fma_f32 v[8:9], v[8:9], 4.0, 4.0 op_sel_hi:[1,0,0]
	v_pk_fma_f32 v[10:11], v[42:43], s[22:23], v[10:11] op_sel_hi:[1,0,1]
	v_pk_mul_f32 v[12:13], v[12:13], v[20:21]
	v_med3_f32 v10, v10, s78, v204
	v_pk_mul_f32 v[8:9], v[8:9], v[12:13]
	v_pk_add_f32 v[12:13], v[22:23], 1.0 op_sel_hi:[1,0]
	v_med3_f32 v11, v11, s78, v204
	v_rcp_f32_e32 v12, v12
	v_rcp_f32_e32 v13, v13
	v_pk_fma_f32 v[4:5], v[36:37], s[22:23], v[4:5] op_sel_hi:[1,0,1]
	v_pk_fma_f32 v[10:11], v[10:11], 4.0, 4.0 op_sel_hi:[1,0,0]
	v_min_f32_e32 v4, 0x40e00000, v4
	v_pk_mul_f32 v[12:13], v[14:15], v[12:13]
	v_min_f32_e32 v5, 0x40e00000, v5
	v_pk_mul_f32 v[10:11], v[10:11], v[12:13]
	v_pk_mul_f32 v[12:13], v[4:5], s[24:25] op_sel_hi:[1,0]
	v_pk_fma_f32 v[6:7], v[38:39], s[22:23], v[6:7] op_sel_hi:[1,0,1]
	v_exp_f32_e32 v12, v12
	v_exp_f32_e32 v13, v13
	v_min_f32_e32 v6, 0x40e00000, v6
	v_min_f32_e32 v7, 0x40e00000, v7
	v_pk_mul_f32 v[14:15], v[6:7], s[24:25] op_sel_hi:[1,0]
	v_pk_add_f32 v[12:13], v[12:13], 1.0 op_sel_hi:[1,0]
	v_exp_f32_e32 v14, v14
	v_rcp_f32_e32 v12, v12
	v_rcp_f32_e32 v13, v13
	v_exp_f32_e32 v15, v15
	v_pk_fma_f32 v[0:1], v[32:33], s[22:23], v[0:1] op_sel_hi:[1,0,1]
	v_pk_fma_f32 v[2:3], v[34:35], s[22:23], v[2:3] op_sel_hi:[1,0,1]
	v_med3_f32 v0, v0, s78, v204
	v_med3_f32 v1, v1, s78, v204
	v_pk_mul_f32 v[4:5], v[4:5], v[12:13]
	v_pk_fma_f32 v[0:1], v[0:1], 4.0, 4.0 op_sel_hi:[1,0,0]
	v_med3_f32 v2, v2, s78, v204
	v_pk_mul_f32 v[0:1], v[0:1], v[4:5]
	v_pk_add_f32 v[4:5], v[14:15], 1.0 op_sel_hi:[1,0]
	v_med3_f32 v3, v3, s78, v204
	v_rcp_f32_e32 v4, v4
	v_rcp_f32_e32 v5, v5
	s_nop 0
	v_pk_mul_f32 v[4:5], v[6:7], v[4:5]
	v_cvt_pk_fp8_f32 v247, v0, v1
	v_cvt_pk_fp8_f32 v246, v8, v9
	v_pk_fma_f32 v[0:1], v[2:3], 4.0, 4.0 op_sel_hi:[1,0,0]
	v_cvt_pk_fp8_f32 v246, v10, v11 op_sel:[0,0,1]
	v_pk_mul_f32 v[0:1], v[0:1], v[4:5]
	s_nop 0
	v_cvt_pk_fp8_f32 v247, v0, v1 op_sel:[0,0,1]
	v_add_u32_e32 v0, 0xb0, v18
	v_ashrrev_i32_e32 v1, 31, v0
	v_lshlrev_b64 v[0:1], 10, v[0:1]
	v_lshl_add_u64 v[0:1], s[14:15], 0, v[0:1]
	v_lshl_add_u64 v[0:1], v[0:1], 0, v[16:17]
	s_nop 1
	v_permlane16_swap_b32_e32 v244, v246
	v_permlane16_swap_b32_e32 v245, v247
	v_lshl_add_u64 v[248:249], v[0:1], 0, v[250:251]
	global_store_dwordx4 v[248:249], v[244:247], off
	s_nop 1
	s_cbranch_vccnz .LBB0_1700
	s_andn2_b64 vcc, exec, s[12:13]
	s_cbranch_vccnz .LBB0_1699
	s_barrier
	s_branch .LBB0_1699

.LBB0_1796:
	s_lshl_b32 s27, s81, 10
	s_and_b32 s27, s27, 0x400
	v_mov_b32_e32 v17, v171
	v_mov_b32_e32 v16, v204
	s_add_i32 s27, s67, s27
	s_and_b64 vcc, exec, s[2:3]
	v_lshl_add_u32 v0, v16, 5, s27
	s_lshl_b32 s27, s80, 8
	s_or_b32 s27, s27, s66
	ds_read_b128 v[12:15], v0
	ds_read_b128 v[8:11], v0 offset:16
	ds_read_b128 v[4:7], v0 offset:512
	ds_read_b128 v[0:3], v0 offset:528
	v_lshl_add_u32 v16, v16, 3, s27
	s_lshl_b32 s27, s79, 8
	s_add_i32 s27, s27, s68
	v_add_u32_e32 v18, s27, v17
	s_waitcnt lgkmcnt(0)
	v_pk_fma_f32 v[22:23], v[158:159], s[22:23], v[14:15] op_sel_hi:[1,0,1]
	v_pk_fma_f32 v[24:25], v[156:157], s[22:23], v[12:13] op_sel_hi:[1,0,1]
	v_ashrrev_i32_e32 v19, 31, v18
	v_pk_mul_f32 v[22:23], v[22:23], s[24:25] op_sel_hi:[1,0]
	v_pk_mul_f32 v[24:25], v[24:25], s[24:25] op_sel_hi:[1,0]
	v_pk_fma_f32 v[28:29], v[152:153], s[22:23], v[8:9] op_sel_hi:[1,0,1]
	v_lshlrev_b64 v[20:21], 10, v[18:19]
	v_pk_mul_f32 v[28:29], v[28:29], s[24:25] op_sel_hi:[1,0]
	v_med3_f32 v19, v24, s75, v210
	v_med3_f32 v24, v25, s75, v210
	v_med3_f32 v25, v22, s75, v210
	v_med3_f32 v30, v23, s75, v210
	v_cvt_pk_fp8_f32 v22, v19, v24
	v_med3_f32 v19, v28, s75, v210
	v_med3_f32 v24, v29, s75, v210
	v_cvt_pk_fp8_f32 v23, v19, v24
	v_pk_fma_f32 v[26:27], v[154:155], s[22:23], v[10:11] op_sel_hi:[1,0,1]
	v_cvt_pk_fp8_f32 v22, v25, v30 op_sel:[0,0,1]
	v_pk_mul_f32 v[26:27], v[26:27], s[24:25] op_sel_hi:[1,0]
	v_pk_fma_f32 v[30:31], v[144:145], s[22:23], v[0:1] op_sel_hi:[1,0,1]
	v_med3_f32 v19, v26, s75, v210
	v_med3_f32 v24, v27, s75, v210
	v_cvt_pk_fp8_f32 v23, v19, v24 op_sel:[0,0,1]
	v_pk_fma_f32 v[24:25], v[150:151], s[22:23], v[6:7] op_sel_hi:[1,0,1]
	v_pk_fma_f32 v[26:27], v[148:149], s[22:23], v[4:5] op_sel_hi:[1,0,1]
	v_pk_mul_f32 v[24:25], v[24:25], s[24:25] op_sel_hi:[1,0]
	v_pk_mul_f32 v[26:27], v[26:27], s[24:25] op_sel_hi:[1,0]
	v_pk_mul_f32 v[30:31], v[30:31], s[24:25] op_sel_hi:[1,0]
	v_med3_f32 v19, v26, s75, v210
	v_med3_f32 v26, v27, s75, v210
	v_med3_f32 v27, v24, s75, v210
	v_med3_f32 v144, v25, s75, v210
	v_cvt_pk_fp8_f32 v24, v19, v26
	v_med3_f32 v19, v30, s75, v210
	v_med3_f32 v26, v31, s75, v210
	v_cvt_pk_fp8_f32 v25, v19, v26
	v_pk_fma_f32 v[28:29], v[146:147], s[22:23], v[2:3] op_sel_hi:[1,0,1]
	v_cvt_pk_fp8_f32 v24, v27, v144 op_sel:[0,0,1]
	v_pk_mul_f32 v[28:29], v[28:29], s[24:25] op_sel_hi:[1,0]
	v_ashrrev_i32_e32 v17, 31, v16
	v_med3_f32 v19, v28, s75, v210
	v_med3_f32 v26, v29, s75, v210
	v_cvt_pk_fp8_f32 v25, v19, v26 op_sel:[0,0,1]
	v_lshl_add_u64 v[20:21], s[12:13], 0, v[20:21]
	v_lshl_add_u64 v[20:21], v[20:21], 0, v[16:17]
	s_nop 1
	v_permlane16_swap_b32_e32 v22, v24
	v_permlane16_swap_b32_e32 v23, v25
	v_lshl_add_u64 v[248:249], v[20:21], 0, v[250:251]
	global_store_dwordx4 v[248:249], v[22:25], off
	s_nop 1
	v_pk_fma_f32 v[22:23], v[142:143], s[22:23], v[14:15] op_sel_hi:[1,0,1]
	v_pk_fma_f32 v[24:25], v[140:141], s[22:23], v[12:13] op_sel_hi:[1,0,1]
	v_pk_mul_f32 v[22:23], v[22:23], s[24:25] op_sel_hi:[1,0]
	v_pk_mul_f32 v[24:25], v[24:25], s[24:25] op_sel_hi:[1,0]
	v_pk_fma_f32 v[28:29], v[136:137], s[22:23], v[8:9] op_sel_hi:[1,0,1]
	v_med3_f32 v19, v24, s75, v210
	v_pk_mul_f32 v[28:29], v[28:29], s[24:25] op_sel_hi:[1,0]
	v_med3_f32 v24, v25, s75, v210
	v_med3_f32 v25, v22, s75, v210
	v_med3_f32 v30, v23, s75, v210
	v_cvt_pk_fp8_f32 v22, v19, v24
	v_med3_f32 v19, v28, s75, v210
	v_med3_f32 v24, v29, s75, v210
	v_cvt_pk_fp8_f32 v23, v19, v24
	v_pk_fma_f32 v[26:27], v[138:139], s[22:23], v[10:11] op_sel_hi:[1,0,1]
	v_cvt_pk_fp8_f32 v22, v25, v30 op_sel:[0,0,1]
	v_pk_mul_f32 v[26:27], v[26:27], s[24:25] op_sel_hi:[1,0]
	v_pk_fma_f32 v[30:31], v[128:129], s[22:23], v[0:1] op_sel_hi:[1,0,1]
	v_med3_f32 v19, v26, s75, v210
	v_med3_f32 v24, v27, s75, v210
	v_cvt_pk_fp8_f32 v23, v19, v24 op_sel:[0,0,1]
	v_pk_fma_f32 v[24:25], v[134:135], s[22:23], v[6:7] op_sel_hi:[1,0,1]
	v_pk_fma_f32 v[26:27], v[132:133], s[22:23], v[4:5] op_sel_hi:[1,0,1]
	v_pk_mul_f32 v[24:25], v[24:25], s[24:25] op_sel_hi:[1,0]
	v_pk_mul_f32 v[26:27], v[26:27], s[24:25] op_sel_hi:[1,0]
	v_pk_mul_f32 v[30:31], v[30:31], s[24:25] op_sel_hi:[1,0]
	v_med3_f32 v19, v26, s75, v210
	v_med3_f32 v26, v27, s75, v210
	v_med3_f32 v27, v24, s75, v210
	v_med3_f32 v128, v25, s75, v210
	v_cvt_pk_fp8_f32 v24, v19, v26
	v_med3_f32 v19, v30, s75, v210
	v_med3_f32 v26, v31, s75, v210
	v_cvt_pk_fp8_f32 v25, v19, v26
	v_pk_fma_f32 v[28:29], v[130:131], s[22:23], v[2:3] op_sel_hi:[1,0,1]
	v_add_u32_e32 v20, 16, v18
	v_pk_mul_f32 v[28:29], v[28:29], s[24:25] op_sel_hi:[1,0]
	v_ashrrev_i32_e32 v21, 31, v20
	v_med3_f32 v19, v28, s75, v210
	v_med3_f32 v26, v29, s75, v210
	v_lshlrev_b64 v[20:21], 10, v[20:21]
	v_cvt_pk_fp8_f32 v24, v27, v128 op_sel:[0,0,1]
	v_cvt_pk_fp8_f32 v25, v19, v26 op_sel:[0,0,1]
	v_lshl_add_u64 v[20:21], s[12:13], 0, v[20:21]
	v_lshl_add_u64 v[20:21], v[20:21], 0, v[16:17]
	s_nop 1
	v_permlane16_swap_b32_e32 v22, v24
	v_permlane16_swap_b32_e32 v23, v25
	v_lshl_add_u64 v[248:249], v[20:21], 0, v[250:251]
	global_store_dwordx4 v[248:249], v[22:25], off
	s_nop 1
	v_pk_fma_f32 v[22:23], v[126:127], s[22:23], v[14:15] op_sel_hi:[1,0,1]
	v_pk_fma_f32 v[24:25], v[124:125], s[22:23], v[12:13] op_sel_hi:[1,0,1]
	v_pk_mul_f32 v[22:23], v[22:23], s[24:25] op_sel_hi:[1,0]
	v_pk_mul_f32 v[24:25], v[24:25], s[24:25] op_sel_hi:[1,0]
	v_pk_fma_f32 v[28:29], v[120:121], s[22:23], v[8:9] op_sel_hi:[1,0,1]
	v_med3_f32 v19, v24, s75, v210
	v_pk_mul_f32 v[28:29], v[28:29], s[24:25] op_sel_hi:[1,0]
	v_med3_f32 v24, v25, s75, v210
	v_med3_f32 v25, v22, s75, v210
	v_med3_f32 v30, v23, s75, v210
	v_cvt_pk_fp8_f32 v22, v19, v24
	v_med3_f32 v19, v28, s75, v210
	v_med3_f32 v24, v29, s75, v210
	v_cvt_pk_fp8_f32 v23, v19, v24
	v_pk_fma_f32 v[26:27], v[122:123], s[22:23], v[10:11] op_sel_hi:[1,0,1]
	v_cvt_pk_fp8_f32 v22, v25, v30 op_sel:[0,0,1]
	v_pk_mul_f32 v[26:27], v[26:27], s[24:25] op_sel_hi:[1,0]
	v_pk_fma_f32 v[30:31], v[112:113], s[22:23], v[0:1] op_sel_hi:[1,0,1]
	v_med3_f32 v19, v26, s75, v210
	v_med3_f32 v24, v27, s75, v210
	v_cvt_pk_fp8_f32 v23, v19, v24 op_sel:[0,0,1]
	v_pk_fma_f32 v[24:25], v[118:119], s[22:23], v[6:7] op_sel_hi:[1,0,1]
	v_pk_fma_f32 v[26:27], v[116:117], s[22:23], v[4:5] op_sel_hi:[1,0,1]
	v_pk_mul_f32 v[24:25], v[24:25], s[24:25] op_sel_hi:[1,0]
	v_pk_mul_f32 v[26:27], v[26:27], s[24:25] op_sel_hi:[1,0]
	v_pk_mul_f32 v[30:31], v[30:31], s[24:25] op_sel_hi:[1,0]
	v_med3_f32 v19, v26, s75, v210
	v_med3_f32 v26, v27, s75, v210
	v_med3_f32 v27, v24, s75, v210
	v_med3_f32 v112, v25, s75, v210
	v_cvt_pk_fp8_f32 v24, v19, v26
	v_med3_f32 v19, v30, s75, v210
	v_med3_f32 v26, v31, s75, v210
	v_cvt_pk_fp8_f32 v25, v19, v26
	v_pk_fma_f32 v[28:29], v[114:115], s[22:23], v[2:3] op_sel_hi:[1,0,1]
	v_add_u32_e32 v20, 32, v18
	v_pk_mul_f32 v[28:29], v[28:29], s[24:25] op_sel_hi:[1,0]
	v_ashrrev_i32_e32 v21, 31, v20
	v_med3_f32 v19, v28, s75, v210
	v_med3_f32 v26, v29, s75, v210
	v_lshlrev_b64 v[20:21], 10, v[20:21]
	v_cvt_pk_fp8_f32 v24, v27, v112 op_sel:[0,0,1]
	v_cvt_pk_fp8_f32 v25, v19, v26 op_sel:[0,0,1]
	v_lshl_add_u64 v[20:21], s[12:13], 0, v[20:21]
	v_lshl_add_u64 v[20:21], v[20:21], 0, v[16:17]
	s_nop 1
	v_permlane16_swap_b32_e32 v22, v24
	v_permlane16_swap_b32_e32 v23, v25
	v_lshl_add_u64 v[248:249], v[20:21], 0, v[250:251]
	global_store_dwordx4 v[248:249], v[22:25], off
	s_nop 1
	v_pk_fma_f32 v[22:23], v[110:111], s[22:23], v[14:15] op_sel_hi:[1,0,1]
	v_pk_fma_f32 v[24:25], v[108:109], s[22:23], v[12:13] op_sel_hi:[1,0,1]
	v_pk_mul_f32 v[22:23], v[22:23], s[24:25] op_sel_hi:[1,0]
	v_pk_mul_f32 v[24:25], v[24:25], s[24:25] op_sel_hi:[1,0]
	v_pk_fma_f32 v[28:29], v[104:105], s[22:23], v[8:9] op_sel_hi:[1,0,1]
	v_med3_f32 v19, v24, s75, v210
	v_pk_mul_f32 v[28:29], v[28:29], s[24:25] op_sel_hi:[1,0]
	v_med3_f32 v24, v25, s75, v210
	v_med3_f32 v25, v22, s75, v210
	v_med3_f32 v30, v23, s75, v210
	v_cvt_pk_fp8_f32 v22, v19, v24
	v_med3_f32 v19, v28, s75, v210
	v_med3_f32 v24, v29, s75, v210
	v_cvt_pk_fp8_f32 v23, v19, v24
	v_pk_fma_f32 v[26:27], v[106:107], s[22:23], v[10:11] op_sel_hi:[1,0,1]
	v_cvt_pk_fp8_f32 v22, v25, v30 op_sel:[0,0,1]
	v_pk_mul_f32 v[26:27], v[26:27], s[24:25] op_sel_hi:[1,0]
	v_pk_fma_f32 v[30:31], v[96:97], s[22:23], v[0:1] op_sel_hi:[1,0,1]
	v_med3_f32 v19, v26, s75, v210
	v_med3_f32 v24, v27, s75, v210
	v_cvt_pk_fp8_f32 v23, v19, v24 op_sel:[0,0,1]
	v_pk_fma_f32 v[24:25], v[102:103], s[22:23], v[6:7] op_sel_hi:[1,0,1]
	v_pk_fma_f32 v[26:27], v[100:101], s[22:23], v[4:5] op_sel_hi:[1,0,1]
	v_pk_mul_f32 v[24:25], v[24:25], s[24:25] op_sel_hi:[1,0]
	v_pk_mul_f32 v[26:27], v[26:27], s[24:25] op_sel_hi:[1,0]
	v_pk_mul_f32 v[30:31], v[30:31], s[24:25] op_sel_hi:[1,0]
	v_med3_f32 v19, v26, s75, v210
	v_med3_f32 v26, v27, s75, v210
	v_med3_f32 v27, v24, s75, v210
	v_med3_f32 v96, v25, s75, v210
	v_cvt_pk_fp8_f32 v24, v19, v26
	v_med3_f32 v19, v30, s75, v210
	v_med3_f32 v26, v31, s75, v210
	v_cvt_pk_fp8_f32 v25, v19, v26
	v_pk_fma_f32 v[28:29], v[98:99], s[22:23], v[2:3] op_sel_hi:[1,0,1]
	v_add_u32_e32 v20, 48, v18
	v_pk_mul_f32 v[28:29], v[28:29], s[24:25] op_sel_hi:[1,0]
	v_ashrrev_i32_e32 v21, 31, v20
	v_med3_f32 v19, v28, s75, v210
	v_med3_f32 v26, v29, s75, v210
	v_lshlrev_b64 v[20:21], 10, v[20:21]
	v_cvt_pk_fp8_f32 v24, v27, v96 op_sel:[0,0,1]
	v_cvt_pk_fp8_f32 v25, v19, v26 op_sel:[0,0,1]
	v_lshl_add_u64 v[20:21], s[12:13], 0, v[20:21]
	v_lshl_add_u64 v[20:21], v[20:21], 0, v[16:17]
	s_nop 1
	v_permlane16_swap_b32_e32 v22, v24
	v_permlane16_swap_b32_e32 v23, v25
	v_lshl_add_u64 v[248:249], v[20:21], 0, v[250:251]
	global_store_dwordx4 v[248:249], v[22:25], off
	s_nop 1
	v_pk_fma_f32 v[22:23], v[94:95], s[22:23], v[14:15] op_sel_hi:[1,0,1]
	v_pk_fma_f32 v[24:25], v[92:93], s[22:23], v[12:13] op_sel_hi:[1,0,1]
	v_pk_mul_f32 v[22:23], v[22:23], s[24:25] op_sel_hi:[1,0]
	v_pk_mul_f32 v[24:25], v[24:25], s[24:25] op_sel_hi:[1,0]
	v_pk_fma_f32 v[28:29], v[88:89], s[22:23], v[8:9] op_sel_hi:[1,0,1]
	v_med3_f32 v19, v24, s75, v210
	v_pk_mul_f32 v[28:29], v[28:29], s[24:25] op_sel_hi:[1,0]
	v_med3_f32 v24, v25, s75, v210
	v_med3_f32 v25, v22, s75, v210
	v_med3_f32 v30, v23, s75, v210
	v_cvt_pk_fp8_f32 v22, v19, v24
	v_med3_f32 v19, v28, s75, v210
	v_med3_f32 v24, v29, s75, v210
	v_cvt_pk_fp8_f32 v23, v19, v24
	v_pk_fma_f32 v[26:27], v[90:91], s[22:23], v[10:11] op_sel_hi:[1,0,1]
	v_cvt_pk_fp8_f32 v22, v25, v30 op_sel:[0,0,1]
	v_pk_mul_f32 v[26:27], v[26:27], s[24:25] op_sel_hi:[1,0]
	v_pk_fma_f32 v[30:31], v[80:81], s[22:23], v[0:1] op_sel_hi:[1,0,1]
	v_med3_f32 v19, v26, s75, v210
	v_med3_f32 v24, v27, s75, v210
	v_cvt_pk_fp8_f32 v23, v19, v24 op_sel:[0,0,1]
	v_pk_fma_f32 v[24:25], v[86:87], s[22:23], v[6:7] op_sel_hi:[1,0,1]
	v_pk_fma_f32 v[26:27], v[84:85], s[22:23], v[4:5] op_sel_hi:[1,0,1]
	v_pk_mul_f32 v[24:25], v[24:25], s[24:25] op_sel_hi:[1,0]
	v_pk_mul_f32 v[26:27], v[26:27], s[24:25] op_sel_hi:[1,0]
	v_pk_mul_f32 v[30:31], v[30:31], s[24:25] op_sel_hi:[1,0]
	v_med3_f32 v19, v26, s75, v210
	v_med3_f32 v26, v27, s75, v210
	v_med3_f32 v27, v24, s75, v210
	v_med3_f32 v80, v25, s75, v210
	v_cvt_pk_fp8_f32 v24, v19, v26
	v_med3_f32 v19, v30, s75, v210
	v_med3_f32 v26, v31, s75, v210
	v_cvt_pk_fp8_f32 v25, v19, v26
	v_pk_fma_f32 v[28:29], v[82:83], s[22:23], v[2:3] op_sel_hi:[1,0,1]
	v_add_u32_e32 v20, 0x80, v18
	v_pk_mul_f32 v[28:29], v[28:29], s[24:25] op_sel_hi:[1,0]
	v_ashrrev_i32_e32 v21, 31, v20
	v_med3_f32 v19, v28, s75, v210
	v_med3_f32 v26, v29, s75, v210
	v_lshlrev_b64 v[20:21], 10, v[20:21]
	v_cvt_pk_fp8_f32 v24, v27, v80 op_sel:[0,0,1]
	v_cvt_pk_fp8_f32 v25, v19, v26 op_sel:[0,0,1]
	v_lshl_add_u64 v[20:21], s[12:13], 0, v[20:21]
	v_lshl_add_u64 v[20:21], v[20:21], 0, v[16:17]
	s_nop 1
	v_permlane16_swap_b32_e32 v22, v24
	v_permlane16_swap_b32_e32 v23, v25
	v_lshl_add_u64 v[248:249], v[20:21], 0, v[250:251]
	global_store_dwordx4 v[248:249], v[22:25], off
	s_nop 1
	v_pk_fma_f32 v[22:23], v[78:79], s[22:23], v[14:15] op_sel_hi:[1,0,1]
	v_pk_fma_f32 v[24:25], v[76:77], s[22:23], v[12:13] op_sel_hi:[1,0,1]
	v_pk_mul_f32 v[22:23], v[22:23], s[24:25] op_sel_hi:[1,0]
	v_pk_mul_f32 v[24:25], v[24:25], s[24:25] op_sel_hi:[1,0]
	v_pk_fma_f32 v[28:29], v[72:73], s[22:23], v[8:9] op_sel_hi:[1,0,1]
	v_med3_f32 v19, v24, s75, v210
	v_pk_mul_f32 v[28:29], v[28:29], s[24:25] op_sel_hi:[1,0]
	v_med3_f32 v24, v25, s75, v210
	v_med3_f32 v25, v22, s75, v210
	v_med3_f32 v30, v23, s75, v210
	v_cvt_pk_fp8_f32 v22, v19, v24
	v_med3_f32 v19, v28, s75, v210
	v_med3_f32 v24, v29, s75, v210
	v_cvt_pk_fp8_f32 v23, v19, v24
	v_pk_fma_f32 v[26:27], v[74:75], s[22:23], v[10:11] op_sel_hi:[1,0,1]
	v_cvt_pk_fp8_f32 v22, v25, v30 op_sel:[0,0,1]
	v_pk_mul_f32 v[26:27], v[26:27], s[24:25] op_sel_hi:[1,0]
	v_pk_fma_f32 v[30:31], v[64:65], s[22:23], v[0:1] op_sel_hi:[1,0,1]
	v_med3_f32 v19, v26, s75, v210
	v_med3_f32 v24, v27, s75, v210
	v_cvt_pk_fp8_f32 v23, v19, v24 op_sel:[0,0,1]
	v_pk_fma_f32 v[24:25], v[70:71], s[22:23], v[6:7] op_sel_hi:[1,0,1]
	v_pk_fma_f32 v[26:27], v[68:69], s[22:23], v[4:5] op_sel_hi:[1,0,1]
	v_pk_mul_f32 v[24:25], v[24:25], s[24:25] op_sel_hi:[1,0]
	v_pk_mul_f32 v[26:27], v[26:27], s[24:25] op_sel_hi:[1,0]
	v_pk_mul_f32 v[30:31], v[30:31], s[24:25] op_sel_hi:[1,0]
	v_med3_f32 v19, v26, s75, v210
	v_med3_f32 v26, v27, s75, v210
	v_med3_f32 v27, v24, s75, v210
	v_med3_f32 v64, v25, s75, v210
	v_cvt_pk_fp8_f32 v24, v19, v26
	v_med3_f32 v19, v30, s75, v210
	v_med3_f32 v26, v31, s75, v210
	v_cvt_pk_fp8_f32 v25, v19, v26
	v_pk_fma_f32 v[28:29], v[66:67], s[22:23], v[2:3] op_sel_hi:[1,0,1]
	v_add_u32_e32 v20, 0x90, v18
	v_pk_mul_f32 v[28:29], v[28:29], s[24:25] op_sel_hi:[1,0]
	v_ashrrev_i32_e32 v21, 31, v20
	v_med3_f32 v19, v28, s75, v210
	v_med3_f32 v26, v29, s75, v210
	v_lshlrev_b64 v[20:21], 10, v[20:21]
	v_cvt_pk_fp8_f32 v24, v27, v64 op_sel:[0,0,1]
	v_cvt_pk_fp8_f32 v25, v19, v26 op_sel:[0,0,1]
	v_lshl_add_u64 v[20:21], s[12:13], 0, v[20:21]
	v_lshl_add_u64 v[20:21], v[20:21], 0, v[16:17]
	s_nop 1
	v_permlane16_swap_b32_e32 v22, v24
	v_permlane16_swap_b32_e32 v23, v25
	v_lshl_add_u64 v[248:249], v[20:21], 0, v[250:251]
	global_store_dwordx4 v[248:249], v[22:25], off
	s_nop 1
	v_pk_fma_f32 v[22:23], v[62:63], s[22:23], v[14:15] op_sel_hi:[1,0,1]
	v_pk_fma_f32 v[24:25], v[60:61], s[22:23], v[12:13] op_sel_hi:[1,0,1]
	v_pk_mul_f32 v[22:23], v[22:23], s[24:25] op_sel_hi:[1,0]
	v_pk_mul_f32 v[24:25], v[24:25], s[24:25] op_sel_hi:[1,0]
	v_pk_fma_f32 v[28:29], v[56:57], s[22:23], v[8:9] op_sel_hi:[1,0,1]
	v_med3_f32 v19, v24, s75, v210
	v_pk_mul_f32 v[28:29], v[28:29], s[24:25] op_sel_hi:[1,0]
	v_med3_f32 v24, v25, s75, v210
	v_med3_f32 v25, v22, s75, v210
	v_med3_f32 v30, v23, s75, v210
	v_cvt_pk_fp8_f32 v22, v19, v24
	v_med3_f32 v19, v28, s75, v210
	v_med3_f32 v24, v29, s75, v210
	v_cvt_pk_fp8_f32 v23, v19, v24
	v_pk_fma_f32 v[26:27], v[58:59], s[22:23], v[10:11] op_sel_hi:[1,0,1]
	v_cvt_pk_fp8_f32 v22, v25, v30 op_sel:[0,0,1]
	v_pk_mul_f32 v[26:27], v[26:27], s[24:25] op_sel_hi:[1,0]
	v_pk_fma_f32 v[30:31], v[48:49], s[22:23], v[0:1] op_sel_hi:[1,0,1]
	v_med3_f32 v19, v26, s75, v210
	v_med3_f32 v24, v27, s75, v210
	v_cvt_pk_fp8_f32 v23, v19, v24 op_sel:[0,0,1]
	v_pk_fma_f32 v[24:25], v[54:55], s[22:23], v[6:7] op_sel_hi:[1,0,1]
	v_pk_fma_f32 v[26:27], v[52:53], s[22:23], v[4:5] op_sel_hi:[1,0,1]
	v_pk_mul_f32 v[24:25], v[24:25], s[24:25] op_sel_hi:[1,0]
	v_pk_mul_f32 v[26:27], v[26:27], s[24:25] op_sel_hi:[1,0]
	v_pk_mul_f32 v[30:31], v[30:31], s[24:25] op_sel_hi:[1,0]
	v_med3_f32 v19, v26, s75, v210
	v_med3_f32 v26, v27, s75, v210
	v_med3_f32 v27, v24, s75, v210
	v_med3_f32 v48, v25, s75, v210
	v_cvt_pk_fp8_f32 v24, v19, v26
	v_med3_f32 v19, v30, s75, v210
	v_med3_f32 v26, v31, s75, v210
	v_cvt_pk_fp8_f32 v25, v19, v26
	v_pk_fma_f32 v[28:29], v[50:51], s[22:23], v[2:3] op_sel_hi:[1,0,1]
	v_add_u32_e32 v20, 0xa0, v18
	v_pk_mul_f32 v[28:29], v[28:29], s[24:25] op_sel_hi:[1,0]
	v_ashrrev_i32_e32 v21, 31, v20
	v_med3_f32 v19, v28, s75, v210
	v_med3_f32 v26, v29, s75, v210
	v_lshlrev_b64 v[20:21], 10, v[20:21]
	v_cvt_pk_fp8_f32 v24, v27, v48 op_sel:[0,0,1]
	v_cvt_pk_fp8_f32 v25, v19, v26 op_sel:[0,0,1]
	v_lshl_add_u64 v[20:21], s[12:13], 0, v[20:21]
	v_pk_fma_f32 v[12:13], v[44:45], s[22:23], v[12:13] op_sel_hi:[1,0,1]
	v_lshl_add_u64 v[20:21], v[20:21], 0, v[16:17]
	v_pk_mul_f32 v[12:13], v[12:13], s[24:25] op_sel_hi:[1,0]
	v_pk_fma_f32 v[8:9], v[40:41], s[22:23], v[8:9] op_sel_hi:[1,0,1]
	s_nop 1
	v_permlane16_swap_b32_e32 v22, v24
	v_permlane16_swap_b32_e32 v23, v25
	v_lshl_add_u64 v[248:249], v[20:21], 0, v[250:251]
	global_store_dwordx4 v[248:249], v[22:25], off
	s_nop 1
	v_pk_mul_f32 v[8:9], v[8:9], s[24:25] op_sel_hi:[1,0]
	v_med3_f32 v20, v12, s75, v210
	v_med3_f32 v13, v13, s75, v210
	v_cvt_pk_fp8_f32 v12, v20, v13
	v_med3_f32 v8, v8, s75, v210
	v_med3_f32 v9, v9, s75, v210
	v_cvt_pk_fp8_f32 v13, v8, v9
	v_pk_fma_f32 v[10:11], v[42:43], s[22:23], v[10:11] op_sel_hi:[1,0,1]
	v_pk_fma_f32 v[4:5], v[36:37], s[22:23], v[4:5] op_sel_hi:[1,0,1]
	v_pk_mul_f32 v[10:11], v[10:11], s[24:25] op_sel_hi:[1,0]
	v_pk_mul_f32 v[4:5], v[4:5], s[24:25] op_sel_hi:[1,0]
	v_med3_f32 v8, v10, s75, v210
	v_med3_f32 v9, v11, s75, v210
	v_pk_fma_f32 v[0:1], v[32:33], s[22:23], v[0:1] op_sel_hi:[1,0,1]
	v_cvt_pk_fp8_f32 v13, v8, v9 op_sel:[0,0,1]
	v_pk_mul_f32 v[0:1], v[0:1], s[24:25] op_sel_hi:[1,0]
	v_med3_f32 v8, v4, s75, v210
	v_med3_f32 v5, v5, s75, v210
	v_cvt_pk_fp8_f32 v4, v8, v5
	v_med3_f32 v0, v0, s75, v210
	v_med3_f32 v1, v1, s75, v210
	v_pk_fma_f32 v[14:15], v[46:47], s[22:23], v[14:15] op_sel_hi:[1,0,1]
	v_cvt_pk_fp8_f32 v5, v0, v1
	v_pk_mul_f32 v[14:15], v[14:15], s[24:25] op_sel_hi:[1,0]
	v_pk_fma_f32 v[6:7], v[38:39], s[22:23], v[6:7] op_sel_hi:[1,0,1]
	v_pk_fma_f32 v[2:3], v[34:35], s[22:23], v[2:3] op_sel_hi:[1,0,1]
	v_add_u32_e32 v18, 0xb0, v18
	v_med3_f32 v14, v14, s75, v210
	v_med3_f32 v15, v15, s75, v210
	v_pk_mul_f32 v[6:7], v[6:7], s[24:25] op_sel_hi:[1,0]
	v_pk_mul_f32 v[2:3], v[2:3], s[24:25] op_sel_hi:[1,0]
	v_ashrrev_i32_e32 v19, 31, v18
	v_cvt_pk_fp8_f32 v12, v14, v15 op_sel:[0,0,1]
	v_med3_f32 v6, v6, s75, v210
	v_med3_f32 v7, v7, s75, v210
	v_med3_f32 v0, v2, s75, v210
	v_med3_f32 v1, v3, s75, v210
	v_lshlrev_b64 v[18:19], 10, v[18:19]
	v_cvt_pk_fp8_f32 v4, v6, v7 op_sel:[0,0,1]
	v_cvt_pk_fp8_f32 v5, v0, v1 op_sel:[0,0,1]
	v_lshl_add_u64 v[0:1], s[12:13], 0, v[18:19]
	v_lshl_add_u64 v[0:1], v[0:1], 0, v[16:17]
	s_mov_b64 s[2:3], -1
	global_store_dwordx2 v[0:1], v[12:13], off
	global_store_dwordx2 v[0:1], v[4:5], off offset:128
	s_cbranch_vccnz .LBB0_1783
	s_andn2_b64 vcc, exec, s[10:11]
	s_cbranch_vccnz .LBB0_1782
	s_barrier
	s_branch .LBB0_1782
